# conversion split rebalanced: router phase converts experts 0-8, in-projection tail 9-10, Hyena hook 11-31 (router waves are the critical path of the router phase)
# speedup vs baseline: 1.0148x; 1.0148x over previous
.LBB0_479:
	s_cmpk_lg_u32 s3, 0x100
	s_cbranch_scc1 .Lp2t_skip
	s_cmpk_lt_u32 s2, 0x88
	s_cbranch_scc1 .Lp2t_skip
	s_mov_b64 s[28:29], s[4:5]
	s_lshr_b32 s33, s92, 6
	v_mbcnt_lo_u32_b32 v65, -1, 0
	v_mbcnt_hi_u32_b32 v65, -1, v65
	s_mov_b64 s[16:17], s[86:87]
	s_mov_b64 s[18:19], s[80:81]
	s_mov_b32 s8, s33
	s_sub_i32 s0, s2, 0x88
	s_lshl_b32 s0, s0, 3
	s_add_i32 s20, s8, s0
	s_cmpk_gt_i32 s20, 0x17ff
	s_cbranch_scc1 .Lp2t_end
	s_add_i32 s0, s20, 0x11400
	s_add_i32 s14, s20, 0x4800
	s_cmpk_lt_i32 s20, 0x1000
	s_cselect_b32 s9, s14, s0
	s_cmp_gt_i32 s9, 0xffff
	s_cbranch_scc0 .Lp2t_1227
	s_load_dwordx2 s[0:1], s[16:17], 0x110
	s_add_i32 s4, s9, 0xffff0000
	s_mov_b32 s7, 0
	s_lshr_b32 s6, s4, 10
	s_lshl_b64 s[4:5], s[6:7], 24
	s_waitcnt lgkmcnt(0)
	s_add_u32 s0, s0, s4
	s_addc_u32 s1, s1, s5
	s_lshl_b32 s4, s9, 1
	s_and_b32 s10, s4, 0x780
	s_lshl_b32 s4, s10, 13
	s_add_u32 s0, s0, s4
	s_addc_u32 s1, s1, 0
	s_lshl_b32 s4, s9, 5
	s_and_b32 s11, s4, 0x7e0
	s_lshl_b32 s4, s11, 2
	s_add_u32 s4, s0, s4
	s_addc_u32 s5, s1, 0
	s_lshl_b64 s[0:1], s[6:7], 22
	s_lshl_b32 s6, s11, 11
	s_add_u32 s0, s18, s0
	s_addc_u32 s1, s19, s1
	s_add_u32 s0, s0, s6
	s_addc_u32 s1, s1, 0
	s_add_u32 s0, s0, s10
	s_addc_u32 s1, s1, 0
	s_add_u32 s0, s0, 0x24e00000
	s_addc_u32 s1, s1, 0
	s_mov_b32 s21, 0x42800000
	s_cbranch_execz .Lp2t_1228
	s_branch .Lp2t_1229

.Lp2t_1233:
	s_add_i32 s20, s20, s22
	s_cmpk_lt_i32 s20, 0x1800
	s_cselect_b64 s[8:9], -1, 0
	s_cmpk_gt_i32 s20, 0x17ff
	s_cbranch_scc1 .Lp2t_1239
	s_add_i32 s0, s20, 0x11400
	s_add_i32 s14, s20, 0x4800
	s_cmpk_lt_i32 s20, 0x1000
	s_cselect_b32 s27, s14, s0
	s_cmp_gt_i32 s27, 0xffff
	s_mov_b64 s[12:13], -1
	s_cbranch_scc0 .Lp2t_1236
	s_load_dwordx2 s[0:1], s[16:17], 0x110
	s_add_i32 s4, s27, 0xffff0000
	s_lshr_b32 s4, s4, 10
	s_lshl_b64 s[10:11], s[4:5], 24
	s_waitcnt lgkmcnt(0)
	s_add_u32 s0, s0, s10
	s_addc_u32 s1, s1, s11
	s_lshl_b32 s10, s27, 1
	s_and_b32 s12, s10, 0x780
	s_lshl_b32 s10, s12, 13
	s_add_u32 s0, s0, s10
	s_addc_u32 s1, s1, 0
	s_lshl_b32 s10, s27, 5
	s_and_b32 s13, s10, 0x7e0
	s_lshl_b32 s10, s13, 2
	s_add_u32 s10, s0, s10
	s_addc_u32 s11, s1, 0
	s_lshl_b64 s[0:1], s[4:5], 22
	s_lshl_b32 s4, s13, 11
	s_add_u32 s0, s23, s0
	s_addc_u32 s1, s24, s1
	s_add_u32 s0, s0, s4
	s_addc_u32 s1, s1, 0
	s_add_u32 s0, s0, s12
	s_addc_u32 s1, s1, 0
	s_mov_b64 s[12:13], 0

.Lp2t_1239:
	s_waitcnt vmcnt(15)
	v_mul_f32_e32 v130, s26, v0
	s_waitcnt vmcnt(14)
	v_mul_f32_e32 v175, s26, v4
	v_mov_b32_e32 v176, v131
	v_cvt_pk_fp8_f32 v176, v130, v175
	s_waitcnt vmcnt(11)
	v_mul_f32_e32 v130, s26, v16
	s_waitcnt vmcnt(10)
	v_mul_f32_e32 v175, s26, v20
	v_mov_b32_e32 v177, v131
	v_cvt_pk_fp8_f32 v177, v130, v175
	v_mul_f32_e32 v178, s26, v8
	v_mul_f32_e32 v179, s26, v12
	s_waitcnt vmcnt(9)
	v_mul_f32_e32 v130, s26, v24
	s_waitcnt vmcnt(8)
	v_mul_f32_e32 v175, s26, v28
	v_cvt_pk_fp8_f32 v176, v178, v179 op_sel:[0,0,1]
	v_cvt_pk_fp8_f32 v177, v130, v175 op_sel:[0,0,1]
	s_waitcnt vmcnt(7)
	v_mul_f32_e32 v130, s26, v32
	s_waitcnt vmcnt(6)
	v_mul_f32_e32 v175, s26, v36
	v_mov_b32_e32 v178, v131
	v_cvt_pk_fp8_f32 v178, v130, v175
	s_waitcnt vmcnt(3)
	v_mul_f32_e32 v130, s26, v48
	s_waitcnt vmcnt(2)
	v_mul_f32_e32 v175, s26, v52
	v_mov_b32_e32 v179, v131
	v_cvt_pk_fp8_f32 v179, v130, v175
	v_mul_f32_e32 v180, s26, v40
	v_mul_f32_e32 v181, s26, v44
	s_waitcnt vmcnt(1)
	v_mul_f32_e32 v130, s26, v56
	s_waitcnt vmcnt(0)
	v_mul_f32_e32 v175, s26, v60
	v_cvt_pk_fp8_f32 v178, v180, v181 op_sel:[0,0,1]
	v_cvt_pk_fp8_f32 v179, v130, v175 op_sel:[0,0,1]
	v_mul_f32_e32 v130, s26, v1
	v_mul_f32_e32 v175, s26, v5
	v_mov_b32_e32 v180, v131
	v_cvt_pk_fp8_f32 v180, v130, v175
	v_mul_f32_e32 v130, s26, v17
	v_mul_f32_e32 v175, s26, v21
	v_mov_b32_e32 v181, v131
	v_cvt_pk_fp8_f32 v181, v130, v175
	v_mul_f32_e32 v182, s26, v9
	v_mul_f32_e32 v183, s26, v13
	v_mul_f32_e32 v130, s26, v25
	v_mul_f32_e32 v175, s26, v29
	v_cvt_pk_fp8_f32 v180, v182, v183 op_sel:[0,0,1]
	v_cvt_pk_fp8_f32 v181, v130, v175 op_sel:[0,0,1]
	v_mul_f32_e32 v130, s26, v33
	v_mul_f32_e32 v175, s26, v37
	v_mov_b32_e32 v182, v131
	v_cvt_pk_fp8_f32 v182, v130, v175
	v_mul_f32_e32 v130, s26, v49
	v_mul_f32_e32 v175, s26, v53
	v_mov_b32_e32 v183, v131
	v_cvt_pk_fp8_f32 v183, v130, v175
	v_mul_f32_e32 v184, s26, v41
	v_mul_f32_e32 v185, s26, v45
	v_mul_f32_e32 v130, s26, v57
	v_mul_f32_e32 v175, s26, v61
	v_cvt_pk_fp8_f32 v182, v184, v185 op_sel:[0,0,1]
	v_cvt_pk_fp8_f32 v183, v130, v175 op_sel:[0,0,1]
	v_mul_f32_e32 v130, s26, v2
	v_mul_f32_e32 v175, s26, v6
	v_mov_b32_e32 v184, v131
	v_cvt_pk_fp8_f32 v184, v130, v175
	v_mul_f32_e32 v130, s26, v18
	v_mul_f32_e32 v175, s26, v22
	v_mov_b32_e32 v185, v131
	v_cvt_pk_fp8_f32 v185, v130, v175
	v_mul_f32_e32 v186, s26, v10
	v_mul_f32_e32 v187, s26, v14
	v_mul_f32_e32 v130, s26, v26
	v_mul_f32_e32 v175, s26, v30
	v_cvt_pk_fp8_f32 v184, v186, v187 op_sel:[0,0,1]
	v_cvt_pk_fp8_f32 v185, v130, v175 op_sel:[0,0,1]
	v_mul_f32_e32 v130, s26, v34
	v_mul_f32_e32 v175, s26, v38
	v_mov_b32_e32 v186, v131
	v_cvt_pk_fp8_f32 v186, v130, v175
	v_mul_f32_e32 v130, s26, v50
	v_mul_f32_e32 v175, s26, v54
	v_mov_b32_e32 v187, v131
	v_cvt_pk_fp8_f32 v187, v130, v175
	v_mul_f32_e32 v188, s26, v42
	v_mul_f32_e32 v189, s26, v46
	v_mul_f32_e32 v130, s26, v58
	v_mul_f32_e32 v175, s26, v62
	v_cvt_pk_fp8_f32 v186, v188, v189 op_sel:[0,0,1]
	v_cvt_pk_fp8_f32 v187, v130, v175 op_sel:[0,0,1]
	v_mul_f32_e32 v130, s26, v3
	v_mul_f32_e32 v175, s26, v7
	v_mov_b32_e32 v188, v131
	v_cvt_pk_fp8_f32 v188, v130, v175
	v_mul_f32_e32 v130, s26, v19
	v_mul_f32_e32 v175, s26, v23
	v_mov_b32_e32 v189, v131
	v_cvt_pk_fp8_f32 v189, v130, v175
	v_mul_f32_e32 v190, s26, v11
	v_mul_f32_e32 v191, s26, v15
	v_mul_f32_e32 v130, s26, v27
	v_mul_f32_e32 v175, s26, v31
	v_cvt_pk_fp8_f32 v188, v190, v191 op_sel:[0,0,1]
	v_cvt_pk_fp8_f32 v189, v130, v175 op_sel:[0,0,1]
	v_mul_f32_e32 v130, s26, v35
	v_mul_f32_e32 v175, s26, v39
	v_mov_b32_e32 v190, v131
	v_cvt_pk_fp8_f32 v190, v130, v175
	v_mul_f32_e32 v130, s26, v51
	v_mul_f32_e32 v175, s26, v55
	v_mov_b32_e32 v191, v131
	v_cvt_pk_fp8_f32 v191, v130, v175
	v_mul_f32_e32 v192, s26, v43
	v_mul_f32_e32 v193, s26, v47
	v_mul_f32_e32 v130, s26, v59
	v_mul_f32_e32 v175, s26, v63
	v_cvt_pk_fp8_f32 v190, v192, v193 op_sel:[0,0,1]
	v_cvt_pk_fp8_f32 v191, v130, v175 op_sel:[0,0,1]
	ds_write_b128 v129, v[176:179]
	ds_write_b128 v129, v[180:183] offset:144
	ds_write_b128 v129, v[184:187] offset:288
	ds_write_b128 v129, v[188:191] offset:432
	s_waitcnt lgkmcnt(0)
	ds_read_b128 v[176:179], v174
	ds_read_b128 v[180:183], v174 offset:1152
	v_lshl_add_u64 v[188:189], s[6:7], 0, v[164:165]
	v_lshl_add_u64 v[184:185], v[188:189], 0, v[166:167]
	v_lshl_add_u64 v[190:191], v[188:189], 0, v[168:169]
	s_waitcnt lgkmcnt(1)
	global_store_dwordx4 v[184:185], v[176:179], off nt
	ds_read_b128 v[176:179], v174 offset:2304
	ds_read_b128 v[184:187], v174 offset:3456
	s_waitcnt lgkmcnt(2)
	global_store_dwordx4 v[190:191], v[180:183], off nt
	s_andn2_b64 vcc, exec, s[8:9]
	s_mov_b64 s[8:9], -1
	v_lshl_add_u64 v[180:181], v[188:189], 0, v[170:171]
	s_waitcnt lgkmcnt(1)
	global_store_dwordx4 v[180:181], v[176:179], off nt
	s_nop 1
	v_lshl_add_u64 v[176:177], v[188:189], 0, v[172:173]
	s_waitcnt lgkmcnt(0)
	global_store_dwordx4 v[176:177], v[184:187], off nt
	s_waitcnt lgkmcnt(0)
	s_cbranch_vccnz .Lp2t_1232
	s_add_i32 s27, s20, s22
	s_cmpk_gt_i32 s27, 0x17ff
	s_cselect_b64 s[8:9], -1, 0
	s_and_b64 vcc, exec, s[8:9]
	s_cbranch_vccnz .Lp2t_1231
	s_add_i32 s4, s27, 0x11400
	s_add_i32 s14, s27, 0x4800
	s_cmpk_lt_i32 s27, 0x1000
	s_cselect_b32 s20, s14, s4
	s_cmp_gt_i32 s20, 0xffff
	s_mov_b64 s[12:13], -1
	s_cbranch_scc0 .Lp2t_1243
	s_load_dwordx2 s[6:7], s[16:17], 0x110
	s_add_i32 s4, s20, 0xffff0000
	s_lshr_b32 s4, s4, 10
	s_lshl_b64 s[10:11], s[4:5], 24
	s_waitcnt lgkmcnt(0)
	s_add_u32 s6, s6, s10
	s_addc_u32 s7, s7, s11
	s_lshl_b32 s10, s20, 1
	s_and_b32 s12, s10, 0x780
	s_lshl_b32 s10, s12, 13
	s_add_u32 s6, s6, s10
	s_addc_u32 s7, s7, 0
	s_lshl_b32 s10, s20, 5
	s_and_b32 s13, s10, 0x7e0
	s_lshl_b32 s10, s13, 2
	s_add_u32 s10, s6, s10
	s_addc_u32 s11, s7, 0
	s_lshl_b64 s[6:7], s[4:5], 22
	s_lshl_b32 s4, s13, 11
	s_add_u32 s6, s23, s6
	s_addc_u32 s7, s24, s7
	s_add_u32 s4, s6, s4
	s_addc_u32 s7, s7, 0
	s_add_u32 s6, s4, s12
	s_addc_u32 s7, s7, 0
	s_mov_b64 s[12:13], 0

.LBB0_742:
	s_abs_i32 s7, s3
	v_cvt_f32_u32_e32 v0, s7
	v_readlane_b32 s86, v255, 12
	v_readlane_b32 s87, v255, 13
	s_sub_i32 s8, 0, s7
	v_rcp_iflag_f32_e32 v0, v0
	s_mov_b64 s[0:1], s[86:87]
	s_mov_b32 s6, 0
	s_sub_i32 s4, 0x3eff, s2
	v_mul_f32_e32 v0, 0x4f7ffffe, v0
	v_cvt_u32_f32_e32 v0, v0
	v_readlane_b32 s92, v255, 2
	v_readfirstlane_b32 s9, v0
	s_mul_i32 s8, s8, s9
	s_mul_hi_u32 s8, s9, s8
	v_mbcnt_lo_u32_b32 v1, -1, s6
	s_xor_b32 s6, s4, s3
	s_abs_i32 s4, s4
	s_add_i32 s9, s9, s8
	s_mul_hi_u32 s8, s4, s9
	s_mul_i32 s9, s8, s7
	s_sub_i32 s4, s4, s9
	s_ashr_i32 s6, s6, 31
	s_add_i32 s9, s8, 1
	s_sub_i32 s10, s4, s7
	s_cmp_ge_u32 s4, s7
	s_cselect_b32 s8, s9, s8
	s_cselect_b32 s4, s10, s4
	s_add_i32 s9, s8, 1
	s_cmp_ge_u32 s4, s7
	s_cselect_b32 s4, s9, s8
	s_xor_b32 s4, s4, s6
	s_sub_i32 s59, s4, s6
	s_min_i32 s4, s59, 0
	s_mul_i32 s4, s4, s3
	s_add_i32 s4, s4, s2
	s_mul_hi_i32 s6, s4, 0x2aaaaaab
	s_lshr_b32 s7, s6, 31
	s_ashr_i32 s6, s6, 7
	s_add_i32 s7, s6, s7
	s_add_i32 s6, s7, 11
	s_mulk_i32 s7, 0x300
	v_mbcnt_hi_u32_b32 v1, -1, v1
	s_sub_i32 s12, s4, s7
	s_mov_b32 s5, 0
	v_or_b32_e32 v192, s92, v1
	s_mov_b64 s[14:15], s[86:87]
	s_cmpk_gt_i32 s12, 0x1ff
	s_cbranch_scc0 .LBB0_744
	s_load_dwordx2 s[8:9], s[14:15], 0x110
	s_ashr_i32 s7, s6, 31
	s_lshl_b64 s[10:11], s[6:7], 24
	s_waitcnt lgkmcnt(0)
	s_add_u32 s8, s8, s10
	s_addc_u32 s9, s9, s11
	s_lshl_b32 s4, s12, 3
	s_and_b32 s4, s4, 0x7fffffc0
	s_addk_i32 s4, 0xf000
	s_mov_b32 s7, 8
	s_cbranch_execz .LBB0_745
	s_branch .LBB0_746

.LBB0_746:
	s_lshl_b64 s[4:5], s[4:5], 13
	s_add_u32 s4, s8, s4
	s_addc_u32 s5, s9, s5
	s_lshl_b32 s6, s12, s7
	s_and_b32 s6, s6, 0x700
	s_lshl_b32 s6, s6, 2
	s_add_u32 s4, s4, s6
	s_addc_u32 s5, s5, 0
	s_cmp_lt_i32 s59, 0
	v_lshlrev_b32_e32 v0, 2, v192
	v_and_b32_e32 v180, 0xfc, v0
	s_cselect_b64 s[6:7], -1, 0
	v_cndmask_b32_e64 v0, v180, 0, s[6:7]
	s_and_b64 s[6:7], s[6:7], exec
	v_ashrrev_i32_e32 v6, 3, v192
	s_cselect_b32 s6, 0, 0x800
	v_and_b32_e32 v181, -8, v6
	v_lshlrev_b32_e32 v0, 2, v0
	v_mov_b32_e32 v1, 0
	v_lshl_add_u64 v[0:1], s[4:5], 0, v[0:1]
	v_mad_i64_i32 v[2:3], s[4:5], s6, v181, 0
	v_or_b32_e32 v182, 1, v181
	v_lshl_add_u64 v[2:3], v[2:3], 2, v[0:1]
	v_mad_i64_i32 v[4:5], s[4:5], s6, v182, 0
	v_or_b32_e32 v183, 2, v181
	v_lshl_add_u64 v[4:5], v[4:5], 2, v[0:1]
	global_load_dwordx4 v[48:51], v[2:3], off nt
	global_load_dwordx4 v[52:55], v[4:5], off nt
	v_mad_i64_i32 v[2:3], s[4:5], s6, v183, 0
	v_or_b32_e32 v184, 3, v181
	v_lshl_add_u64 v[2:3], v[2:3], 2, v[0:1]
	v_mad_i64_i32 v[4:5], s[4:5], s6, v184, 0
	v_or_b32_e32 v185, 4, v181
	v_lshl_add_u64 v[4:5], v[4:5], 2, v[0:1]
	global_load_dwordx4 v[64:67], v[2:3], off nt
	global_load_dwordx4 v[68:71], v[4:5], off nt
	v_mad_i64_i32 v[2:3], s[4:5], s6, v185, 0
	s_waitcnt vmcnt(0)
	v_or_b32_e32 v186, 5, v181
	v_lshl_add_u64 v[2:3], v[2:3], 2, v[0:1]
	v_mad_i64_i32 v[4:5], s[4:5], s6, v186, 0
	v_or_b32_e32 v187, 6, v181
	v_lshl_add_u64 v[4:5], v[4:5], 2, v[0:1]
	global_load_dwordx4 v[40:43], v[2:3], off nt
	global_load_dwordx4 v[44:47], v[4:5], off nt
	v_mad_i64_i32 v[2:3], s[4:5], s6, v187, 0
	v_or_b32_e32 v188, 7, v6
	v_lshl_add_u64 v[2:3], v[2:3], 2, v[0:1]
	v_mad_i64_i32 v[4:5], s[4:5], s6, v188, 0
	v_lshl_add_u64 v[0:1], v[4:5], 2, v[0:1]
	global_load_dwordx4 v[56:59], v[2:3], off nt
	global_load_dwordx4 v[60:63], v[0:1], off nt
	s_min_i32 s4, s59, 1
	s_mul_i32 s4, s4, s3
	s_add_i32 s5, s4, s2
	s_mul_hi_i32 s4, s5, 0x2aaaaaab
	s_lshr_b32 s6, s4, 31
	s_ashr_i32 s4, s4, 7
	s_add_i32 s6, s4, s6
	s_add_i32 s4, s6, 11
	s_mulk_i32 s6, 0x300
	s_sub_i32 s12, s5, s6
	v_readlane_b32 s88, v255, 6
	v_readlane_b32 s90, v255, 3
	s_cmpk_gt_i32 s12, 0x1ff
	s_mov_b32 s7, 0
	v_readlane_b32 s89, v255, 7
	v_readlane_b32 s85, v255, 5
	v_readlane_b32 s91, v255, 4
	s_cbranch_scc0 .LBB0_748
	s_load_dwordx2 s[8:9], s[14:15], 0x110
	s_ashr_i32 s5, s4, 31
	s_lshl_b64 s[10:11], s[4:5], 24
	s_waitcnt lgkmcnt(0)
	s_add_u32 s8, s8, s10
	s_addc_u32 s9, s9, s11
	s_lshl_b32 s5, s12, 3
	s_and_b32 s5, s5, 0x7fffffc0
	s_add_i32 s6, s5, 0xfffff000
	s_load_dwordx2 s[16:17], s[0:1], 0x138
	s_mov_b32 s0, 8
	s_cbranch_execz .LBB0_749
	s_branch .LBB0_750

.LBB0_805:
	s_or_b64 exec, exec, s[0:1]
	v_lshlrev_b32_e32 v0, 2, v122
	v_and_b32_e32 v0, -8, v0
	v_lshlrev_b32_e32 v1, 3, v123
	v_add3_u32 v2, v219, v0, v1
	v_mov_b32_e32 v0, v104
	v_mov_b32_e32 v1, v96
	v_mov_b32_e32 v96, v105
	ds_write2_b64 v2, v[0:1], v[96:97] offset1:1
	v_mov_b32_e32 v0, v102
	v_mov_b32_e32 v1, v110
	v_mov_b32_e32 v110, v103
	ds_write2_b64 v2, v[0:1], v[110:111] offset0:2 offset1:3
	v_mov_b32_e32 v0, v106
	v_mov_b32_e32 v1, v112
	v_mov_b32_e32 v112, v107
	ds_write2_b64 v2, v[0:1], v[112:113] offset0:4 offset1:5
	v_mov_b32_e32 v0, v108
	v_mov_b32_e32 v1, v114
	v_mov_b32_e32 v114, v109
	ds_write2_b64 v2, v[0:1], v[114:115] offset0:6 offset1:7
	s_waitcnt lgkmcnt(0)
	s_barrier
	ds_read_b64 v[112:113], v222
	ds_read_b64 v[110:111], v223 offset:2048
	ds_read_b64 v[108:109], v224 offset:4096
	ds_read_b64 v[106:107], v225 offset:6144
	ds_read_b64 v[104:105], v226 offset:8192
	ds_read_b64 v[102:103], v227 offset:10240
	ds_read_b64 v[100:101], v228 offset:12288
	ds_read_b64 v[98:99], v229 offset:14336
	s_waitcnt lgkmcnt(6)
	v_pk_add_f32 v[96:97], v[110:111], 0 op_sel_hi:[1,0]
	s_waitcnt lgkmcnt(5)
	v_pk_add_f32 v[120:121], v[108:109], 0 op_sel_hi:[1,0]
	s_waitcnt lgkmcnt(2)
	v_pk_add_f32 v[114:115], v[102:103], 0 op_sel_hi:[1,0]
	s_waitcnt lgkmcnt(1)
	v_pk_add_f32 v[122:123], v[100:101], 0 op_sel_hi:[1,0]
	v_pk_add_f32 v[116:117], v[96:97], v[114:115]
	v_pk_add_f32 v[96:97], v[96:97], v[114:115] neg_lo:[0,1] neg_hi:[0,1]
	v_pk_fma_f32 v[114:115], v[102:103], s[28:29], v[110:111] op_sel:[1,0,0] op_sel_hi:[0,1,1]
	s_mov_b32 s8, s34
	s_mov_b32 s9, s30
	v_pk_add_f32 v[124:125], v[120:121], v[122:123]
	v_pk_add_f32 v[120:121], v[120:121], v[122:123] neg_lo:[0,1] neg_hi:[0,1]
	v_pk_fma_f32 v[122:123], v[100:101], s[28:29], v[108:109] op_sel:[1,0,0] op_sel_hi:[0,1,1]
	v_pk_add_f32 v[128:129], v[106:107], 0 op_sel_hi:[1,0]
	s_waitcnt lgkmcnt(0)
	v_pk_add_f32 v[130:131], v[98:99], 0 op_sel_hi:[1,0]
	v_pk_mul_f32 v[136:137], v[114:115], s[8:9] op_sel_hi:[0,1]
	s_mov_b32 s0, s35
	s_mov_b32 s1, s34
	s_mov_b32 s6, s37
	s_mov_b32 s7, s36
	v_pk_add_f32 v[132:133], v[128:129], v[130:131]
	v_pk_add_f32 v[128:129], v[128:129], v[130:131] neg_lo:[0,1] neg_hi:[0,1]
	v_pk_fma_f32 v[130:131], v[98:99], s[28:29], v[106:107] op_sel:[1,0,0] op_sel_hi:[0,1,1]
	v_pk_fma_f32 v[114:115], v[114:115], s[0:1], v[136:137] op_sel:[1,0,0]
	v_pk_mul_f32 v[136:137], v[122:123], s[6:7] op_sel_hi:[0,1]
	s_mov_b32 s12, s37
	s_mov_b32 s4, s35
	s_mov_b32 s5, s38
	v_pk_fma_f32 v[122:123], v[122:123], s[12:13], v[136:137] op_sel:[1,0,0] op_sel_hi:[1,0,1]
	v_pk_mul_f32 v[136:137], v[130:131], s[4:5] op_sel_hi:[0,1]
	v_pk_fma_f32 v[130:131], v[130:131], s[34:35], v[136:137] op_sel:[1,0,0]
	v_pk_mul_f32 v[136:137], v[96:97], s[6:7] op_sel_hi:[0,1]
	s_mov_b32 s19, s26
	v_pk_fma_f32 v[118:119], v[102:103], s[26:27], v[110:111] op_sel:[1,0,0] op_sel_hi:[0,1,1]
	v_pk_fma_f32 v[96:97], v[96:97], s[12:13], v[136:137] op_sel:[1,0,0] op_sel_hi:[1,0,1]
	v_pk_mul_f32 v[136:137], v[120:121], s[18:19] op_sel_hi:[0,1]
	s_mov_b32 s50, s27
	s_mov_b32 s51, s18
	v_pk_add_f32 v[4:5], v[112:113], 0 op_sel_hi:[1,0]
	v_pk_add_f32 v[6:7], v[104:105], 0 op_sel_hi:[1,0]
	v_pk_fma_f32 v[134:135], v[98:99], s[26:27], v[106:107] op_sel:[1,0,0] op_sel_hi:[0,1,1]
	v_pk_fma_f32 v[120:121], v[120:121], s[50:51], v[136:137] op_sel:[1,0,0]
	v_pk_mul_f32 v[136:137], v[118:119], s[4:5] op_sel_hi:[0,1]
	s_mov_b32 s39, s35
	v_pk_add_f32 v[80:81], v[4:5], v[6:7]
	v_pk_fma_f32 v[118:119], v[118:119], s[34:35], v[136:137] op_sel:[1,0,0]
	v_pk_mul_f32 v[136:137], v[134:135], s[38:39] op_sel_hi:[0,1]
	s_mov_b32 s31, s38
	v_pk_add_f32 v[4:5], v[4:5], v[6:7] neg_lo:[0,1] neg_hi:[0,1]
	v_pk_fma_f32 v[6:7], v[104:105], s[28:29], v[112:113] op_sel:[1,0,0] op_sel_hi:[0,1,1]
	v_pk_fma_f32 v[126:127], v[100:101], s[26:27], v[108:109] op_sel:[1,0,0] op_sel_hi:[0,1,1]
	v_mul_f32_e32 v86, 0xbf3504f3, v128
	v_pk_fma_f32 v[134:135], v[134:135], s[30:31], v[136:137] op_sel:[1,0,0]
	v_pk_add_f32 v[136:137], v[80:81], v[124:125]
	v_pk_add_f32 v[80:81], v[80:81], v[124:125] neg_lo:[0,1] neg_hi:[0,1]
	v_pk_add_f32 v[124:125], v[116:117], v[132:133]
	v_pk_add_f32 v[116:117], v[116:117], v[132:133] neg_lo:[0,1] neg_hi:[0,1]
	v_pk_fma_f32 v[128:129], v[128:129], s[6:7], v[86:87] op_sel:[1,0,0] op_sel_hi:[1,1,0]
	v_mul_f32_e32 v86, 0xbf3504f3, v126
	v_pk_add_f32 v[132:133], v[136:137], v[124:125]
	v_pk_add_f32 v[124:125], v[136:137], v[124:125] neg_lo:[0,1] neg_hi:[0,1]
	v_pk_fma_f32 v[136:137], v[116:117], s[28:29], v[80:81] op_sel:[1,0,0] op_sel_hi:[0,1,1]
	v_pk_fma_f32 v[80:81], v[116:117], s[26:27], v[80:81] op_sel:[1,0,0] op_sel_hi:[0,1,1]
	v_pk_add_f32 v[116:117], v[6:7], v[122:123]
	v_pk_add_f32 v[6:7], v[6:7], v[122:123] neg_lo:[0,1] neg_hi:[0,1]
	v_pk_add_f32 v[122:123], v[114:115], v[130:131]
	v_pk_add_f32 v[114:115], v[114:115], v[130:131] neg_lo:[0,1] neg_hi:[0,1]
	v_pk_fma_f32 v[82:83], v[104:105], s[26:27], v[112:113] op_sel:[1,0,0] op_sel_hi:[0,1,1]
	v_pk_fma_f32 v[126:127], v[126:127], s[6:7], v[86:87] op_sel:[1,0,0] op_sel_hi:[1,1,0]
	v_pk_add_f32 v[130:131], v[116:117], v[122:123]
	v_pk_add_f32 v[116:117], v[116:117], v[122:123] neg_lo:[0,1] neg_hi:[0,1]
	v_pk_fma_f32 v[122:123], v[114:115], s[28:29], v[6:7] op_sel:[1,0,0] op_sel_hi:[0,1,1]
	v_pk_fma_f32 v[6:7], v[114:115], s[26:27], v[6:7] op_sel:[1,0,0] op_sel_hi:[0,1,1]
	v_pk_add_f32 v[114:115], v[4:5], v[120:121]
	v_pk_add_f32 v[4:5], v[4:5], v[120:121] neg_lo:[0,1] neg_hi:[0,1]
	v_pk_add_f32 v[120:121], v[96:97], v[128:129]
	v_pk_add_f32 v[96:97], v[96:97], v[128:129] neg_lo:[0,1] neg_hi:[0,1]
	v_mov_b32_e32 v160, v215
	v_mov_b32_e32 v3, v220
	v_mov_b32_e32 v1, v221
	v_mov_b32_e32 v2, v217
	v_mov_b32_e32 v0, v218
	v_pk_add_f32 v[128:129], v[114:115], v[120:121]
	v_pk_add_f32 v[114:115], v[114:115], v[120:121] neg_lo:[0,1] neg_hi:[0,1]
	v_pk_fma_f32 v[120:121], v[96:97], s[28:29], v[4:5] op_sel:[1,0,0] op_sel_hi:[0,1,1]
	v_pk_fma_f32 v[4:5], v[96:97], s[26:27], v[4:5] op_sel:[1,0,0] op_sel_hi:[0,1,1]
	v_pk_add_f32 v[96:97], v[82:83], v[126:127]
	v_pk_add_f32 v[82:83], v[82:83], v[126:127] neg_lo:[0,1] neg_hi:[0,1]
	v_pk_add_f32 v[126:127], v[118:119], v[134:135]
	v_pk_add_f32 v[118:119], v[118:119], v[134:135] neg_lo:[0,1] neg_hi:[0,1]
	v_pk_add_f32 v[134:135], v[96:97], v[126:127]
	v_pk_add_f32 v[96:97], v[96:97], v[126:127] neg_lo:[0,1] neg_hi:[0,1]
	v_pk_fma_f32 v[126:127], v[118:119], s[28:29], v[82:83] op_sel:[1,0,0] op_sel_hi:[0,1,1]
	v_pk_fma_f32 v[82:83], v[118:119], s[26:27], v[82:83] op_sel:[1,0,0] op_sel_hi:[0,1,1]
	v_pk_mul_f32 v[118:119], v[2:3], s[28:29]
	v_mov_b32_e32 v86, v3
	v_pk_mul_f32 v[138:139], v[2:3], v[2:3] op_sel_hi:[1,0]
	v_pk_mul_f32 v[158:159], v[2:3], v[130:131] op_sel_hi:[1,0]
	v_pk_fma_f32 v[138:139], v[86:87], v[118:119], v[138:139] op_sel:[0,1,0] op_sel_hi:[0,0,1]
	v_pk_mul_f32 v[142:143], v[138:139], s[28:29]
	v_pk_mul_f32 v[144:145], v[138:139], v[138:139] op_sel_hi:[1,0]
	v_pk_mul_f32 v[140:141], v[2:3], v[138:139] op_sel_hi:[1,0]
	v_pk_fma_f32 v[144:145], v[138:139], v[142:143], v[144:145] op_sel:[1,1,0] op_sel_hi:[1,0,1]
	v_pk_fma_f32 v[140:141], v[138:139], v[118:119], v[140:141] op_sel:[1,1,0] op_sel_hi:[1,0,1]
	v_pk_mul_f32 v[146:147], v[2:3], v[144:145] op_sel_hi:[1,0]
	v_pk_mul_f32 v[150:151], v[140:141], s[28:29]
	v_pk_fma_f32 v[146:147], v[144:145], v[118:119], v[146:147] op_sel:[1,1,0] op_sel_hi:[1,0,1]
	v_pk_fma_f32 v[118:119], v[130:131], v[118:119], v[158:159] op_sel:[1,1,0] op_sel_hi:[1,0,1]
	v_pk_mul_f32 v[130:131], v[138:139], v[128:129] op_sel_hi:[1,0]
	v_pk_mul_f32 v[148:149], v[138:139], v[144:145] op_sel_hi:[1,0]
	v_pk_fma_f32 v[128:129], v[128:129], v[142:143], v[130:131] op_sel:[1,1,0] op_sel_hi:[1,0,1]
	v_pk_mul_f32 v[130:131], v[134:135], v[140:141] op_sel_hi:[0,1]
	v_pk_mul_f32 v[154:155], v[144:145], s[28:29]
	v_pk_fma_f32 v[130:131], v[134:135], v[150:151], v[130:131] op_sel:[1,1,0] op_sel_hi:[1,0,1]
	v_pk_mul_f32 v[134:135], v[136:137], v[144:145] op_sel_hi:[0,1]
	v_pk_fma_f32 v[148:149], v[144:145], v[142:143], v[148:149] op_sel:[1,1,0] op_sel_hi:[1,0,1]
	v_pk_mul_f32 v[152:153], v[140:141], v[144:145] op_sel_hi:[1,0]
	v_pk_fma_f32 v[134:135], v[136:137], v[154:155], v[134:135] op_sel:[1,1,0] op_sel_hi:[1,0,1]
	v_pk_mul_f32 v[136:137], v[146:147], s[28:29]
	v_pk_mul_f32 v[142:143], v[122:123], v[146:147] op_sel_hi:[0,1]
	v_pk_fma_f32 v[152:153], v[144:145], v[150:151], v[152:153] op_sel:[1,1,0] op_sel_hi:[1,0,1]
	v_pk_mul_f32 v[156:157], v[144:145], v[144:145] op_sel_hi:[1,0]
	v_pk_fma_f32 v[122:123], v[122:123], v[136:137], v[142:143] op_sel:[1,1,0] op_sel_hi:[1,0,1]
	v_pk_mul_f32 v[136:137], v[148:149], s[28:29]
	v_pk_mul_f32 v[142:143], v[120:121], v[148:149] op_sel_hi:[0,1]
	v_pk_fma_f32 v[156:157], v[144:145], v[154:155], v[156:157] op_sel:[1,1,0] op_sel_hi:[1,0,1]
	v_pk_fma_f32 v[120:121], v[120:121], v[136:137], v[142:143] op_sel:[1,1,0] op_sel_hi:[1,0,1]
	v_pk_mul_f32 v[136:137], v[152:153], s[28:29]
	v_pk_mul_f32 v[142:143], v[126:127], v[152:153] op_sel_hi:[0,1]
	v_pk_fma_f32 v[126:127], v[126:127], v[136:137], v[142:143] op_sel:[1,1,0] op_sel_hi:[1,0,1]
	v_pk_mul_f32 v[136:137], v[156:157], s[28:29]
	v_pk_mul_f32 v[2:3], v[2:3], v[156:157] op_sel_hi:[0,1]
	v_pk_mul_f32 v[142:143], v[124:125], v[156:157] op_sel_hi:[0,1]
	v_pk_fma_f32 v[2:3], v[86:87], v[136:137], v[2:3] op_sel:[0,1,0] op_sel_hi:[0,0,1]
	v_pk_fma_f32 v[124:125], v[124:125], v[136:137], v[142:143] op_sel:[1,1,0] op_sel_hi:[1,0,1]
	v_pk_mul_f32 v[142:143], v[2:3], s[28:29]
	v_pk_mul_f32 v[2:3], v[116:117], v[2:3] op_sel_hi:[0,1]
	v_pk_fma_f32 v[2:3], v[116:117], v[142:143], v[2:3] op_sel:[1,1,0] op_sel_hi:[1,0,1]
	v_pk_mul_f32 v[116:117], v[138:139], v[156:157] op_sel_hi:[0,1]
	v_pk_fma_f32 v[116:117], v[138:139], v[136:137], v[116:117] op_sel:[1,1,0] op_sel_hi:[1,0,1]
	v_ashrrev_i32_e32 v86, 4, v160
	v_pk_mul_f32 v[138:139], v[116:117], s[28:29]
	v_pk_mul_f32 v[116:117], v[114:115], v[116:117] op_sel_hi:[0,1]
	v_pk_fma_f32 v[114:115], v[114:115], v[138:139], v[116:117] op_sel:[1,1,0] op_sel_hi:[1,0,1]
	v_pk_mul_f32 v[116:117], v[140:141], v[156:157] op_sel_hi:[0,1]
	v_pk_fma_f32 v[116:117], v[140:141], v[136:137], v[116:117] op_sel:[1,1,0] op_sel_hi:[1,0,1]
	s_add_i32 s56, s62, -2
	v_pk_mul_f32 v[138:139], v[116:117], s[28:29]
	v_pk_mul_f32 v[116:117], v[96:97], v[116:117] op_sel_hi:[0,1]
	v_pk_fma_f32 v[96:97], v[96:97], v[138:139], v[116:117] op_sel:[1,1,0] op_sel_hi:[1,0,1]
	v_pk_mul_f32 v[116:117], v[144:145], v[156:157] op_sel_hi:[0,1]
	v_pk_fma_f32 v[116:117], v[144:145], v[136:137], v[116:117] op_sel:[1,1,0] op_sel_hi:[1,0,1]
	v_add_u32_e32 v236, v196, v197
	v_pk_mul_f32 v[138:139], v[116:117], s[28:29]
	v_pk_mul_f32 v[116:117], v[80:81], v[116:117] op_sel_hi:[0,1]
	v_pk_fma_f32 v[80:81], v[80:81], v[138:139], v[116:117] op_sel:[1,1,0] op_sel_hi:[1,0,1]
	v_pk_mul_f32 v[116:117], v[156:157], v[146:147] op_sel_hi:[1,0]
	v_add_u32_e32 v237, v196, v198
	v_pk_fma_f32 v[116:117], v[146:147], v[136:137], v[116:117] op_sel:[1,1,0] op_sel_hi:[1,0,1]
	s_nop 0
	v_pk_mul_f32 v[138:139], v[116:117], s[28:29]
	v_pk_mul_f32 v[116:117], v[6:7], v[116:117] op_sel_hi:[0,1]
	v_pk_fma_f32 v[6:7], v[6:7], v[138:139], v[116:117] op_sel:[1,1,0] op_sel_hi:[1,0,1]
	v_pk_mul_f32 v[116:117], v[156:157], v[148:149] op_sel_hi:[1,0]
	s_nop 0
	v_pk_fma_f32 v[116:117], v[148:149], v[136:137], v[116:117] op_sel:[1,1,0] op_sel_hi:[1,0,1]
	s_nop 0
	v_pk_mul_f32 v[138:139], v[116:117], s[28:29]
	v_pk_mul_f32 v[116:117], v[4:5], v[116:117] op_sel_hi:[0,1]
	v_pk_fma_f32 v[4:5], v[4:5], v[138:139], v[116:117] op_sel:[1,1,0] op_sel_hi:[1,0,1]
	v_pk_mul_f32 v[116:117], v[156:157], v[152:153] op_sel_hi:[1,0]
	s_nop 0
	v_pk_fma_f32 v[116:117], v[152:153], v[136:137], v[116:117] op_sel:[1,1,0] op_sel_hi:[1,0,1]
	s_nop 0
	v_pk_mul_f32 v[136:137], v[116:117], s[28:29]
	v_pk_mul_f32 v[116:117], v[82:83], v[116:117] op_sel_hi:[0,1]
	v_pk_fma_f32 v[82:83], v[82:83], v[136:137], v[116:117] op_sel:[1,1,0] op_sel_hi:[1,0,1]
	v_lshlrev_b32_e32 v116, 3, v160
	v_add_u32_e32 v158, v219, v116
	v_lshl_add_u32 v117, v86, 3, v158
	ds_write_b64 v117, v[132:133]
	v_add_u32_e32 v117, 0x100, v160
	v_ashrrev_i32_e32 v117, 4, v117
	v_lshl_add_u32 v117, v117, 3, v158
	ds_write_b64 v117, v[118:119] offset:2048
	v_add_u32_e32 v117, 0x200, v160
	v_ashrrev_i32_e32 v117, 4, v117
	v_lshl_add_u32 v117, v117, 3, v158
	ds_write_b64 v117, v[128:129] offset:4096
	v_add_u32_e32 v117, 0x300, v160
	v_ashrrev_i32_e32 v117, 4, v117
	v_lshl_add_u32 v117, v117, 3, v158
	ds_write_b64 v117, v[130:131] offset:6144
	v_add_u32_e32 v117, 0x400, v160
	v_ashrrev_i32_e32 v117, 4, v117
	v_lshl_add_u32 v117, v117, 3, v158
	ds_write_b64 v117, v[134:135] offset:8192
	v_add_u32_e32 v117, 0x500, v160
	v_ashrrev_i32_e32 v117, 4, v117
	v_lshl_add_u32 v117, v117, 3, v158
	ds_write_b64 v117, v[122:123] offset:10240
	v_add_u32_e32 v117, 0x600, v160
	v_ashrrev_i32_e32 v117, 4, v117
	v_lshl_add_u32 v117, v117, 3, v158
	ds_write_b64 v117, v[120:121] offset:12288
	v_add_u32_e32 v117, 0x700, v160
	v_ashrrev_i32_e32 v117, 4, v117
	v_lshl_add_u32 v117, v117, 3, v158
	ds_write_b64 v117, v[126:127] offset:14336
	v_add_u32_e32 v117, 0x800, v160
	v_ashrrev_i32_e32 v117, 4, v117
	v_lshl_add_u32 v117, v117, 3, v158
	ds_write_b64 v117, v[124:125] offset:16384
	v_add_u32_e32 v117, 0x900, v160
	v_ashrrev_i32_e32 v117, 4, v117
	v_lshl_add_u32 v117, v117, 3, v158
	ds_write_b64 v117, v[2:3] offset:18432
	v_add_u32_e32 v2, 0xa00, v160
	v_ashrrev_i32_e32 v2, 4, v2
	v_lshl_add_u32 v2, v2, 3, v158
	ds_write_b64 v2, v[114:115] offset:20480
	v_add_u32_e32 v2, 0xb00, v160
	v_ashrrev_i32_e32 v2, 4, v2
	v_lshl_add_u32 v2, v2, 3, v158
	ds_write_b64 v2, v[96:97] offset:22528
	v_add_u32_e32 v2, 0xc00, v160
	v_ashrrev_i32_e32 v2, 4, v2
	v_lshl_add_u32 v2, v2, 3, v158
	ds_write_b64 v2, v[80:81] offset:24576
	v_add_u32_e32 v2, 0xd00, v160
	v_ashrrev_i32_e32 v2, 4, v2
	v_lshl_add_u32 v2, v2, 3, v158
	ds_write_b64 v2, v[6:7] offset:26624
	v_add_u32_e32 v2, 0xe00, v160
	v_ashrrev_i32_e32 v2, 4, v2
	v_lshl_add_u32 v2, v2, 3, v158
	ds_write_b64 v2, v[4:5] offset:28672
	v_add_u32_e32 v2, 0xf00, v160
	v_ashrrev_i32_e32 v2, 4, v2
	v_lshl_add_u32 v2, v2, 3, v158
	ds_write_b64 v2, v[82:83] offset:30720
	v_lshlrev_b32_e32 v2, 8, v86
	v_lshl_add_u32 v3, v86, 7, v219
	v_lshlrev_b32_e32 v4, 11, v86
	v_and_b32_e32 v5, 0x78, v116
	v_add3_u32 v159, v3, v4, v5
	v_ashrrev_i32_e32 v2, 1, v2
	s_waitcnt lgkmcnt(0)
	s_barrier
	ds_read_b64 v[6:7], v159
	v_add_u32_e32 v2, v219, v2
	v_add3_u32 v161, v2, v4, v5
	ds_read2_b64 v[2:5], v161 offset0:17 offset1:34
	ds_read2_b64 v[80:83], v161 offset0:51 offset1:68
	ds_read2_b64 v[114:117], v161 offset0:85 offset1:102
	ds_read2_b64 v[118:121], v161 offset0:119 offset1:136
	ds_read2_b64 v[122:125], v161 offset0:153 offset1:170
	ds_read2_b64 v[126:129], v161 offset0:187 offset1:204
	ds_read2_b64 v[130:133], v161 offset0:221 offset1:238
	ds_read_b64 v[96:97], v161 offset:2040
	v_pk_mul_f32 v[136:137], v[0:1], v[0:1] op_sel_hi:[1,0]
	s_waitcnt lgkmcnt(4)
	v_pk_add_f32 v[134:135], v[6:7], v[120:121]
	v_pk_add_f32 v[6:7], v[6:7], v[120:121] neg_lo:[0,1] neg_hi:[0,1]
	s_waitcnt lgkmcnt(2)
	v_pk_add_f32 v[120:121], v[82:83], v[128:129]
	v_pk_add_f32 v[82:83], v[82:83], v[128:129] neg_lo:[0,1] neg_hi:[0,1]
	v_pk_add_f32 v[128:129], v[134:135], v[120:121]
	v_pk_add_f32 v[120:121], v[134:135], v[120:121] neg_lo:[0,1] neg_hi:[0,1]
	v_pk_fma_f32 v[134:135], v[82:83], s[28:29], v[6:7] op_sel:[1,0,0] op_sel_hi:[0,1,1]
	v_pk_fma_f32 v[6:7], v[82:83], s[26:27], v[6:7] op_sel:[1,0,0] op_sel_hi:[0,1,1]
	v_pk_add_f32 v[82:83], v[2:3], v[122:123]
	v_pk_add_f32 v[2:3], v[2:3], v[122:123] neg_lo:[0,1] neg_hi:[0,1]
	s_waitcnt lgkmcnt(1)
	v_pk_add_f32 v[122:123], v[114:115], v[130:131]
	v_pk_add_f32 v[114:115], v[114:115], v[130:131] neg_lo:[0,1] neg_hi:[0,1]
	v_pk_add_f32 v[130:131], v[82:83], v[122:123]
	v_pk_add_f32 v[82:83], v[82:83], v[122:123] neg_lo:[0,1] neg_hi:[0,1]
	v_pk_fma_f32 v[122:123], v[114:115], s[28:29], v[2:3] op_sel:[1,0,0] op_sel_hi:[0,1,1]
	v_pk_fma_f32 v[2:3], v[114:115], s[26:27], v[2:3] op_sel:[1,0,0] op_sel_hi:[0,1,1]
	v_pk_add_f32 v[114:115], v[4:5], v[124:125]
	v_pk_add_f32 v[4:5], v[4:5], v[124:125] neg_lo:[0,1] neg_hi:[0,1]
	v_pk_add_f32 v[124:125], v[116:117], v[132:133]
	v_pk_add_f32 v[116:117], v[116:117], v[132:133] neg_lo:[0,1] neg_hi:[0,1]
	v_pk_add_f32 v[132:133], v[114:115], v[124:125]
	v_pk_add_f32 v[114:115], v[114:115], v[124:125] neg_lo:[0,1] neg_hi:[0,1]
	v_pk_fma_f32 v[124:125], v[116:117], s[28:29], v[4:5] op_sel:[1,0,0] op_sel_hi:[0,1,1]
	v_pk_fma_f32 v[4:5], v[116:117], s[26:27], v[4:5] op_sel:[1,0,0] op_sel_hi:[0,1,1]
	v_pk_add_f32 v[116:117], v[80:81], v[126:127]
	v_pk_add_f32 v[80:81], v[80:81], v[126:127] neg_lo:[0,1] neg_hi:[0,1]
	s_waitcnt lgkmcnt(0)
	v_pk_add_f32 v[126:127], v[118:119], v[96:97]
	v_pk_add_f32 v[96:97], v[118:119], v[96:97] neg_lo:[0,1] neg_hi:[0,1]
	v_pk_add_f32 v[118:119], v[116:117], v[126:127]
	v_pk_add_f32 v[116:117], v[116:117], v[126:127] neg_lo:[0,1] neg_hi:[0,1]
	v_pk_fma_f32 v[126:127], v[96:97], s[28:29], v[80:81] op_sel:[1,0,0] op_sel_hi:[0,1,1]
	v_pk_fma_f32 v[80:81], v[96:97], s[26:27], v[80:81] op_sel:[1,0,0] op_sel_hi:[0,1,1]
	v_pk_mul_f32 v[96:97], v[122:123], s[8:9] op_sel_hi:[0,1]
	v_pk_fma_f32 v[96:97], v[122:123], s[0:1], v[96:97] op_sel:[1,0,0]
	v_pk_mul_f32 v[122:123], v[124:125], s[6:7] op_sel_hi:[0,1]
	v_pk_fma_f32 v[122:123], v[124:125], s[12:13], v[122:123] op_sel:[1,0,0] op_sel_hi:[1,0,1]
	v_pk_mul_f32 v[124:125], v[126:127], s[4:5] op_sel_hi:[0,1]
	v_pk_fma_f32 v[124:125], v[126:127], s[34:35], v[124:125] op_sel:[1,0,0]
	v_pk_mul_f32 v[126:127], v[82:83], s[6:7] op_sel_hi:[0,1]
	v_pk_fma_f32 v[82:83], v[82:83], s[12:13], v[126:127] op_sel:[1,0,0] op_sel_hi:[1,0,1]
	v_pk_mul_f32 v[126:127], v[114:115], s[18:19] op_sel_hi:[0,1]
	v_pk_fma_f32 v[114:115], v[114:115], s[50:51], v[126:127] op_sel:[1,0,0]
	v_pk_mul_f32 v[126:127], v[2:3], s[4:5] op_sel_hi:[0,1]
	v_pk_fma_f32 v[2:3], v[2:3], s[34:35], v[126:127] op_sel:[1,0,0]
	v_pk_mul_f32 v[126:127], v[80:81], s[38:39] op_sel_hi:[0,1]
	v_mul_f32_e32 v86, 0xbf3504f3, v116
	v_pk_fma_f32 v[80:81], v[80:81], s[30:31], v[126:127] op_sel:[1,0,0]
	v_pk_add_f32 v[126:127], v[128:129], v[132:133]
	v_pk_add_f32 v[128:129], v[128:129], v[132:133] neg_lo:[0,1] neg_hi:[0,1]
	v_pk_add_f32 v[132:133], v[130:131], v[118:119]
	v_pk_add_f32 v[118:119], v[130:131], v[118:119] neg_lo:[0,1] neg_hi:[0,1]
	v_pk_fma_f32 v[116:117], v[116:117], s[6:7], v[86:87] op_sel:[1,0,0] op_sel_hi:[1,1,0]
	v_mul_f32_e32 v86, 0xbf3504f3, v4
	v_pk_add_f32 v[130:131], v[126:127], v[132:133]
	v_pk_add_f32 v[126:127], v[126:127], v[132:133] neg_lo:[0,1] neg_hi:[0,1]
	v_pk_fma_f32 v[132:133], v[118:119], s[28:29], v[128:129] op_sel:[1,0,0] op_sel_hi:[0,1,1]
	v_pk_fma_f32 v[118:119], v[118:119], s[26:27], v[128:129] op_sel:[1,0,0] op_sel_hi:[0,1,1]
	v_pk_add_f32 v[128:129], v[134:135], v[122:123]
	v_pk_add_f32 v[122:123], v[134:135], v[122:123] neg_lo:[0,1] neg_hi:[0,1]
	v_pk_add_f32 v[134:135], v[96:97], v[124:125]
	v_pk_add_f32 v[96:97], v[96:97], v[124:125] neg_lo:[0,1] neg_hi:[0,1]
	v_pk_fma_f32 v[4:5], v[4:5], s[6:7], v[86:87] op_sel:[1,0,0] op_sel_hi:[1,1,0]
	v_pk_add_f32 v[124:125], v[128:129], v[134:135]
	v_pk_add_f32 v[128:129], v[128:129], v[134:135] neg_lo:[0,1] neg_hi:[0,1]
	v_pk_fma_f32 v[134:135], v[96:97], s[28:29], v[122:123] op_sel:[1,0,0] op_sel_hi:[0,1,1]
	v_pk_fma_f32 v[96:97], v[96:97], s[26:27], v[122:123] op_sel:[1,0,0] op_sel_hi:[0,1,1]
	v_pk_add_f32 v[122:123], v[120:121], v[114:115]
	v_pk_add_f32 v[114:115], v[120:121], v[114:115] neg_lo:[0,1] neg_hi:[0,1]
	v_pk_add_f32 v[120:121], v[82:83], v[116:117]
	v_pk_add_f32 v[82:83], v[82:83], v[116:117] neg_lo:[0,1] neg_hi:[0,1]
	v_pk_add_f32 v[116:117], v[122:123], v[120:121]
	v_pk_add_f32 v[120:121], v[122:123], v[120:121] neg_lo:[0,1] neg_hi:[0,1]
	v_pk_fma_f32 v[122:123], v[82:83], s[28:29], v[114:115] op_sel:[1,0,0] op_sel_hi:[0,1,1]
	v_pk_fma_f32 v[82:83], v[82:83], s[26:27], v[114:115] op_sel:[1,0,0] op_sel_hi:[0,1,1]
	v_pk_add_f32 v[114:115], v[6:7], v[4:5]
	v_pk_add_f32 v[4:5], v[6:7], v[4:5] neg_lo:[0,1] neg_hi:[0,1]
	v_pk_add_f32 v[6:7], v[2:3], v[80:81]
	v_pk_add_f32 v[2:3], v[2:3], v[80:81] neg_lo:[0,1] neg_hi:[0,1]
	v_pk_add_f32 v[80:81], v[114:115], v[6:7]
	v_pk_add_f32 v[6:7], v[114:115], v[6:7] neg_lo:[0,1] neg_hi:[0,1]
	v_pk_fma_f32 v[114:115], v[2:3], s[28:29], v[4:5] op_sel:[1,0,0] op_sel_hi:[0,1,1]
	v_pk_fma_f32 v[2:3], v[2:3], s[26:27], v[4:5] op_sel:[1,0,0] op_sel_hi:[0,1,1]
	v_pk_mul_f32 v[4:5], v[0:1], s[28:29]
	v_mov_b32_e32 v86, v1
	v_pk_fma_f32 v[136:137], v[86:87], v[4:5], v[136:137] op_sel:[0,1,0] op_sel_hi:[0,0,1]
	v_pk_mul_f32 v[140:141], v[136:137], s[28:29]
	v_pk_mul_f32 v[142:143], v[136:137], v[136:137] op_sel_hi:[1,0]
	v_pk_mul_f32 v[138:139], v[0:1], v[136:137] op_sel_hi:[1,0]
	v_pk_fma_f32 v[142:143], v[136:137], v[140:141], v[142:143] op_sel:[1,1,0] op_sel_hi:[1,0,1]
	v_pk_mul_f32 v[156:157], v[0:1], v[124:125] op_sel_hi:[1,0]
	v_pk_mul_f32 v[144:145], v[0:1], v[142:143] op_sel_hi:[1,0]
	v_pk_fma_f32 v[138:139], v[136:137], v[4:5], v[138:139] op_sel:[1,1,0] op_sel_hi:[1,0,1]
	v_pk_fma_f32 v[144:145], v[142:143], v[4:5], v[144:145] op_sel:[1,1,0] op_sel_hi:[1,0,1]
	v_pk_fma_f32 v[4:5], v[124:125], v[4:5], v[156:157] op_sel:[1,1,0] op_sel_hi:[1,0,1]
	v_pk_mul_f32 v[124:125], v[136:137], v[116:117] op_sel_hi:[1,0]
	v_pk_mul_f32 v[148:149], v[138:139], s[28:29]
	v_pk_fma_f32 v[116:117], v[116:117], v[140:141], v[124:125] op_sel:[1,1,0] op_sel_hi:[1,0,1]
	v_pk_mul_f32 v[124:125], v[138:139], v[80:81] op_sel_hi:[1,0]
	v_pk_mul_f32 v[146:147], v[136:137], v[142:143] op_sel_hi:[1,0]
	v_pk_mul_f32 v[152:153], v[142:143], s[28:29]
	v_pk_fma_f32 v[80:81], v[80:81], v[148:149], v[124:125] op_sel:[1,1,0] op_sel_hi:[1,0,1]
	v_pk_mul_f32 v[124:125], v[142:143], v[132:133] op_sel_hi:[1,0]
	v_pk_fma_f32 v[146:147], v[142:143], v[140:141], v[146:147] op_sel:[1,1,0] op_sel_hi:[1,0,1]
	v_pk_mul_f32 v[150:151], v[138:139], v[142:143] op_sel_hi:[1,0]
	v_pk_fma_f32 v[124:125], v[132:133], v[152:153], v[124:125] op_sel:[1,1,0] op_sel_hi:[1,0,1]
	v_pk_mul_f32 v[132:133], v[144:145], s[28:29]
	v_pk_mul_f32 v[140:141], v[144:145], v[134:135] op_sel_hi:[1,0]
	v_pk_fma_f32 v[150:151], v[142:143], v[148:149], v[150:151] op_sel:[1,1,0] op_sel_hi:[1,0,1]
	v_pk_mul_f32 v[154:155], v[142:143], v[142:143] op_sel_hi:[1,0]
	v_pk_fma_f32 v[132:133], v[134:135], v[132:133], v[140:141] op_sel:[1,1,0] op_sel_hi:[1,0,1]
	v_pk_mul_f32 v[134:135], v[146:147], s[28:29]
	v_pk_mul_f32 v[140:141], v[146:147], v[122:123] op_sel_hi:[1,0]
	v_pk_fma_f32 v[154:155], v[142:143], v[152:153], v[154:155] op_sel:[1,1,0] op_sel_hi:[1,0,1]
	v_pk_fma_f32 v[122:123], v[122:123], v[134:135], v[140:141] op_sel:[1,1,0] op_sel_hi:[1,0,1]
	v_pk_mul_f32 v[134:135], v[150:151], s[28:29]
	v_pk_mul_f32 v[140:141], v[150:151], v[114:115] op_sel_hi:[1,0]
	v_pk_mul_f32 v[0:1], v[0:1], v[154:155] op_sel_hi:[0,1]
	v_pk_fma_f32 v[114:115], v[114:115], v[134:135], v[140:141] op_sel:[1,1,0] op_sel_hi:[1,0,1]
	v_pk_mul_f32 v[134:135], v[154:155], s[28:29]
	v_pk_mul_f32 v[140:141], v[154:155], v[126:127] op_sel_hi:[1,0]
	v_pk_fma_f32 v[0:1], v[86:87], v[134:135], v[0:1] op_sel:[0,1,0] op_sel_hi:[0,0,1]
	v_pk_fma_f32 v[126:127], v[126:127], v[134:135], v[140:141] op_sel:[1,1,0] op_sel_hi:[1,0,1]
	v_pk_mul_f32 v[140:141], v[0:1], s[28:29]
	v_pk_mul_f32 v[0:1], v[0:1], v[128:129] op_sel_hi:[1,0]
	s_mov_b32 s13, 0x62700000
	v_pk_fma_f32 v[0:1], v[128:129], v[140:141], v[0:1] op_sel:[1,1,0] op_sel_hi:[1,0,1]
	v_pk_mul_f32 v[128:129], v[136:137], v[154:155] op_sel_hi:[0,1]
	v_pk_fma_f32 v[128:129], v[136:137], v[134:135], v[128:129] op_sel:[1,1,0] op_sel_hi:[1,0,1]
	v_lshl_add_u32 v86, v160, 7, v158
	v_pk_mul_f32 v[136:137], v[128:129], s[28:29]
	v_pk_mul_f32 v[128:129], v[128:129], v[120:121] op_sel_hi:[1,0]
	s_nop 0
	v_pk_fma_f32 v[120:121], v[120:121], v[136:137], v[128:129] op_sel:[1,1,0] op_sel_hi:[1,0,1]
	v_pk_mul_f32 v[128:129], v[138:139], v[154:155] op_sel_hi:[0,1]
	v_pk_fma_f32 v[128:129], v[138:139], v[134:135], v[128:129] op_sel:[1,1,0] op_sel_hi:[1,0,1]
	s_nop 0
	v_pk_mul_f32 v[136:137], v[128:129], s[28:29]
	v_pk_mul_f32 v[128:129], v[128:129], v[6:7] op_sel_hi:[1,0]
	s_nop 0
	v_pk_fma_f32 v[6:7], v[6:7], v[136:137], v[128:129] op_sel:[1,1,0] op_sel_hi:[1,0,1]
	v_pk_mul_f32 v[128:129], v[142:143], v[154:155] op_sel_hi:[0,1]
	v_pk_fma_f32 v[128:129], v[142:143], v[134:135], v[128:129] op_sel:[1,1,0] op_sel_hi:[1,0,1]
	s_nop 0
	v_pk_mul_f32 v[136:137], v[128:129], s[28:29]
	v_pk_mul_f32 v[128:129], v[128:129], v[118:119] op_sel_hi:[1,0]
	s_nop 0
	v_pk_fma_f32 v[118:119], v[118:119], v[136:137], v[128:129] op_sel:[1,1,0] op_sel_hi:[1,0,1]
	v_pk_mul_f32 v[128:129], v[154:155], v[144:145] op_sel_hi:[1,0]
	s_nop 0
	v_pk_fma_f32 v[128:129], v[144:145], v[134:135], v[128:129] op_sel:[1,1,0] op_sel_hi:[1,0,1]
	s_nop 0
	v_pk_mul_f32 v[136:137], v[128:129], s[28:29]
	v_pk_mul_f32 v[128:129], v[128:129], v[96:97] op_sel_hi:[1,0]
	s_nop 0
	v_pk_fma_f32 v[96:97], v[96:97], v[136:137], v[128:129] op_sel:[1,1,0] op_sel_hi:[1,0,1]
	v_pk_mul_f32 v[128:129], v[154:155], v[146:147] op_sel_hi:[1,0]
	s_nop 0
	v_pk_fma_f32 v[128:129], v[146:147], v[134:135], v[128:129] op_sel:[1,1,0] op_sel_hi:[1,0,1]
	s_nop 0
	v_pk_mul_f32 v[136:137], v[128:129], s[28:29]
	v_pk_mul_f32 v[128:129], v[128:129], v[82:83] op_sel_hi:[1,0]
	s_nop 0
	v_pk_fma_f32 v[82:83], v[82:83], v[136:137], v[128:129] op_sel:[1,1,0] op_sel_hi:[1,0,1]
	v_pk_mul_f32 v[128:129], v[154:155], v[150:151] op_sel_hi:[1,0]
	s_nop 0
	v_pk_fma_f32 v[128:129], v[150:151], v[134:135], v[128:129] op_sel:[1,1,0] op_sel_hi:[1,0,1]
	s_nop 0
	v_pk_mul_f32 v[134:135], v[128:129], s[28:29]
	v_pk_mul_f32 v[128:129], v[128:129], v[2:3] op_sel_hi:[1,0]
	s_nop 0
	v_pk_fma_f32 v[2:3], v[2:3], v[134:135], v[128:129] op_sel:[1,1,0] op_sel_hi:[1,0,1]
	ds_write_b64 v159, v[130:131]
	ds_write2_b64 v161, v[4:5], v[116:117] offset0:17 offset1:34
	ds_write2_b64 v161, v[80:81], v[124:125] offset0:51 offset1:68
	ds_write2_b64 v161, v[132:133], v[122:123] offset0:85 offset1:102
	ds_write2_b64 v161, v[114:115], v[126:127] offset0:119 offset1:136
	ds_write2_b64 v161, v[0:1], v[120:121] offset0:153 offset1:170
	ds_write2_b64 v161, v[6:7], v[118:119] offset0:187 offset1:204
	ds_write2_b64 v161, v[96:97], v[82:83] offset0:221 offset1:238
	ds_write_b64 v161, v[2:3] offset:2040
	v_lshl_add_u64 v[96:97], s[16:17], 0, v[94:95]
	v_add_co_u32_e32 v0, vcc, s13, v96
	s_mov_b32 s13, 0x62701000
	s_nop 0
	v_addc_co_u32_e32 v1, vcc, 0, v97, vcc
	v_add_co_u32_e32 v2, vcc, s13, v96
	s_mov_b32 s13, 0x62702000
	s_nop 0
	v_addc_co_u32_e32 v3, vcc, 0, v97, vcc
	v_add_co_u32_e32 v4, vcc, s13, v96
	s_mov_b32 s13, 0x62703000
	s_nop 0
	v_addc_co_u32_e32 v5, vcc, 0, v97, vcc
	v_add_co_u32_e32 v6, vcc, s13, v96
	s_nop 1
	v_addc_co_u32_e32 v7, vcc, 0, v97, vcc
	global_load_dword v136, v[2:3], off offset:-4096
	global_load_dword v138, v[0:1], off offset:1024
	global_load_dword v139, v[0:1], off offset:2048
	global_load_dword v140, v[0:1], off offset:3072
	global_load_dword v141, v[2:3], off
	global_load_dword v142, v[4:5], off offset:1024
	global_load_dword v143, v[4:5], off offset:2048
	global_load_dword v144, v[4:5], off offset:3072
	global_load_dword v145, v[2:3], off offset:1024
	global_load_dword v146, v[2:3], off offset:2048
	global_load_dword v147, v[2:3], off offset:3072
	global_load_dword v148, v[6:7], off offset:-4096
	global_load_dword v149, v[6:7], off
	global_load_dword v150, v[6:7], off offset:1024
	global_load_dword v151, v[6:7], off offset:2048
	global_load_dword v152, v[6:7], off offset:3072
	s_waitcnt lgkmcnt(0)
	s_barrier
	ds_read2_b64 v[0:3], v86 offset1:1
	ds_read2_b64 v[4:7], v86 offset0:2 offset1:3
	ds_read2_b64 v[80:83], v86 offset0:8 offset1:9
	ds_read2_b64 v[114:117], v86 offset0:4 offset1:5
	ds_read2_b64 v[118:121], v86 offset0:6 offset1:7
	ds_read2_b64 v[122:125], v86 offset0:12 offset1:13
	ds_read2_b64 v[126:129], v86 offset0:10 offset1:11
	ds_read2_b64 v[130:133], v86 offset0:14 offset1:15
	s_waitcnt lgkmcnt(5)
	v_pk_add_f32 v[134:135], v[0:1], v[80:81]
	v_pk_add_f32 v[0:1], v[0:1], v[80:81] neg_lo:[0,1] neg_hi:[0,1]
	s_waitcnt lgkmcnt(2)
	v_pk_add_f32 v[80:81], v[114:115], v[122:123]
	v_pk_add_f32 v[114:115], v[114:115], v[122:123] neg_lo:[0,1] neg_hi:[0,1]
	v_pk_add_f32 v[122:123], v[134:135], v[80:81]
	v_pk_add_f32 v[80:81], v[134:135], v[80:81] neg_lo:[0,1] neg_hi:[0,1]
	v_pk_fma_f32 v[134:135], v[114:115], s[28:29], v[0:1] op_sel:[1,0,0] op_sel_hi:[0,1,1]
	v_pk_fma_f32 v[0:1], v[114:115], s[26:27], v[0:1] op_sel:[1,0,0] op_sel_hi:[0,1,1]
	v_pk_add_f32 v[114:115], v[2:3], v[82:83]
	v_pk_add_f32 v[2:3], v[2:3], v[82:83] neg_lo:[0,1] neg_hi:[0,1]
	v_pk_add_f32 v[82:83], v[116:117], v[124:125]
	v_pk_add_f32 v[116:117], v[116:117], v[124:125] neg_lo:[0,1] neg_hi:[0,1]
	v_pk_add_f32 v[124:125], v[114:115], v[82:83]
	v_pk_add_f32 v[82:83], v[114:115], v[82:83] neg_lo:[0,1] neg_hi:[0,1]
	v_pk_fma_f32 v[114:115], v[116:117], s[28:29], v[2:3] op_sel:[1,0,0] op_sel_hi:[0,1,1]
	v_pk_fma_f32 v[2:3], v[116:117], s[26:27], v[2:3] op_sel:[1,0,0] op_sel_hi:[0,1,1]
	s_waitcnt lgkmcnt(1)
	v_pk_add_f32 v[116:117], v[4:5], v[126:127]
	v_pk_add_f32 v[4:5], v[4:5], v[126:127] neg_lo:[0,1] neg_hi:[0,1]
	s_waitcnt lgkmcnt(0)
	v_pk_add_f32 v[126:127], v[118:119], v[130:131]
	v_pk_add_f32 v[118:119], v[118:119], v[130:131] neg_lo:[0,1] neg_hi:[0,1]
	v_pk_add_f32 v[130:131], v[116:117], v[126:127]
	v_pk_add_f32 v[116:117], v[116:117], v[126:127] neg_lo:[0,1] neg_hi:[0,1]
	v_pk_fma_f32 v[126:127], v[118:119], s[28:29], v[4:5] op_sel:[1,0,0] op_sel_hi:[0,1,1]
	v_pk_fma_f32 v[4:5], v[118:119], s[26:27], v[4:5] op_sel:[1,0,0] op_sel_hi:[0,1,1]
	v_pk_add_f32 v[118:119], v[6:7], v[128:129]
	v_pk_add_f32 v[6:7], v[6:7], v[128:129] neg_lo:[0,1] neg_hi:[0,1]
	v_pk_add_f32 v[128:129], v[120:121], v[132:133]
	v_pk_add_f32 v[120:121], v[120:121], v[132:133] neg_lo:[0,1] neg_hi:[0,1]
	v_pk_add_f32 v[132:133], v[118:119], v[128:129]
	v_pk_add_f32 v[118:119], v[118:119], v[128:129] neg_lo:[0,1] neg_hi:[0,1]
	v_pk_fma_f32 v[128:129], v[120:121], s[28:29], v[6:7] op_sel:[1,0,0] op_sel_hi:[0,1,1]
	v_pk_fma_f32 v[6:7], v[120:121], s[26:27], v[6:7] op_sel:[1,0,0] op_sel_hi:[0,1,1]
	v_pk_mul_f32 v[120:121], v[114:115], s[8:9] op_sel_hi:[0,1]
	v_pk_fma_f32 v[114:115], v[114:115], s[0:1], v[120:121] op_sel:[1,0,0]
	v_pk_mul_f32 v[120:121], v[126:127], s[6:7] op_sel_hi:[0,1]
	v_pk_fma_f32 v[120:121], v[126:127], s[12:13], v[120:121] op_sel:[1,0,0] op_sel_hi:[1,0,1]
	v_pk_mul_f32 v[126:127], v[128:129], s[4:5] op_sel_hi:[0,1]
	v_pk_fma_f32 v[126:127], v[128:129], s[34:35], v[126:127] op_sel:[1,0,0]
	v_pk_mul_f32 v[128:129], v[82:83], s[6:7] op_sel_hi:[0,1]
	v_pk_fma_f32 v[82:83], v[82:83], s[12:13], v[128:129] op_sel:[1,0,0] op_sel_hi:[1,0,1]
	v_pk_mul_f32 v[128:129], v[116:117], s[18:19] op_sel_hi:[0,1]
	v_pk_fma_f32 v[116:117], v[116:117], s[50:51], v[128:129] op_sel:[1,0,0]
	v_pk_mul_f32 v[128:129], v[2:3], s[4:5] op_sel_hi:[0,1]
	v_pk_fma_f32 v[2:3], v[2:3], s[34:35], v[128:129] op_sel:[1,0,0]
	v_pk_mul_f32 v[128:129], v[6:7], s[38:39] op_sel_hi:[0,1]
	v_mul_f32_e32 v86, 0xbf3504f3, v118
	v_pk_fma_f32 v[6:7], v[6:7], s[30:31], v[128:129] op_sel:[1,0,0]
	v_pk_add_f32 v[128:129], v[122:123], v[130:131]
	v_pk_add_f32 v[122:123], v[122:123], v[130:131] neg_lo:[0,1] neg_hi:[0,1]
	v_pk_add_f32 v[130:131], v[124:125], v[132:133]
	v_pk_add_f32 v[124:125], v[124:125], v[132:133] neg_lo:[0,1] neg_hi:[0,1]
	v_pk_fma_f32 v[118:119], v[118:119], s[6:7], v[86:87] op_sel:[1,0,0] op_sel_hi:[1,1,0]
	v_mul_f32_e32 v86, 0xbf3504f3, v4
	v_pk_add_f32 v[132:133], v[128:129], v[130:131]
	v_pk_add_f32 v[128:129], v[128:129], v[130:131] neg_lo:[0,1] neg_hi:[0,1]
	v_pk_fma_f32 v[130:131], v[124:125], s[28:29], v[122:123] op_sel:[1,0,0] op_sel_hi:[0,1,1]
	v_pk_fma_f32 v[122:123], v[124:125], s[26:27], v[122:123] op_sel:[1,0,0] op_sel_hi:[0,1,1]
	v_pk_add_f32 v[124:125], v[134:135], v[120:121]
	v_pk_add_f32 v[120:121], v[134:135], v[120:121] neg_lo:[0,1] neg_hi:[0,1]
	v_pk_add_f32 v[134:135], v[114:115], v[126:127]
	v_pk_add_f32 v[114:115], v[114:115], v[126:127] neg_lo:[0,1] neg_hi:[0,1]
	v_pk_fma_f32 v[4:5], v[4:5], s[6:7], v[86:87] op_sel:[1,0,0] op_sel_hi:[1,1,0]
	v_pk_add_f32 v[126:127], v[124:125], v[134:135]
	v_pk_add_f32 v[124:125], v[124:125], v[134:135] neg_lo:[0,1] neg_hi:[0,1]
	v_pk_fma_f32 v[134:135], v[114:115], s[28:29], v[120:121] op_sel:[1,0,0] op_sel_hi:[0,1,1]
	v_pk_fma_f32 v[114:115], v[114:115], s[26:27], v[120:121] op_sel:[1,0,0] op_sel_hi:[0,1,1]
	v_pk_add_f32 v[120:121], v[80:81], v[116:117]
	v_pk_add_f32 v[80:81], v[80:81], v[116:117] neg_lo:[0,1] neg_hi:[0,1]
	v_pk_add_f32 v[116:117], v[82:83], v[118:119]
	v_pk_add_f32 v[82:83], v[82:83], v[118:119] neg_lo:[0,1] neg_hi:[0,1]
	v_pk_add_f32 v[118:119], v[120:121], v[116:117]
	v_pk_add_f32 v[116:117], v[120:121], v[116:117] neg_lo:[0,1] neg_hi:[0,1]
	v_pk_fma_f32 v[120:121], v[82:83], s[28:29], v[80:81] op_sel:[1,0,0] op_sel_hi:[0,1,1]
	v_pk_fma_f32 v[80:81], v[82:83], s[26:27], v[80:81] op_sel:[1,0,0] op_sel_hi:[0,1,1]
	v_pk_add_f32 v[82:83], v[0:1], v[4:5]
	v_pk_add_f32 v[0:1], v[0:1], v[4:5] neg_lo:[0,1] neg_hi:[0,1]
	v_pk_add_f32 v[4:5], v[2:3], v[6:7]
	v_pk_add_f32 v[2:3], v[2:3], v[6:7] neg_lo:[0,1] neg_hi:[0,1]
	v_pk_add_f32 v[6:7], v[82:83], v[4:5]
	v_pk_add_f32 v[4:5], v[82:83], v[4:5] neg_lo:[0,1] neg_hi:[0,1]
	v_pk_fma_f32 v[82:83], v[2:3], s[28:29], v[0:1] op_sel:[1,0,0] op_sel_hi:[0,1,1]
	v_pk_fma_f32 v[0:1], v[2:3], s[26:27], v[0:1] op_sel:[1,0,0] op_sel_hi:[0,1,1]
	s_waitcnt vmcnt(15)
	v_lshlrev_b32_e32 v2, 16, v136
	v_and_b32_e32 v3, 0xffff0000, v136
	v_pk_mul_f32 v[136:137], v[2:3], s[28:29]
	v_pk_mul_f32 v[2:3], v[132:133], v[2:3] op_sel_hi:[0,1]
	v_pk_fma_f32 v[2:3], v[132:133], v[136:137], v[2:3] op_sel:[1,1,0] op_sel_hi:[1,0,1]
	s_waitcnt vmcnt(14)
	v_lshlrev_b32_e32 v132, 16, v138
	v_and_b32_e32 v133, 0xffff0000, v138
	v_pk_mul_f32 v[136:137], v[132:133], s[28:29]
	v_pk_mul_f32 v[132:133], v[126:127], v[132:133] op_sel_hi:[0,1]
	v_pk_fma_f32 v[126:127], v[126:127], v[136:137], v[132:133] op_sel:[1,1,0] op_sel_hi:[1,0,1]
	s_waitcnt vmcnt(13)
	v_lshlrev_b32_e32 v132, 16, v139
	v_and_b32_e32 v133, 0xffff0000, v139
	v_pk_mul_f32 v[136:137], v[132:133], s[28:29]
	v_pk_mul_f32 v[132:133], v[118:119], v[132:133] op_sel_hi:[0,1]
	v_pk_fma_f32 v[118:119], v[118:119], v[136:137], v[132:133] op_sel:[1,1,0] op_sel_hi:[1,0,1]
	s_waitcnt vmcnt(12)
	v_lshlrev_b32_e32 v132, 16, v140
	v_and_b32_e32 v133, 0xffff0000, v140
	v_pk_mul_f32 v[136:137], v[132:133], s[28:29]
	v_pk_mul_f32 v[132:133], v[6:7], v[132:133] op_sel_hi:[0,1]
	v_pk_fma_f32 v[6:7], v[6:7], v[136:137], v[132:133] op_sel:[1,1,0] op_sel_hi:[1,0,1]
	s_waitcnt vmcnt(11)
	v_lshlrev_b32_e32 v132, 16, v141
	v_and_b32_e32 v133, 0xffff0000, v141
	v_pk_mul_f32 v[136:137], v[132:133], s[28:29]
	v_pk_mul_f32 v[132:133], v[130:131], v[132:133] op_sel_hi:[0,1]
	v_pk_fma_f32 v[130:131], v[130:131], v[136:137], v[132:133] op_sel:[1,1,0] op_sel_hi:[1,0,1]
	s_waitcnt vmcnt(7)
	v_lshlrev_b32_e32 v132, 16, v145
	v_and_b32_e32 v133, 0xffff0000, v145
	v_pk_mul_f32 v[136:137], v[132:133], s[28:29]
	v_pk_mul_f32 v[132:133], v[134:135], v[132:133] op_sel_hi:[0,1]
	v_pk_fma_f32 v[132:133], v[134:135], v[136:137], v[132:133] op_sel:[1,1,0] op_sel_hi:[1,0,1]
	s_waitcnt vmcnt(6)
	v_lshlrev_b32_e32 v134, 16, v146
	v_and_b32_e32 v135, 0xffff0000, v146
	v_pk_mul_f32 v[136:137], v[134:135], s[28:29]
	v_pk_mul_f32 v[134:135], v[120:121], v[134:135] op_sel_hi:[0,1]
	v_pk_fma_f32 v[120:121], v[120:121], v[136:137], v[134:135] op_sel:[1,1,0] op_sel_hi:[1,0,1]
	s_waitcnt vmcnt(5)
	v_lshlrev_b32_e32 v134, 16, v147
	v_and_b32_e32 v135, 0xffff0000, v147
	v_pk_mul_f32 v[136:137], v[134:135], s[28:29]
	v_pk_mul_f32 v[134:135], v[82:83], v[134:135] op_sel_hi:[0,1]
	v_pk_fma_f32 v[134:135], v[82:83], v[136:137], v[134:135] op_sel:[1,1,0] op_sel_hi:[1,0,1]
	s_waitcnt vmcnt(4)
	v_lshlrev_b32_e32 v82, 16, v148
	v_and_b32_e32 v83, 0xffff0000, v148
	v_pk_mul_f32 v[136:137], v[82:83], s[28:29]
	v_pk_mul_f32 v[82:83], v[128:129], v[82:83] op_sel_hi:[0,1]
	v_pk_fma_f32 v[128:129], v[128:129], v[136:137], v[82:83] op_sel:[1,1,0] op_sel_hi:[1,0,1]
	v_lshlrev_b32_e32 v82, 16, v142
	v_and_b32_e32 v83, 0xffff0000, v142
	v_pk_mul_f32 v[136:137], v[82:83], s[28:29]
	v_pk_mul_f32 v[82:83], v[124:125], v[82:83] op_sel_hi:[0,1]
	v_pk_fma_f32 v[124:125], v[124:125], v[136:137], v[82:83] op_sel:[1,1,0] op_sel_hi:[1,0,1]
	v_lshlrev_b32_e32 v82, 16, v143
	v_and_b32_e32 v83, 0xffff0000, v143
	v_pk_mul_f32 v[136:137], v[82:83], s[28:29]
	v_pk_mul_f32 v[82:83], v[116:117], v[82:83] op_sel_hi:[0,1]
	v_pk_fma_f32 v[116:117], v[116:117], v[136:137], v[82:83] op_sel:[1,1,0] op_sel_hi:[1,0,1]
	v_lshlrev_b32_e32 v82, 16, v144
	v_and_b32_e32 v83, 0xffff0000, v144
	v_pk_mul_f32 v[136:137], v[82:83], s[28:29]
	v_pk_mul_f32 v[82:83], v[4:5], v[82:83] op_sel_hi:[0,1]
	v_pk_fma_f32 v[4:5], v[4:5], v[136:137], v[82:83] op_sel:[1,1,0] op_sel_hi:[1,0,1]
	s_waitcnt vmcnt(3)
	v_lshlrev_b32_e32 v82, 16, v149
	v_and_b32_e32 v83, 0xffff0000, v149
	v_pk_mul_f32 v[136:137], v[82:83], s[28:29]
	v_pk_mul_f32 v[82:83], v[122:123], v[82:83] op_sel_hi:[0,1]
	v_pk_fma_f32 v[122:123], v[122:123], v[136:137], v[82:83] op_sel:[1,1,0] op_sel_hi:[1,0,1]
	s_waitcnt vmcnt(2)
	v_lshlrev_b32_e32 v82, 16, v150
	v_and_b32_e32 v83, 0xffff0000, v150
	v_pk_mul_f32 v[136:137], v[82:83], s[28:29]
	v_pk_mul_f32 v[82:83], v[114:115], v[82:83] op_sel_hi:[0,1]
	v_pk_fma_f32 v[136:137], v[114:115], v[136:137], v[82:83] op_sel:[1,1,0] op_sel_hi:[1,0,1]
	s_waitcnt vmcnt(1)
	v_lshlrev_b32_e32 v82, 16, v151
	v_and_b32_e32 v83, 0xffff0000, v151
	v_pk_mul_f32 v[114:115], v[82:83], s[28:29]
	v_pk_mul_f32 v[82:83], v[80:81], v[82:83] op_sel_hi:[0,1]
	v_pk_fma_f32 v[138:139], v[80:81], v[114:115], v[82:83] op_sel:[1,1,0] op_sel_hi:[1,0,1]
	s_waitcnt vmcnt(0)
	v_lshlrev_b32_e32 v80, 16, v152
	v_and_b32_e32 v81, 0xffff0000, v152
	v_pk_add_f32 v[140:141], v[2:3], v[128:129]
	v_pk_add_f32 v[2:3], v[2:3], v[128:129] neg_lo:[0,1] neg_hi:[0,1]
	v_pk_add_f32 v[128:129], v[130:131], v[122:123]
	v_pk_add_f32 v[122:123], v[130:131], v[122:123] neg_lo:[0,1] neg_hi:[0,1]
	v_pk_mul_f32 v[82:83], v[80:81], s[28:29]
	v_pk_mul_f32 v[80:81], v[0:1], v[80:81] op_sel_hi:[0,1]
	v_pk_add_f32 v[130:131], v[140:141], v[128:129]
	v_pk_add_f32 v[128:129], v[140:141], v[128:129] neg_lo:[0,1] neg_hi:[0,1]
	v_pk_fma_f32 v[140:141], v[122:123], s[26:27], v[2:3] op_sel:[1,0,0] op_sel_hi:[0,1,1]
	v_pk_fma_f32 v[2:3], v[122:123], s[28:29], v[2:3] op_sel:[1,0,0] op_sel_hi:[0,1,1]
	v_pk_add_f32 v[122:123], v[126:127], v[124:125]
	v_pk_add_f32 v[124:125], v[126:127], v[124:125] neg_lo:[0,1] neg_hi:[0,1]
	v_pk_add_f32 v[126:127], v[132:133], v[136:137]
	v_pk_add_f32 v[132:133], v[132:133], v[136:137] neg_lo:[0,1] neg_hi:[0,1]
	v_pk_fma_f32 v[0:1], v[0:1], v[82:83], v[80:81] op_sel:[1,1,0] op_sel_hi:[1,0,1]
	v_pk_add_f32 v[136:137], v[122:123], v[126:127]
	v_pk_add_f32 v[122:123], v[122:123], v[126:127] neg_lo:[0,1] neg_hi:[0,1]
	v_pk_fma_f32 v[126:127], v[132:133], s[26:27], v[124:125] op_sel:[1,0,0] op_sel_hi:[0,1,1]
	v_pk_fma_f32 v[124:125], v[132:133], s[28:29], v[124:125] op_sel:[1,0,0] op_sel_hi:[0,1,1]
	v_pk_add_f32 v[132:133], v[118:119], v[116:117]
	v_pk_add_f32 v[116:117], v[118:119], v[116:117] neg_lo:[0,1] neg_hi:[0,1]
	v_pk_add_f32 v[118:119], v[120:121], v[138:139]
	v_pk_add_f32 v[120:121], v[120:121], v[138:139] neg_lo:[0,1] neg_hi:[0,1]
	v_pk_add_f32 v[138:139], v[132:133], v[118:119]
	v_pk_add_f32 v[118:119], v[132:133], v[118:119] neg_lo:[0,1] neg_hi:[0,1]
	v_pk_fma_f32 v[132:133], v[120:121], s[26:27], v[116:117] op_sel:[1,0,0] op_sel_hi:[0,1,1]
	v_pk_fma_f32 v[116:117], v[120:121], s[28:29], v[116:117] op_sel:[1,0,0] op_sel_hi:[0,1,1]
	v_pk_add_f32 v[120:121], v[6:7], v[4:5]
	v_pk_add_f32 v[4:5], v[6:7], v[4:5] neg_lo:[0,1] neg_hi:[0,1]
	v_pk_add_f32 v[6:7], v[134:135], v[0:1]
	v_pk_add_f32 v[0:1], v[134:135], v[0:1] neg_lo:[0,1] neg_hi:[0,1]
	v_pk_add_f32 v[134:135], v[120:121], v[6:7]
	v_pk_add_f32 v[6:7], v[120:121], v[6:7] neg_lo:[0,1] neg_hi:[0,1]
	v_pk_fma_f32 v[120:121], v[0:1], s[26:27], v[4:5] op_sel:[1,0,0] op_sel_hi:[0,1,1]
	v_pk_fma_f32 v[0:1], v[0:1], s[28:29], v[4:5] op_sel:[1,0,0] op_sel_hi:[0,1,1]
	v_pk_mul_f32 v[4:5], v[126:127], s[34:35] op_sel_hi:[0,1]
	s_mov_b32 s31, s34
	v_mul_f32_e32 v86, 0x3f3504f3, v132
	v_pk_fma_f32 v[4:5], v[126:127], s[30:31], v[4:5] op_sel:[1,0,0]
	v_pk_fma_f32 v[126:127], v[132:133], s[36:37], v[86:87] op_sel:[1,0,0] op_sel_hi:[1,1,0]
	v_pk_mul_f32 v[132:133], v[120:121], s[0:1] op_sel_hi:[0,1]
	s_mov_b32 s19, s27
	v_pk_fma_f32 v[120:121], v[120:121], s[38:39], v[132:133] op_sel:[1,0,0]
	v_pk_mul_f32 v[132:133], v[118:119], s[18:19] op_sel_hi:[0,1]
	s_mov_b32 s6, s26
	s_mov_b32 s7, s18
	v_pk_fma_f32 v[118:119], v[118:119], s[6:7], v[132:133] op_sel:[1,0,0]
	v_pk_mul_f32 v[132:133], v[6:7], s[36:37] op_sel_hi:[0,1]
	v_pk_fma_f32 v[6:7], v[6:7], s[36:37], v[132:133] op_sel:[1,0,0] op_sel_hi:[1,0,1]
	v_pk_mul_f32 v[132:133], v[124:125], s[0:1] op_sel_hi:[0,1]
	s_min_i32 s0, s56, s59
	s_mul_i32 s0, s0, s3
	v_pk_fma_f32 v[124:125], v[124:125], s[38:39], v[132:133] op_sel:[1,0,0]
	v_pk_mul_f32 v[132:133], v[116:117], s[36:37] op_sel_hi:[0,1]
	s_mov_b32 s39, s30
	s_add_i32 s0, s0, s2
	v_pk_fma_f32 v[116:117], v[116:117], s[36:37], v[132:133] op_sel:[1,0,0] op_sel_hi:[1,0,1]
	v_pk_mul_f32 v[132:133], v[0:1], s[38:39] op_sel_hi:[0,1]
	s_mul_hi_i32 s1, s0, 0x2aaaaaab
	v_pk_fma_f32 v[0:1], v[0:1], s[4:5], v[132:133] op_sel:[1,0,0]
	s_lshr_b32 s4, s1, 31
	s_lshr_b32 s1, s1, 7
	v_mul_f32_e32 v86, 0x3f3504f3, v122
	v_pk_add_f32 v[132:133], v[130:131], v[138:139]
	v_pk_add_f32 v[130:131], v[130:131], v[138:139] neg_lo:[0,1] neg_hi:[0,1]
	v_pk_add_f32 v[138:139], v[136:137], v[134:135]
	v_pk_add_f32 v[134:135], v[136:137], v[134:135] neg_lo:[0,1] neg_hi:[0,1]
	s_add_i32 s1, s1, s4
	v_pk_fma_f32 v[122:123], v[122:123], s[36:37], v[86:87] op_sel:[1,0,0] op_sel_hi:[1,1,0]
	v_pk_add_f32 v[136:137], v[132:133], v[138:139]
	v_pk_add_f32 v[132:133], v[132:133], v[138:139] neg_lo:[0,1] neg_hi:[0,1]
	v_pk_fma_f32 v[138:139], v[134:135], s[26:27], v[130:131] op_sel:[1,0,0] op_sel_hi:[0,1,1]
	v_pk_fma_f32 v[130:131], v[134:135], s[28:29], v[130:131] op_sel:[1,0,0] op_sel_hi:[0,1,1]
	v_pk_add_f32 v[134:135], v[140:141], v[126:127]
	v_pk_add_f32 v[126:127], v[140:141], v[126:127] neg_lo:[0,1] neg_hi:[0,1]
	v_pk_add_f32 v[140:141], v[4:5], v[120:121]
	v_pk_add_f32 v[4:5], v[4:5], v[120:121] neg_lo:[0,1] neg_hi:[0,1]
	s_mulk_i32 s1, 0x300
	v_pk_add_f32 v[120:121], v[134:135], v[140:141]
	v_pk_add_f32 v[134:135], v[134:135], v[140:141] neg_lo:[0,1] neg_hi:[0,1]
	v_pk_fma_f32 v[140:141], v[4:5], s[26:27], v[126:127] op_sel:[1,0,0] op_sel_hi:[0,1,1]
	v_pk_fma_f32 v[4:5], v[4:5], s[28:29], v[126:127] op_sel:[1,0,0] op_sel_hi:[0,1,1]
	v_pk_add_f32 v[126:127], v[128:129], v[118:119]
	v_pk_add_f32 v[118:119], v[128:129], v[118:119] neg_lo:[0,1] neg_hi:[0,1]
	v_pk_add_f32 v[128:129], v[122:123], v[6:7]
	v_pk_add_f32 v[6:7], v[122:123], v[6:7] neg_lo:[0,1] neg_hi:[0,1]
	s_sub_i32 s0, s0, s1
	v_mov_b32_e32 v115, v220
	v_mov_b32_e32 v81, v221
	v_mov_b32_e32 v114, v217
	v_mov_b32_e32 v80, v218
	v_mov_b32_e32 v82, v215
	v_pk_add_f32 v[122:123], v[126:127], v[128:129]
	v_pk_add_f32 v[126:127], v[126:127], v[128:129] neg_lo:[0,1] neg_hi:[0,1]
	v_pk_fma_f32 v[128:129], v[6:7], s[26:27], v[118:119] op_sel:[1,0,0] op_sel_hi:[0,1,1]
	v_pk_fma_f32 v[6:7], v[6:7], s[28:29], v[118:119] op_sel:[1,0,0] op_sel_hi:[0,1,1]
	v_pk_add_f32 v[118:119], v[2:3], v[116:117]
	v_pk_add_f32 v[2:3], v[2:3], v[116:117] neg_lo:[0,1] neg_hi:[0,1]
	v_pk_add_f32 v[116:117], v[124:125], v[0:1]
	v_pk_add_f32 v[0:1], v[124:125], v[0:1] neg_lo:[0,1] neg_hi:[0,1]
	s_cmpk_lt_i32 s0, 0x200
	v_pk_add_f32 v[124:125], v[118:119], v[116:117]
	v_pk_add_f32 v[116:117], v[118:119], v[116:117] neg_lo:[0,1] neg_hi:[0,1]
	v_pk_fma_f32 v[118:119], v[0:1], s[26:27], v[2:3] op_sel:[1,0,0] op_sel_hi:[0,1,1]
	v_pk_fma_f32 v[0:1], v[0:1], s[28:29], v[2:3] op_sel:[1,0,0] op_sel_hi:[0,1,1]
	v_lshlrev_b32_e32 v83, 3, v82
	v_lshlrev_b32_e32 v2, 7, v82
	s_cselect_b64 vcc, -1, 0
	v_add3_u32 v2, v219, v83, v2
	v_cndmask_b32_e32 v86, v211, v212, vcc
	ds_write2_b64 v2, v[136:137], v[120:121] offset1:1
	ds_write2_b64 v2, v[122:123], v[124:125] offset0:2 offset1:3
	ds_write2_b64 v2, v[138:139], v[140:141] offset0:4 offset1:5
	ds_write2_b64 v2, v[128:129], v[118:119] offset0:6 offset1:7
	ds_write2_b64 v2, v[132:133], v[134:135] offset0:8 offset1:9
	ds_write2_b64 v2, v[126:127], v[116:117] offset0:10 offset1:11
	ds_write2_b64 v2, v[130:131], v[4:5] offset0:12 offset1:13
	ds_write2_b64 v2, v[6:7], v[0:1] offset0:14 offset1:15
	v_mul_f32_e32 v1, v48, v86
	v_mul_f32_e32 v2, v52, v86
	v_mov_b32_e32 v0, v87
	v_cvt_pk_fp8_f32 v0, v1, v2
	v_mul_f32_e32 v2, v49, v86
	v_mul_f32_e32 v5, v53, v86
	v_mov_b32_e32 v1, v87
	v_cvt_pk_fp8_f32 v1, v2, v5
	v_mul_f32_e32 v3, v64, v86
	v_mul_f32_e32 v4, v68, v86
	v_cvt_pk_fp8_f32 v0, v3, v4 op_sel:[0,0,1]
	v_mul_f32_e32 v2, v65, v86
	v_mul_f32_e32 v3, v69, v86
	v_cvt_pk_fp8_f32 v1, v2, v3 op_sel:[0,0,1]
	v_mul_f32_e32 v3, v50, v86
	v_mul_f32_e32 v4, v54, v86
	v_mov_b32_e32 v2, v87
	v_cvt_pk_fp8_f32 v2, v3, v4
	v_mul_f32_e32 v4, v51, v86
	v_mul_f32_e32 v7, v55, v86
	v_mov_b32_e32 v3, v87
	v_cvt_pk_fp8_f32 v3, v4, v7
	v_mul_f32_e32 v5, v66, v86
	v_mul_f32_e32 v6, v70, v86
	v_cvt_pk_fp8_f32 v2, v5, v6 op_sel:[0,0,1]
	v_mul_f32_e32 v4, v67, v86
	v_mul_f32_e32 v5, v71, v86
	v_cvt_pk_fp8_f32 v3, v4, v5 op_sel:[0,0,1]
	v_mul_f32_e32 v5, v40, v86
	v_mul_f32_e32 v6, v86, v44
	v_mov_b32_e32 v4, v87
	v_cvt_pk_fp8_f32 v4, v5, v6
	v_mul_f32_e32 v6, v41, v86
	v_mul_f32_e32 v41, v86, v45
	v_mov_b32_e32 v5, v87
	v_cvt_pk_fp8_f32 v5, v6, v41
	v_mul_f32_e32 v7, v86, v56
	v_mul_f32_e32 v40, v86, v60
	v_cvt_pk_fp8_f32 v4, v7, v40 op_sel:[0,0,1]
	v_mul_f32_e32 v6, v86, v57
	v_mul_f32_e32 v7, v86, v61
	v_cvt_pk_fp8_f32 v5, v6, v7 op_sel:[0,0,1]
	v_mul_f32_e32 v7, v42, v86
	v_mul_f32_e32 v40, v86, v46
	v_mov_b32_e32 v6, v87
	s_min_i32 s0, s62, s59
	v_cvt_pk_fp8_f32 v6, v7, v40
	v_mul_f32_e32 v40, v43, v86
	v_mul_f32_e32 v43, v86, v47
	v_mov_b32_e32 v7, v87
	s_mul_i32 s0, s0, s3
	v_cvt_pk_fp8_f32 v7, v40, v43
	s_add_i32 s1, s0, s2
	s_mul_hi_i32 s0, s1, 0x2aaaaaab
	v_mul_f32_e32 v41, v86, v58
	v_mul_f32_e32 v42, v86, v62
	s_lshr_b32 s4, s0, 31
	s_ashr_i32 s0, s0, 7
	v_cvt_pk_fp8_f32 v6, v41, v42 op_sel:[0,0,1]
	v_mul_f32_e32 v40, v86, v59
	v_mul_f32_e32 v41, v86, v63
	s_add_i32 s4, s0, s4
	v_cvt_pk_fp8_f32 v7, v40, v41 op_sel:[0,0,1]
	s_add_i32 s0, s4, 11
	s_mulk_i32 s4, 0x300
	s_sub_i32 s19, s1, s4
	s_cmpk_lt_i32 s19, 0x200
	s_cselect_b64 s[4:5], -1, 0
	s_cmpk_gt_i32 s19, 0x1ff
	s_mov_b64 s[12:13], -1
	s_waitcnt lgkmcnt(0)
	s_barrier
	ds_write_b128 v236, v[0:3]
	ds_write_b128 v237, v[4:7]
	s_cbranch_scc0 .LBB0_807
	s_load_dwordx2 s[6:7], s[14:15], 0x110
	s_ashr_i32 s1, s0, 31
	s_lshl_b64 s[12:13], s[0:1], 24
	s_mov_b32 s9, s18
	s_waitcnt lgkmcnt(0)
	s_add_u32 s6, s6, s12
	s_addc_u32 s7, s7, s13
	s_lshl_b32 s1, s19, 3
	s_and_b32 s1, s1, 0x7fffffc0
	s_add_i32 s8, s1, 0xfffff000
	s_mov_b64 s[12:13], 0

.LBB0_809:
	s_lshl_b64 s[8:9], s[8:9], 13
	s_add_u32 s0, s6, s8
	s_addc_u32 s7, s7, s9
	s_lshl_b32 s1, s19, s1
	s_and_b32 s1, s1, 0x700
	s_lshl_b32 s1, s1, 2
	s_add_u32 s6, s0, s1
	s_addc_u32 s7, s7, 0
	s_cmp_gt_i32 s62, s59
	s_cselect_b64 s[0:1], -1, 0
	v_cndmask_b32_e64 v0, v180, 0, s[0:1]
	s_and_b64 s[8:9], s[0:1], exec
	s_cselect_b32 s8, 0, 0x800
	v_lshlrev_b32_e32 v86, 2, v0
	v_lshl_add_u64 v[40:41], s[6:7], 0, v[86:87]
	v_mad_i64_i32 v[0:1], s[6:7], s8, v181, 0
	v_mad_i64_i32 v[2:3], s[6:7], s8, v182, 0
	v_lshl_add_u64 v[0:1], v[0:1], 2, v[40:41]
	v_lshl_add_u64 v[2:3], v[2:3], 2, v[40:41]
	global_load_dwordx4 v[48:51], v[0:1], off nt
	global_load_dwordx4 v[52:55], v[2:3], off nt
	v_mad_i64_i32 v[0:1], s[6:7], s8, v183, 0
	v_mad_i64_i32 v[2:3], s[6:7], s8, v184, 0
	v_lshl_add_u64 v[0:1], v[0:1], 2, v[40:41]
	v_lshl_add_u64 v[2:3], v[2:3], 2, v[40:41]
	global_load_dwordx4 v[56:59], v[0:1], off nt
	global_load_dwordx4 v[60:63], v[2:3], off nt
	v_mad_i64_i32 v[0:1], s[6:7], s8, v185, 0
	v_mad_i64_i32 v[2:3], s[6:7], s8, v186, 0
	v_mad_i64_i32 v[42:43], s[6:7], s8, v187, 0
	v_mad_i64_i32 v[44:45], s[6:7], s8, v188, 0
	v_lshl_add_u64 v[0:1], v[0:1], 2, v[40:41]
	v_lshl_add_u64 v[4:5], v[2:3], 2, v[40:41]
	v_lshl_add_u64 v[42:43], v[42:43], 2, v[40:41]
	v_lshl_add_u64 v[44:45], v[44:45], 2, v[40:41]
	global_load_dwordx4 v[0:3], v[0:1], off nt
	s_nop 0
	global_load_dwordx4 v[4:7], v[4:5], off nt
	s_nop 0
	global_load_dwordx4 v[40:43], v[42:43], off nt
	s_nop 0
	global_load_dwordx4 v[44:47], v[44:45], off nt
	s_add_i32 s19, s62, -3
	s_cmp_gt_i32 s62, 2
	s_cselect_b32 s6, s19, 0
	s_min_i32 s6, s6, s59
	s_mul_i32 s6, s6, s3
	s_add_i32 s7, s6, s2
	s_mul_hi_i32 s6, s7, 0x2aaaaaab
	s_lshr_b32 s8, s6, 31
	s_ashr_i32 s6, s6, 7
	s_add_i32 s8, s6, s8
	s_add_i32 s6, s8, 11
	s_mulk_i32 s8, 0x300
	s_sub_i32 s31, s7, s8
	s_ashr_i32 s7, s6, 31
	s_cmpk_gt_i32 s31, 0x1ff
	s_mov_b64 s[12:13], -1
	s_cbranch_scc0 .LBB0_811
	s_lshl_b32 s8, s31, 3
	s_and_b32 s12, s8, 0x7fffffc0
	s_lshl_b32 s8, s31, 19
	s_and_b32 s13, s8, 0x380000
	s_lshl_b64 s[8:9], s[6:7], 22
	s_add_u32 s8, s16, s8
	s_addc_u32 s9, s17, s9
	s_add_u32 s8, s8, s13
	s_addc_u32 s9, s9, 0
	s_add_u32 s8, s8, s12
	s_addc_u32 s9, s9, 0
	s_add_u32 s8, s8, 0x24dff000
	s_addc_u32 s9, s9, 0
	s_mov_b64 s[12:13], 0

.LBB0_813:
	s_add_i32 s76, s62, 1
	s_cmp_lt_i32 s62, 3
	s_cselect_b64 s[6:7], -1, 0
	s_cmp_gt_i32 s19, s59
	s_cselect_b64 s[50:51], -1, 0
	s_or_b64 s[6:7], s[6:7], s[50:51]
	s_and_b64 s[6:7], s[6:7], exec
	s_cselect_b32 s6, s65, s8
	s_cselect_b32 s8, 0x80, s12
	v_mul_i32_i24_e32 v64, s8, v191
	v_or_b32_e32 v64, v64, v189
	v_ashrrev_i32_e32 v65, 31, v64
	s_cselect_b32 s7, s66, s9
	v_lshlrev_b64 v[64:65], 11, v[64:65]
	v_add_u32_e32 v235, v199, v190
	v_lshl_add_u64 v[64:65], s[6:7], 0, v[64:65]
	v_lshl_add_u64 v[116:117], v[64:65], 0, v[88:89]
	v_add_u32_e32 v238, v199, v200
	ds_read_b32 v64, v235
	ds_read_b32 v65, v235 offset:1040
	ds_read_b32 v66, v235 offset:2080
	ds_read_b32 v67, v235 offset:3120
	ds_read_b32 v68, v238
	ds_read_b32 v69, v238 offset:1040
	ds_read_b32 v70, v238 offset:2080
	ds_read_b32 v71, v238 offset:3120
	s_waitcnt lgkmcnt(4)
	global_store_dwordx4 v[116:117], v[64:67], off nt
	v_pk_mul_f32 v[80:81], v[80:81], s[28:29]
	s_mov_b32 s31, s34
	v_mul_i32_i24_e32 v64, s8, v201
	v_or_b32_e32 v64, v64, v189
	v_ashrrev_i32_e32 v65, 31, v64
	v_lshlrev_b64 v[64:65], 11, v[64:65]
	v_lshl_add_u64 v[64:65], s[6:7], 0, v[64:65]
	v_lshl_add_u64 v[64:65], v[64:65], 0, v[88:89]
	s_waitcnt lgkmcnt(0)
	global_store_dwordx4 v[64:65], v[68:71], off nt
	v_ashrrev_i32_e32 v64, 4, v82
	v_lshlrev_b32_e32 v65, 8, v64
	v_pk_mul_f32 v[142:143], v[80:81], s[28:29]
	v_pk_mul_f32 v[144:145], v[80:81], v[80:81] op_sel_hi:[1,0]
	v_ashrrev_i32_e32 v65, 1, v65
	v_pk_fma_f32 v[144:145], v[80:81], v[142:143], v[144:145] op_sel:[1,1,0] op_sel_hi:[1,0,1]
	v_lshlrev_b32_e32 v67, 11, v64
	v_and_b32_e32 v68, 0x78, v83
	v_add_u32_e32 v65, v219, v65
	v_pk_mul_f32 v[148:149], v[144:145], s[28:29]
	v_pk_mul_f32 v[150:151], v[144:145], v[144:145] op_sel_hi:[1,0]
	v_lshl_add_u32 v66, v64, 7, v219
	v_add3_u32 v65, v65, v67, v68
	v_pk_fma_f32 v[150:151], v[144:145], v[148:149], v[150:151] op_sel:[1,1,0] op_sel_hi:[1,0,1]
	v_add3_u32 v166, v66, v67, v68
	ds_read2_b64 v[66:69], v65 offset0:17 offset1:34
	ds_read2_b64 v[116:119], v65 offset0:51 offset1:68
	ds_read2_b64 v[120:123], v65 offset0:85 offset1:102
	ds_read2_b64 v[124:127], v65 offset0:119 offset1:136
	ds_read2_b64 v[128:131], v65 offset0:153 offset1:170
	ds_read2_b64 v[132:135], v65 offset0:187 offset1:204
	ds_read2_b64 v[136:139], v65 offset0:221 offset1:238
	ds_read_b64 v[70:71], v166
	ds_read_b64 v[140:141], v65 offset:2040
	v_pk_mul_f32 v[146:147], v[80:81], v[144:145] op_sel_hi:[1,0]
	v_pk_mul_f32 v[152:153], v[80:81], v[150:151] op_sel_hi:[1,0]
	s_waitcnt lgkmcnt(8)
	v_pk_mul_f32 v[164:165], v[80:81], v[66:67] op_sel_hi:[1,0]
	v_pk_fma_f32 v[146:147], v[144:145], v[142:143], v[146:147] op_sel:[1,1,0] op_sel_hi:[1,0,1]
	v_pk_fma_f32 v[152:153], v[150:151], v[142:143], v[152:153] op_sel:[1,1,0] op_sel_hi:[1,0,1]
	v_pk_fma_f32 v[66:67], v[66:67], v[142:143], v[164:165] op_sel:[1,1,0] op_sel_hi:[1,0,1]
	v_pk_mul_f32 v[142:143], v[144:145], v[68:69] op_sel_hi:[1,0]
	v_pk_mul_f32 v[156:157], v[146:147], s[28:29]
	v_pk_fma_f32 v[68:69], v[68:69], v[148:149], v[142:143] op_sel:[1,1,0] op_sel_hi:[1,0,1]
	s_waitcnt lgkmcnt(7)
	v_pk_mul_f32 v[142:143], v[146:147], v[116:117] op_sel_hi:[1,0]
	v_pk_mul_f32 v[154:155], v[144:145], v[150:151] op_sel_hi:[1,0]
	v_pk_mul_f32 v[160:161], v[150:151], s[28:29]
	v_pk_fma_f32 v[116:117], v[116:117], v[156:157], v[142:143] op_sel:[1,1,0] op_sel_hi:[1,0,1]
	v_pk_mul_f32 v[142:143], v[150:151], v[118:119] op_sel_hi:[1,0]
	v_pk_fma_f32 v[154:155], v[150:151], v[148:149], v[154:155] op_sel:[1,1,0] op_sel_hi:[1,0,1]
	v_pk_mul_f32 v[158:159], v[146:147], v[150:151] op_sel_hi:[1,0]
	v_pk_fma_f32 v[118:119], v[118:119], v[160:161], v[142:143] op_sel:[1,1,0] op_sel_hi:[1,0,1]
	v_pk_mul_f32 v[142:143], v[152:153], s[28:29]
	s_waitcnt lgkmcnt(6)
	v_pk_mul_f32 v[148:149], v[152:153], v[120:121] op_sel_hi:[1,0]
	v_pk_fma_f32 v[158:159], v[150:151], v[156:157], v[158:159] op_sel:[1,1,0] op_sel_hi:[1,0,1]
	v_pk_mul_f32 v[162:163], v[150:151], v[150:151] op_sel_hi:[1,0]
	v_pk_fma_f32 v[120:121], v[120:121], v[142:143], v[148:149] op_sel:[1,1,0] op_sel_hi:[1,0,1]
	v_pk_mul_f32 v[142:143], v[154:155], s[28:29]
	v_pk_mul_f32 v[148:149], v[154:155], v[122:123] op_sel_hi:[1,0]
	v_pk_fma_f32 v[162:163], v[150:151], v[160:161], v[162:163] op_sel:[1,1,0] op_sel_hi:[1,0,1]
	v_pk_fma_f32 v[122:123], v[122:123], v[142:143], v[148:149] op_sel:[1,1,0] op_sel_hi:[1,0,1]
	v_pk_mul_f32 v[142:143], v[158:159], s[28:29]
	s_waitcnt lgkmcnt(5)
	v_pk_mul_f32 v[148:149], v[158:159], v[124:125] op_sel_hi:[1,0]
	s_mov_b32 s6, s35
	v_pk_fma_f32 v[124:125], v[124:125], v[142:143], v[148:149] op_sel:[1,1,0] op_sel_hi:[1,0,1]
	v_pk_mul_f32 v[142:143], v[162:163], s[28:29]
	v_pk_mul_f32 v[148:149], v[162:163], v[126:127] op_sel_hi:[1,0]
	s_mov_b32 s7, s34
	v_pk_fma_f32 v[126:127], v[126:127], v[142:143], v[148:149] op_sel:[1,1,0] op_sel_hi:[1,0,1]
	v_pk_mul_f32 v[148:149], v[80:81], v[162:163] op_sel_hi:[0,1]
	v_pk_fma_f32 v[80:81], v[80:81], v[142:143], v[148:149] op_sel:[1,1,0] op_sel_hi:[1,0,1]
	s_mov_b32 s39, s35
	v_pk_mul_f32 v[148:149], v[80:81], s[28:29]
	s_waitcnt lgkmcnt(4)
	v_pk_mul_f32 v[80:81], v[80:81], v[128:129] op_sel_hi:[1,0]
	s_mov_b32 s19, s27
	v_pk_fma_f32 v[80:81], v[128:129], v[148:149], v[80:81] op_sel:[1,1,0] op_sel_hi:[1,0,1]
	v_pk_mul_f32 v[128:129], v[144:145], v[162:163] op_sel_hi:[0,1]
	v_pk_fma_f32 v[128:129], v[144:145], v[142:143], v[128:129] op_sel:[1,1,0] op_sel_hi:[1,0,1]
	s_mov_b32 s8, s26
	v_pk_mul_f32 v[144:145], v[128:129], s[28:29]
	v_pk_mul_f32 v[128:129], v[128:129], v[130:131] op_sel_hi:[1,0]
	s_mov_b32 s9, s18
	v_pk_fma_f32 v[128:129], v[130:131], v[144:145], v[128:129] op_sel:[1,1,0] op_sel_hi:[1,0,1]
	v_pk_mul_f32 v[130:131], v[146:147], v[162:163] op_sel_hi:[0,1]
	v_pk_fma_f32 v[130:131], v[146:147], v[142:143], v[130:131] op_sel:[1,1,0] op_sel_hi:[1,0,1]
	v_add_u32_e32 v240, v202, v197
	v_pk_mul_f32 v[144:145], v[130:131], s[28:29]
	s_waitcnt lgkmcnt(3)
	v_pk_mul_f32 v[130:131], v[130:131], v[132:133] op_sel_hi:[1,0]
	v_add_u32_e32 v241, v202, v198
	v_pk_fma_f32 v[130:131], v[132:133], v[144:145], v[130:131] op_sel:[1,1,0] op_sel_hi:[1,0,1]
	v_pk_mul_f32 v[132:133], v[150:151], v[162:163] op_sel_hi:[0,1]
	v_pk_fma_f32 v[132:133], v[150:151], v[142:143], v[132:133] op_sel:[1,1,0] op_sel_hi:[1,0,1]
	s_mov_b64 s[52:53], -1
	v_pk_mul_f32 v[144:145], v[132:133], s[28:29]
	v_pk_mul_f32 v[132:133], v[132:133], v[134:135] op_sel_hi:[1,0]
	s_nop 0
	v_pk_fma_f32 v[132:133], v[134:135], v[144:145], v[132:133] op_sel:[1,1,0] op_sel_hi:[1,0,1]
	v_pk_mul_f32 v[134:135], v[162:163], v[152:153] op_sel_hi:[1,0]
	s_nop 0
	v_pk_fma_f32 v[134:135], v[152:153], v[142:143], v[134:135] op_sel:[1,1,0] op_sel_hi:[1,0,1]
	s_nop 0
	v_pk_mul_f32 v[144:145], v[134:135], s[28:29]
	s_waitcnt lgkmcnt(2)
	v_pk_mul_f32 v[134:135], v[134:135], v[136:137] op_sel_hi:[1,0]
	s_nop 0
	v_pk_fma_f32 v[134:135], v[136:137], v[144:145], v[134:135] op_sel:[1,1,0] op_sel_hi:[1,0,1]
	v_pk_mul_f32 v[136:137], v[162:163], v[154:155] op_sel_hi:[1,0]
	s_nop 0
	v_pk_fma_f32 v[136:137], v[154:155], v[142:143], v[136:137] op_sel:[1,1,0] op_sel_hi:[1,0,1]
	s_nop 0
	v_pk_mul_f32 v[144:145], v[136:137], s[28:29]
	v_pk_mul_f32 v[136:137], v[136:137], v[138:139] op_sel_hi:[1,0]
	s_nop 0
	v_pk_fma_f32 v[136:137], v[138:139], v[144:145], v[136:137] op_sel:[1,1,0] op_sel_hi:[1,0,1]
	v_pk_mul_f32 v[138:139], v[162:163], v[158:159] op_sel_hi:[1,0]
	s_nop 0
	v_pk_fma_f32 v[138:139], v[158:159], v[142:143], v[138:139] op_sel:[1,1,0] op_sel_hi:[1,0,1]
	s_nop 0
	v_pk_mul_f32 v[142:143], v[138:139], s[28:29]
	s_waitcnt lgkmcnt(0)
	v_pk_mul_f32 v[138:139], v[138:139], v[140:141] op_sel_hi:[1,0]
	s_nop 0
	v_pk_fma_f32 v[138:139], v[140:141], v[142:143], v[138:139] op_sel:[1,1,0] op_sel_hi:[1,0,1]
	v_pk_add_f32 v[140:141], v[70:71], v[126:127]
	v_pk_add_f32 v[70:71], v[70:71], v[126:127] neg_lo:[0,1] neg_hi:[0,1]
	v_pk_add_f32 v[126:127], v[118:119], v[132:133]
	v_pk_add_f32 v[118:119], v[118:119], v[132:133] neg_lo:[0,1] neg_hi:[0,1]
	v_pk_add_f32 v[132:133], v[140:141], v[126:127]
	v_pk_add_f32 v[126:127], v[140:141], v[126:127] neg_lo:[0,1] neg_hi:[0,1]
	v_pk_fma_f32 v[140:141], v[118:119], s[26:27], v[70:71] op_sel:[1,0,0] op_sel_hi:[0,1,1]
	v_pk_fma_f32 v[70:71], v[118:119], s[28:29], v[70:71] op_sel:[1,0,0] op_sel_hi:[0,1,1]
	v_pk_add_f32 v[118:119], v[66:67], v[80:81]
	v_pk_add_f32 v[66:67], v[66:67], v[80:81] neg_lo:[0,1] neg_hi:[0,1]
	v_pk_add_f32 v[80:81], v[120:121], v[134:135]
	v_pk_add_f32 v[120:121], v[120:121], v[134:135] neg_lo:[0,1] neg_hi:[0,1]
	v_pk_add_f32 v[134:135], v[118:119], v[80:81]
	v_pk_add_f32 v[80:81], v[118:119], v[80:81] neg_lo:[0,1] neg_hi:[0,1]
	v_pk_fma_f32 v[118:119], v[120:121], s[26:27], v[66:67] op_sel:[1,0,0] op_sel_hi:[0,1,1]
	v_pk_fma_f32 v[66:67], v[120:121], s[28:29], v[66:67] op_sel:[1,0,0] op_sel_hi:[0,1,1]
	v_pk_add_f32 v[120:121], v[68:69], v[128:129]
	v_pk_add_f32 v[68:69], v[68:69], v[128:129] neg_lo:[0,1] neg_hi:[0,1]
	v_pk_add_f32 v[128:129], v[122:123], v[136:137]
	v_pk_add_f32 v[122:123], v[122:123], v[136:137] neg_lo:[0,1] neg_hi:[0,1]
	v_pk_add_f32 v[136:137], v[120:121], v[128:129]
	v_pk_add_f32 v[120:121], v[120:121], v[128:129] neg_lo:[0,1] neg_hi:[0,1]
	v_pk_fma_f32 v[128:129], v[122:123], s[26:27], v[68:69] op_sel:[1,0,0] op_sel_hi:[0,1,1]
	v_pk_fma_f32 v[68:69], v[122:123], s[28:29], v[68:69] op_sel:[1,0,0] op_sel_hi:[0,1,1]
	v_pk_add_f32 v[122:123], v[116:117], v[130:131]
	v_pk_add_f32 v[116:117], v[116:117], v[130:131] neg_lo:[0,1] neg_hi:[0,1]
	v_pk_add_f32 v[130:131], v[124:125], v[138:139]
	v_pk_add_f32 v[124:125], v[124:125], v[138:139] neg_lo:[0,1] neg_hi:[0,1]
	v_pk_add_f32 v[138:139], v[122:123], v[130:131]
	v_pk_add_f32 v[122:123], v[122:123], v[130:131] neg_lo:[0,1] neg_hi:[0,1]
	v_pk_fma_f32 v[130:131], v[124:125], s[26:27], v[116:117] op_sel:[1,0,0] op_sel_hi:[0,1,1]
	v_pk_fma_f32 v[116:117], v[124:125], s[28:29], v[116:117] op_sel:[1,0,0] op_sel_hi:[0,1,1]
	v_pk_mul_f32 v[124:125], v[118:119], s[34:35] op_sel_hi:[0,1]
	v_mul_f32_e32 v86, 0x3f3504f3, v128
	v_pk_fma_f32 v[118:119], v[118:119], s[30:31], v[124:125] op_sel:[1,0,0]
	v_pk_fma_f32 v[124:125], v[128:129], s[36:37], v[86:87] op_sel:[1,0,0] op_sel_hi:[1,1,0]
	v_pk_mul_f32 v[128:129], v[130:131], s[6:7] op_sel_hi:[0,1]
	v_pk_fma_f32 v[128:129], v[130:131], s[38:39], v[128:129] op_sel:[1,0,0]
	v_pk_mul_f32 v[130:131], v[120:121], s[18:19] op_sel_hi:[0,1]
	v_pk_fma_f32 v[120:121], v[120:121], s[8:9], v[130:131] op_sel:[1,0,0]
	v_pk_mul_f32 v[130:131], v[122:123], s[36:37] op_sel_hi:[0,1]
	v_pk_fma_f32 v[122:123], v[122:123], s[36:37], v[130:131] op_sel:[1,0,0] op_sel_hi:[1,0,1]
	v_pk_mul_f32 v[130:131], v[66:67], s[6:7] op_sel_hi:[0,1]
	v_pk_fma_f32 v[66:67], v[66:67], s[38:39], v[130:131] op_sel:[1,0,0]
	v_pk_mul_f32 v[130:131], v[68:69], s[36:37] op_sel_hi:[0,1]
	s_mov_b32 s39, s30
	v_pk_fma_f32 v[68:69], v[68:69], s[36:37], v[130:131] op_sel:[1,0,0] op_sel_hi:[1,0,1]
	v_pk_mul_f32 v[130:131], v[116:117], s[38:39] op_sel_hi:[0,1]
	s_mov_b32 s7, s38
	s_add_i32 s19, s62, -1
	v_pk_fma_f32 v[116:117], v[116:117], s[6:7], v[130:131] op_sel:[1,0,0]
	s_min_i32 s6, s19, s59
	s_mul_i32 s6, s6, s3
	s_add_i32 s6, s6, s2
	s_mul_hi_i32 s7, s6, 0x2aaaaaab
	s_lshr_b32 s8, s7, 31
	s_lshr_b32 s7, s7, 7
	s_add_i32 s7, s7, s8
	v_mul_f32_e32 v86, 0x3f3504f3, v80
	v_pk_add_f32 v[130:131], v[132:133], v[136:137]
	v_pk_add_f32 v[132:133], v[132:133], v[136:137] neg_lo:[0,1] neg_hi:[0,1]
	v_pk_add_f32 v[136:137], v[134:135], v[138:139]
	v_pk_add_f32 v[134:135], v[134:135], v[138:139] neg_lo:[0,1] neg_hi:[0,1]
	s_mulk_i32 s7, 0x300
	v_pk_fma_f32 v[80:81], v[80:81], s[36:37], v[86:87] op_sel:[1,0,0] op_sel_hi:[1,1,0]
	v_pk_add_f32 v[138:139], v[130:131], v[136:137]
	v_pk_add_f32 v[130:131], v[130:131], v[136:137] neg_lo:[0,1] neg_hi:[0,1]
	v_pk_fma_f32 v[136:137], v[134:135], s[26:27], v[132:133] op_sel:[1,0,0] op_sel_hi:[0,1,1]
	v_pk_fma_f32 v[132:133], v[134:135], s[28:29], v[132:133] op_sel:[1,0,0] op_sel_hi:[0,1,1]
	v_pk_add_f32 v[134:135], v[140:141], v[124:125]
	v_pk_add_f32 v[124:125], v[140:141], v[124:125] neg_lo:[0,1] neg_hi:[0,1]
	v_pk_add_f32 v[140:141], v[118:119], v[128:129]
	v_pk_add_f32 v[118:119], v[118:119], v[128:129] neg_lo:[0,1] neg_hi:[0,1]
	s_sub_i32 s6, s6, s7
	v_pk_add_f32 v[128:129], v[134:135], v[140:141]
	v_pk_add_f32 v[134:135], v[134:135], v[140:141] neg_lo:[0,1] neg_hi:[0,1]
	v_pk_fma_f32 v[140:141], v[118:119], s[26:27], v[124:125] op_sel:[1,0,0] op_sel_hi:[0,1,1]
	v_pk_fma_f32 v[118:119], v[118:119], s[28:29], v[124:125] op_sel:[1,0,0] op_sel_hi:[0,1,1]
	v_pk_add_f32 v[124:125], v[126:127], v[120:121]
	v_pk_add_f32 v[120:121], v[126:127], v[120:121] neg_lo:[0,1] neg_hi:[0,1]
	v_pk_add_f32 v[126:127], v[80:81], v[122:123]
	v_pk_add_f32 v[80:81], v[80:81], v[122:123] neg_lo:[0,1] neg_hi:[0,1]
	s_cmpk_lt_i32 s6, 0x200
	v_pk_add_f32 v[122:123], v[124:125], v[126:127]
	v_pk_add_f32 v[124:125], v[124:125], v[126:127] neg_lo:[0,1] neg_hi:[0,1]
	v_pk_fma_f32 v[126:127], v[80:81], s[26:27], v[120:121] op_sel:[1,0,0] op_sel_hi:[0,1,1]
	v_pk_fma_f32 v[80:81], v[80:81], s[28:29], v[120:121] op_sel:[1,0,0] op_sel_hi:[0,1,1]
	v_pk_add_f32 v[120:121], v[70:71], v[68:69]
	v_pk_add_f32 v[68:69], v[70:71], v[68:69] neg_lo:[0,1] neg_hi:[0,1]
	v_pk_add_f32 v[70:71], v[66:67], v[116:117]
	v_pk_add_f32 v[66:67], v[66:67], v[116:117] neg_lo:[0,1] neg_hi:[0,1]
	s_cselect_b64 vcc, -1, 0
	v_pk_add_f32 v[116:117], v[120:121], v[70:71]
	v_pk_add_f32 v[70:71], v[120:121], v[70:71] neg_lo:[0,1] neg_hi:[0,1]
	v_pk_fma_f32 v[120:121], v[66:67], s[26:27], v[68:69] op_sel:[1,0,0] op_sel_hi:[0,1,1]
	v_pk_fma_f32 v[66:67], v[66:67], s[28:29], v[68:69] op_sel:[1,0,0] op_sel_hi:[0,1,1]
	ds_write_b64 v166, v[138:139]
	ds_write2_b64 v65, v[128:129], v[122:123] offset0:17 offset1:34
	ds_write2_b64 v65, v[116:117], v[136:137] offset0:51 offset1:68
	ds_write2_b64 v65, v[140:141], v[126:127] offset0:85 offset1:102
	ds_write2_b64 v65, v[120:121], v[130:131] offset0:119 offset1:136
	ds_write2_b64 v65, v[134:135], v[124:125] offset0:153 offset1:170
	ds_write2_b64 v65, v[70:71], v[132:133] offset0:187 offset1:204
	ds_write2_b64 v65, v[118:119], v[80:81] offset0:221 offset1:238
	ds_write_b64 v65, v[66:67] offset:2040
	v_cndmask_b32_e32 v65, v211, v212, vcc
	v_mul_f32_e32 v20, v65, v20
	v_mul_f32_e32 v66, v65, v16
	v_mov_b32_e32 v16, v87
	v_cvt_pk_fp8_f32 v16, v20, v66
	v_mul_f32_e32 v20, v65, v21
	v_mul_f32_e32 v21, v65, v17
	v_mov_b32_e32 v17, v87
	v_cvt_pk_fp8_f32 v17, v20, v21
	v_mul_f32_e32 v20, v65, v37
	v_mul_f32_e32 v21, v65, v33
	v_mul_f32_e32 v12, v65, v12
	v_cvt_pk_fp8_f32 v17, v20, v21 op_sel:[0,0,1]
	v_mul_f32_e32 v20, v65, v22
	v_mul_f32_e32 v21, v65, v18
	v_mov_b32_e32 v18, v87
	v_cvt_pk_fp8_f32 v18, v20, v21
	v_mul_f32_e32 v20, v65, v23
	v_mul_f32_e32 v21, v65, v19
	v_mov_b32_e32 v19, v87
	v_cvt_pk_fp8_f32 v19, v20, v21
	v_mul_f32_e32 v20, v65, v39
	v_mul_f32_e32 v21, v65, v35
	s_min_i32 s6, s76, s59
	v_cvt_pk_fp8_f32 v19, v20, v21 op_sel:[0,0,1]
	v_mul_f32_e32 v20, v65, v8
	v_mov_b32_e32 v8, v87
	v_cvt_pk_fp8_f32 v8, v12, v20
	v_mul_f32_e32 v12, v65, v13
	v_mul_f32_e32 v13, v65, v9
	v_mov_b32_e32 v9, v87
	v_cvt_pk_fp8_f32 v9, v12, v13
	v_mul_f32_e32 v12, v65, v29
	v_mul_f32_e32 v13, v65, v25
	s_mul_i32 s6, s6, s3
	v_cvt_pk_fp8_f32 v9, v12, v13 op_sel:[0,0,1]
	v_mul_f32_e32 v12, v65, v14
	v_mul_f32_e32 v13, v65, v10
	v_mov_b32_e32 v10, v87
	v_cvt_pk_fp8_f32 v10, v12, v13
	v_mul_f32_e32 v12, v65, v15
	v_mul_f32_e32 v13, v65, v11
	v_mov_b32_e32 v11, v87
	v_cvt_pk_fp8_f32 v11, v12, v13
	s_add_i32 s7, s6, s2
	v_mul_f32_e32 v36, v65, v36
	v_mul_f32_e32 v32, v65, v32
	s_mul_hi_i32 s6, s7, 0x2aaaaaab
	v_cvt_pk_fp8_f32 v16, v36, v32 op_sel:[0,0,1]
	v_mul_f32_e32 v22, v65, v38
	v_mul_f32_e32 v32, v65, v34
	s_lshr_b32 s8, s6, 31
	s_ashr_i32 s6, s6, 7
	v_cvt_pk_fp8_f32 v18, v22, v32 op_sel:[0,0,1]
	v_mul_f32_e32 v21, v65, v28
	v_mul_f32_e32 v22, v65, v24
	v_mul_f32_e32 v14, v65, v30
	v_mul_f32_e32 v20, v65, v26
	v_mul_f32_e32 v12, v65, v31
	v_mul_f32_e32 v13, v65, v27
	s_add_i32 s8, s6, s8
	v_cvt_pk_fp8_f32 v8, v21, v22 op_sel:[0,0,1]
	v_cvt_pk_fp8_f32 v10, v14, v20 op_sel:[0,0,1]
	v_cvt_pk_fp8_f32 v11, v12, v13 op_sel:[0,0,1]
	s_add_i32 s6, s8, 11
	s_mulk_i32 s8, 0x300
	s_sub_i32 s31, s7, s8
	s_cmpk_lt_i32 s31, 0x200
	s_cselect_b64 s[8:9], -1, 0
	s_cmpk_gt_i32 s31, 0x1ff
	s_waitcnt lgkmcnt(0)
	s_barrier
	ds_write_b128 v240, v[16:19]
	ds_write_b128 v241, v[8:11]
	s_cbranch_scc0 .LBB0_815
	s_load_dwordx2 s[12:13], s[14:15], 0x110
	s_ashr_i32 s7, s6, 31
	s_lshl_b64 s[52:53], s[6:7], 24
	s_mov_b32 s51, s18
	s_waitcnt lgkmcnt(0)
	s_add_u32 s12, s12, s52
	s_addc_u32 s13, s13, s53
	s_lshl_b32 s7, s31, 3
	s_and_b32 s7, s7, 0x7fffffc0
	s_add_i32 s50, s7, 0xfffff000
	s_mov_b64 s[52:53], 0

.LBB0_817:
	s_lshl_b64 s[50:51], s[50:51], 13
	s_add_u32 s6, s12, s50
	s_addc_u32 s12, s13, s51
	s_lshl_b32 s7, s31, s7
	s_and_b32 s7, s7, 0x700
	s_lshl_b32 s7, s7, 2
	s_add_u32 s6, s6, s7
	s_addc_u32 s7, s12, 0
	s_cmp_ge_i32 s62, s59
	s_cselect_b64 s[54:55], -1, 0
	v_cndmask_b32_e64 v8, v180, 0, s[54:55]
	s_and_b64 s[12:13], s[54:55], exec
	s_cselect_b32 s12, 0, 0x800
	v_lshlrev_b32_e32 v86, 2, v8
	v_lshl_add_u64 v[8:9], s[6:7], 0, v[86:87]
	v_mad_i64_i32 v[10:11], s[6:7], s12, v181, 0
	v_mad_i64_i32 v[12:13], s[6:7], s12, v182, 0
	v_lshl_add_u64 v[10:11], v[10:11], 2, v[8:9]
	v_lshl_add_u64 v[12:13], v[12:13], 2, v[8:9]
	global_load_dwordx4 v[32:35], v[10:11], off nt
	global_load_dwordx4 v[36:39], v[12:13], off nt
	v_mad_i64_i32 v[10:11], s[6:7], s12, v183, 0
	v_mad_i64_i32 v[12:13], s[6:7], s12, v184, 0
	v_lshl_add_u64 v[10:11], v[10:11], 2, v[8:9]
	v_lshl_add_u64 v[12:13], v[12:13], 2, v[8:9]
	global_load_dwordx4 v[24:27], v[10:11], off nt
	global_load_dwordx4 v[28:31], v[12:13], off nt
	v_mad_i64_i32 v[10:11], s[6:7], s12, v185, 0
	v_mad_i64_i32 v[12:13], s[6:7], s12, v186, 0
	v_lshl_add_u64 v[10:11], v[10:11], 2, v[8:9]
	v_lshl_add_u64 v[12:13], v[12:13], 2, v[8:9]
	global_load_dwordx4 v[16:19], v[10:11], off nt
	global_load_dwordx4 v[20:23], v[12:13], off nt
	v_mad_i64_i32 v[10:11], s[6:7], s12, v187, 0
	v_mad_i64_i32 v[12:13], s[6:7], s12, v188, 0
	v_lshl_add_u64 v[10:11], v[10:11], 2, v[8:9]
	v_lshl_add_u64 v[12:13], v[12:13], 2, v[8:9]
	global_load_dwordx4 v[8:11], v[10:11], off nt
	s_nop 0
	global_load_dwordx4 v[12:15], v[12:13], off nt
	s_cmp_gt_i32 s62, 1
	s_cselect_b32 s6, s56, 0
	s_min_i32 s6, s6, s59
	s_mul_i32 s6, s6, s3
	s_add_i32 s7, s6, s2
	s_mul_hi_i32 s6, s7, 0x2aaaaaab
	s_lshr_b32 s12, s6, 31
	s_ashr_i32 s6, s6, 7
	s_add_i32 s12, s6, s12
	s_add_i32 s6, s12, 11
	s_mulk_i32 s12, 0x300
	s_sub_i32 s31, s7, s12
	s_ashr_i32 s7, s6, 31
	s_cmpk_gt_i32 s31, 0x1ff
	s_mov_b64 s[50:51], -1
	s_cbranch_scc0 .LBB0_819
	s_lshl_b32 s12, s31, 3
	s_and_b32 s33, s12, 0x7fffffc0
	s_lshl_b32 s12, s31, 19
	s_and_b32 s39, s12, 0x380000
	s_lshl_b64 s[12:13], s[6:7], 22
	s_add_u32 s12, s16, s12
	s_addc_u32 s13, s17, s13
	s_add_u32 s12, s12, s39
	s_addc_u32 s13, s13, 0
	s_add_u32 s12, s12, s33
	s_addc_u32 s13, s13, 0
	s_add_u32 s12, s12, 0x24dff000
	s_addc_u32 s13, s13, 0
	s_mov_b64 s[50:51], 0

.LBB0_821:
	s_add_i32 s33, s62, 2
	s_cmp_lt_i32 s62, 2
	s_cselect_b64 s[6:7], -1, 0
	s_cmp_gt_i32 s56, s59
	s_cselect_b64 s[50:51], -1, 0
	s_or_b64 s[6:7], s[6:7], s[50:51]
	s_and_b64 s[6:7], s[6:7], exec
	s_cselect_b32 s6, s65, s12
	s_cselect_b32 s12, 0x80, s39
	v_mul_i32_i24_e32 v65, s12, v191
	v_or_b32_e32 v66, v65, v189
	v_ashrrev_i32_e32 v67, 31, v66
	s_cselect_b32 s7, s66, s13
	v_lshlrev_b64 v[66:67], 11, v[66:67]
	v_add_u32_e32 v239, v203, v190
	v_lshl_add_u64 v[66:67], s[6:7], 0, v[66:67]
	v_lshl_add_u64 v[70:71], v[66:67], 0, v[88:89]
	v_add_u32_e32 v242, v203, v200
	ds_read_b32 v66, v239
	ds_read_b32 v67, v239 offset:1040
	ds_read_b32 v68, v239 offset:2080
	ds_read_b32 v69, v239 offset:3120
	ds_read_b32 v116, v242
	ds_read_b32 v117, v242 offset:1040
	ds_read_b32 v118, v242 offset:2080
	ds_read_b32 v119, v242 offset:3120
	v_mul_i32_i24_e32 v65, s12, v201
	s_waitcnt lgkmcnt(4)
	global_store_dwordx4 v[70:71], v[66:69], off nt
	v_lshlrev_b32_e32 v64, 3, v64
	v_add3_u32 v64, v219, v64, v83
	v_or_b32_e32 v66, v65, v189
	v_ashrrev_i32_e32 v67, 31, v66
	v_lshlrev_b64 v[66:67], 11, v[66:67]
	v_lshl_add_u64 v[66:67], s[6:7], 0, v[66:67]
	v_lshl_add_u64 v[66:67], v[66:67], 0, v[88:89]
	s_waitcnt lgkmcnt(0)
	global_store_dwordx4 v[66:67], v[116:119], off nt
	v_add_u32_e32 v65, 0x100, v82
	v_add_u32_e32 v66, 0x200, v82
	v_add_u32_e32 v67, 0x300, v82
	v_ashrrev_i32_e32 v65, 4, v65
	v_ashrrev_i32_e32 v66, 4, v66
	v_ashrrev_i32_e32 v67, 4, v67
	v_lshlrev_b32_e32 v65, 3, v65
	v_lshlrev_b32_e32 v66, 3, v66
	v_lshlrev_b32_e32 v67, 3, v67
	v_add3_u32 v65, v219, v65, v83
	v_add3_u32 v66, v219, v66, v83
	v_add3_u32 v67, v219, v67, v83
	ds_read_b64 v[116:117], v64
	ds_read_b64 v[130:131], v65 offset:2048
	ds_read_b64 v[122:123], v66 offset:4096
	ds_read_b64 v[132:133], v67 offset:6144
	v_add_u32_e32 v64, 0x400, v82
	v_ashrrev_i32_e32 v64, 4, v64
	v_add_u32_e32 v65, 0x500, v82
	v_add_u32_e32 v66, 0x600, v82
	v_add_u32_e32 v67, 0x700, v82
	v_lshlrev_b32_e32 v64, 3, v64
	v_ashrrev_i32_e32 v65, 4, v65
	v_ashrrev_i32_e32 v66, 4, v66
	v_ashrrev_i32_e32 v67, 4, v67
	v_add3_u32 v64, v219, v64, v83
	v_lshlrev_b32_e32 v65, 3, v65
	v_lshlrev_b32_e32 v66, 3, v66
	v_lshlrev_b32_e32 v67, 3, v67
	v_add3_u32 v65, v219, v65, v83
	v_add3_u32 v66, v219, v66, v83
	v_add3_u32 v67, v219, v67, v83
	ds_read_b64 v[118:119], v64 offset:8192
	ds_read_b64 v[138:139], v65 offset:10240
	ds_read_b64 v[126:127], v66 offset:12288
	ds_read_b64 v[136:137], v67 offset:14336
	v_add_u32_e32 v64, 0x800, v82
	v_ashrrev_i32_e32 v64, 4, v64
	v_add_u32_e32 v65, 0x900, v82
	v_add_u32_e32 v66, 0xa00, v82
	v_add_u32_e32 v67, 0xb00, v82
	v_lshlrev_b32_e32 v64, 3, v64
	v_ashrrev_i32_e32 v65, 4, v65
	v_ashrrev_i32_e32 v66, 4, v66
	v_ashrrev_i32_e32 v67, 4, v67
	v_add3_u32 v64, v219, v64, v83
	v_lshlrev_b32_e32 v65, 3, v65
	v_lshlrev_b32_e32 v66, 3, v66
	v_lshlrev_b32_e32 v67, 3, v67
	v_add3_u32 v65, v219, v65, v83
	v_add3_u32 v66, v219, v66, v83
	v_add3_u32 v67, v219, v67, v83
	ds_read_b64 v[120:121], v64 offset:16384
	ds_read_b64 v[142:143], v65 offset:18432
	ds_read_b64 v[128:129], v66 offset:20480
	ds_read_b64 v[140:141], v67 offset:22528
	v_add_u32_e32 v64, 0xc00, v82
	v_ashrrev_i32_e32 v64, 4, v64
	v_add_u32_e32 v65, 0xd00, v82
	v_add_u32_e32 v66, 0xe00, v82
	v_add_u32_e32 v67, 0xf00, v82
	v_lshlrev_b32_e32 v64, 3, v64
	v_ashrrev_i32_e32 v65, 4, v65
	v_ashrrev_i32_e32 v66, 4, v66
	v_ashrrev_i32_e32 v67, 4, v67
	v_add3_u32 v64, v219, v64, v83
	v_lshlrev_b32_e32 v65, 3, v65
	v_lshlrev_b32_e32 v66, 3, v66
	v_lshlrev_b32_e32 v67, 3, v67
	v_add3_u32 v65, v219, v65, v83
	v_add3_u32 v66, v219, v66, v83
	v_add3_u32 v67, v219, v67, v83
	ds_read_b64 v[124:125], v64 offset:24576
	ds_read_b64 v[146:147], v65 offset:26624
	ds_read_b64 v[134:135], v66 offset:28672
	ds_read_b64 v[144:145], v67 offset:30720
	v_cndmask_b32_e64 v64, v211, v212, s[4:5]
	s_waitcnt vmcnt(19)
	v_mul_f32_e32 v65, v64, v48
	s_waitcnt vmcnt(18)
	v_mul_f32_e32 v52, v64, v52
	v_mov_b32_e32 v48, v87
	v_cvt_pk_fp8_f32 v48, v65, v52
	v_mul_f32_e32 v52, v64, v49
	v_mul_f32_e32 v53, v64, v53
	v_mov_b32_e32 v49, v87
	v_cvt_pk_fp8_f32 v49, v52, v53
	s_waitcnt vmcnt(17)
	v_mul_f32_e32 v52, v64, v57
	s_waitcnt vmcnt(16)
	v_mul_f32_e32 v53, v64, v61
	s_waitcnt vmcnt(14)
	v_mul_f32_e32 v4, v64, v4
	v_cvt_pk_fp8_f32 v49, v52, v53 op_sel:[0,0,1]
	v_mul_f32_e32 v52, v64, v50
	v_mul_f32_e32 v53, v64, v54
	v_mov_b32_e32 v50, v87
	v_cvt_pk_fp8_f32 v50, v52, v53
	v_mul_f32_e32 v52, v64, v51
	v_mul_f32_e32 v53, v64, v55
	v_mov_b32_e32 v51, v87
	v_cvt_pk_fp8_f32 v51, v52, v53
	v_mul_f32_e32 v52, v64, v59
	v_mul_f32_e32 v53, v64, v63
	v_mul_f32_e32 v5, v64, v5
	v_cvt_pk_fp8_f32 v51, v52, v53 op_sel:[0,0,1]
	v_mul_f32_e32 v52, v64, v0
	v_mov_b32_e32 v0, v87
	v_cvt_pk_fp8_f32 v0, v52, v4
	v_mul_f32_e32 v4, v64, v1
	v_mov_b32_e32 v1, v87
	v_cvt_pk_fp8_f32 v1, v4, v5
	s_waitcnt vmcnt(13)
	v_mul_f32_e32 v4, v64, v41
	s_waitcnt vmcnt(12)
	v_mul_f32_e32 v5, v64, v45
	s_min_i32 s4, s33, s59
	v_cvt_pk_fp8_f32 v1, v4, v5 op_sel:[0,0,1]
	v_mul_f32_e32 v4, v64, v2
	v_mul_f32_e32 v5, v64, v6
	v_mov_b32_e32 v2, v87
	s_mul_i32 s4, s4, s3
	v_cvt_pk_fp8_f32 v2, v4, v5
	v_mul_f32_e32 v4, v64, v3
	v_mul_f32_e32 v5, v64, v7
	v_mov_b32_e32 v3, v87
	s_add_i32 s5, s4, s2
	v_cvt_pk_fp8_f32 v3, v4, v5
	s_mul_hi_i32 s4, s5, 0x2aaaaaab
	v_mul_f32_e32 v56, v64, v56
	v_mul_f32_e32 v60, v64, v60
	s_lshr_b32 s6, s4, 31
	s_ashr_i32 s4, s4, 7
	v_cvt_pk_fp8_f32 v48, v56, v60 op_sel:[0,0,1]
	v_mul_f32_e32 v54, v64, v58
	v_mul_f32_e32 v56, v64, v62
	v_mul_f32_e32 v40, v64, v40
	v_mul_f32_e32 v44, v64, v44
	s_add_i32 s6, s4, s6
	v_cvt_pk_fp8_f32 v50, v54, v56 op_sel:[0,0,1]
	v_cvt_pk_fp8_f32 v0, v40, v44 op_sel:[0,0,1]
	v_mul_f32_e32 v6, v64, v42
	v_mul_f32_e32 v40, v64, v46
	v_mul_f32_e32 v4, v64, v43
	v_mul_f32_e32 v5, v64, v47
	s_add_i32 s4, s6, 11
	s_mulk_i32 s6, 0x300
	v_cvt_pk_fp8_f32 v2, v6, v40 op_sel:[0,0,1]
	v_cvt_pk_fp8_f32 v3, v4, v5 op_sel:[0,0,1]
	s_sub_i32 s31, s5, s6
	s_cmpk_lt_i32 s31, 0x200
	s_cselect_b64 s[6:7], -1, 0
	s_cmpk_gt_i32 s31, 0x1ff
	s_mov_b64 s[52:53], -1
	s_waitcnt lgkmcnt(0)
	s_barrier
	ds_write_b128 v236, v[48:51]
	ds_write_b128 v237, v[0:3]
	s_cbranch_scc0 .LBB0_823
	s_load_dwordx2 s[12:13], s[14:15], 0x110
	s_ashr_i32 s5, s4, 31
	s_lshl_b64 s[52:53], s[4:5], 24
	s_mov_b32 s51, s18
	s_waitcnt lgkmcnt(0)
	s_add_u32 s12, s12, s52
	s_addc_u32 s13, s13, s53
	s_lshl_b32 s5, s31, 3
	s_and_b32 s5, s5, 0x7fffffc0
	s_add_i32 s50, s5, 0xfffff000
	s_mov_b64 s[52:53], 0

.LBB0_825:
	s_lshl_b64 s[50:51], s[50:51], 13
	s_add_u32 s4, s12, s50
	s_addc_u32 s12, s13, s51
	s_lshl_b32 s5, s31, s5
	s_and_b32 s5, s5, 0x700
	s_lshl_b32 s5, s5, 2
	s_add_u32 s4, s4, s5
	s_addc_u32 s5, s12, 0
	s_add_i32 s56, s56, 4
	s_cmp_gt_i32 s56, s59
	s_cselect_b64 s[50:51], -1, 0
	v_cndmask_b32_e64 v0, v180, 0, s[50:51]
	s_and_b64 s[12:13], s[50:51], exec
	s_cselect_b32 s12, 0, 0x800
	v_lshlrev_b32_e32 v86, 2, v0
	v_lshl_add_u64 v[0:1], s[4:5], 0, v[86:87]
	v_mad_i64_i32 v[2:3], s[4:5], s12, v181, 0
	v_lshl_add_u64 v[2:3], v[2:3], 2, v[0:1]
	v_mad_i64_i32 v[4:5], s[4:5], s12, v182, 0
	v_lshl_add_u64 v[4:5], v[4:5], 2, v[0:1]
	global_load_dwordx4 v[56:59], v[2:3], off nt
	global_load_dwordx4 v[60:63], v[4:5], off nt
	v_mad_i64_i32 v[2:3], s[4:5], s12, v183, 0
	v_lshl_add_u64 v[2:3], v[2:3], 2, v[0:1]
	v_mad_i64_i32 v[4:5], s[4:5], s12, v184, 0
	v_lshl_add_u64 v[4:5], v[4:5], 2, v[0:1]
	global_load_dwordx4 v[64:67], v[2:3], off nt
	global_load_dwordx4 v[68:71], v[4:5], off nt
	v_mad_i64_i32 v[2:3], s[4:5], s12, v185, 0
	v_lshl_add_u64 v[2:3], v[2:3], 2, v[0:1]
	v_mad_i64_i32 v[4:5], s[4:5], s12, v186, 0
	v_lshl_add_u64 v[4:5], v[4:5], 2, v[0:1]
	global_load_dwordx4 v[40:43], v[2:3], off nt
	global_load_dwordx4 v[44:47], v[4:5], off nt
	v_mad_i64_i32 v[2:3], s[4:5], s12, v187, 0
	v_lshl_add_u64 v[2:3], v[2:3], 2, v[0:1]
	v_mad_i64_i32 v[4:5], s[4:5], s12, v188, 0
	v_lshl_add_u64 v[0:1], v[4:5], 2, v[0:1]
	global_load_dwordx4 v[48:51], v[2:3], off nt
	global_load_dwordx4 v[52:55], v[0:1], off nt
	s_cmp_gt_i32 s62, 0
	s_cselect_b32 s4, s19, 0
	s_min_i32 s4, s4, s59
	s_mul_i32 s4, s4, s3
	s_add_i32 s5, s4, s2
	s_mul_hi_i32 s4, s5, 0x2aaaaaab
	s_lshr_b32 s12, s4, 31
	s_ashr_i32 s4, s4, 7
	s_add_i32 s12, s4, s12
	s_add_i32 s4, s12, 11
	s_mulk_i32 s12, 0x300
	s_sub_i32 s31, s5, s12
	s_ashr_i32 s5, s4, 31
	s_cmpk_gt_i32 s31, 0x1ff
	s_mov_b64 s[52:53], -1
	s_cbranch_scc0 .LBB0_827
	s_lshl_b32 s12, s31, 3
	s_and_b32 s39, s12, 0x7fffffc0
	s_lshl_b32 s12, s31, 19
	s_and_b32 s52, s12, 0x380000
	s_lshl_b64 s[12:13], s[4:5], 22
	s_add_u32 s12, s16, s12
	s_addc_u32 s13, s17, s13
	s_add_u32 s12, s12, s52
	s_addc_u32 s13, s13, 0
	s_add_u32 s12, s12, s39
	s_addc_u32 s13, s13, 0
	s_add_u32 s12, s12, 0x24dff000
	s_addc_u32 s13, s13, 0
	s_mov_b64 s[52:53], 0

.LBB0_829:
	s_add_i32 s77, s62, 3
	s_cmp_lt_i32 s62, 1
	s_cselect_b64 s[4:5], -1, 0
	s_cmp_gt_i32 s19, s59
	s_cselect_b64 s[52:53], -1, 0
	s_or_b64 s[4:5], s[4:5], s[52:53]
	s_and_b64 s[4:5], s[4:5], exec
	s_cselect_b32 s4, s65, s12
	s_cselect_b32 s12, 0x80, s39
	v_mul_i32_i24_e32 v0, s12, v191
	v_or_b32_e32 v0, v0, v189
	v_ashrrev_i32_e32 v1, 31, v0
	s_cselect_b32 s5, s66, s13
	v_lshlrev_b64 v[0:1], 11, v[0:1]
	v_lshl_add_u64 v[0:1], s[4:5], 0, v[0:1]
	v_lshl_add_u64 v[80:81], v[0:1], 0, v[88:89]
	ds_read_b32 v0, v235
	ds_read_b32 v1, v235 offset:1040
	ds_read_b32 v2, v235 offset:2080
	ds_read_b32 v3, v235 offset:3120
	ds_read_b32 v4, v238
	ds_read_b32 v5, v238 offset:1040
	ds_read_b32 v6, v238 offset:2080
	ds_read_b32 v7, v238 offset:3120
	s_waitcnt lgkmcnt(4)
	global_store_dwordx4 v[80:81], v[0:3], off nt
	s_mov_b64 s[56:57], -1
	s_nop 0
	v_mul_i32_i24_e32 v0, s12, v201
	v_or_b32_e32 v0, v0, v189
	v_ashrrev_i32_e32 v1, 31, v0
	v_lshlrev_b64 v[0:1], 11, v[0:1]
	v_lshl_add_u64 v[0:1], s[4:5], 0, v[0:1]
	v_lshl_add_u64 v[0:1], v[0:1], 0, v[88:89]
	s_mov_b32 s4, 0x45700000
	s_waitcnt lgkmcnt(0)
	global_store_dwordx4 v[0:1], v[4:7], off nt
	v_add_co_u32_e32 v0, vcc, s4, v84
	s_mov_b32 s4, 0x46300000
	s_nop 0
	v_addc_co_u32_e32 v1, vcc, 0, v85, vcc
	v_add_co_u32_e32 v4, vcc, s4, v84
	s_min_i32 s4, s77, s59
	s_nop 0
	v_addc_co_u32_e32 v5, vcc, 0, v85, vcc
	global_load_dwordx4 v[0:3], v[0:1], off
	s_nop 0
	global_load_dwordx4 v[4:7], v[4:5], off
	ds_write_b128 v234, v[72:75]
	ds_write_b128 v234, v[76:79] offset:4096
	v_cndmask_b32_e64 v72, v211, v212, s[8:9]
	s_waitcnt vmcnt(21)
	v_mul_f32_e32 v73, v72, v32
	s_waitcnt vmcnt(20)
	v_mul_f32_e32 v36, v72, v36
	v_mov_b32_e32 v32, v87
	v_cvt_pk_fp8_f32 v32, v73, v36
	v_mul_f32_e32 v36, v72, v33
	v_mul_f32_e32 v37, v72, v37
	v_mov_b32_e32 v33, v87
	v_cvt_pk_fp8_f32 v33, v36, v37
	s_waitcnt vmcnt(19)
	v_mul_f32_e32 v24, v72, v24
	s_waitcnt vmcnt(18)
	v_mul_f32_e32 v28, v72, v28
	v_cvt_pk_fp8_f32 v32, v24, v28 op_sel:[0,0,1]
	v_mul_f32_e32 v24, v72, v25
	v_mul_f32_e32 v25, v72, v29
	v_cvt_pk_fp8_f32 v33, v24, v25 op_sel:[0,0,1]
	v_mul_f32_e32 v24, v72, v34
	v_mul_f32_e32 v25, v72, v38
	v_mov_b32_e32 v34, v87
	v_cvt_pk_fp8_f32 v34, v24, v25
	v_mul_f32_e32 v24, v72, v35
	v_mul_f32_e32 v25, v72, v39
	v_mov_b32_e32 v35, v87
	v_cvt_pk_fp8_f32 v35, v24, v25
	v_mul_f32_e32 v24, v72, v27
	v_mul_f32_e32 v25, v72, v31
	s_waitcnt vmcnt(16)
	v_mul_f32_e32 v20, v72, v20
	v_cvt_pk_fp8_f32 v35, v24, v25 op_sel:[0,0,1]
	v_mul_f32_e32 v24, v72, v16
	v_mov_b32_e32 v16, v87
	v_cvt_pk_fp8_f32 v16, v24, v20
	v_mul_f32_e32 v20, v72, v17
	v_mul_f32_e32 v21, v72, v21
	v_mov_b32_e32 v17, v87
	v_cvt_pk_fp8_f32 v17, v20, v21
	s_waitcnt vmcnt(15)
	v_mul_f32_e32 v8, v72, v8
	s_waitcnt vmcnt(14)
	v_mul_f32_e32 v12, v72, v12
	v_cvt_pk_fp8_f32 v16, v8, v12 op_sel:[0,0,1]
	v_mul_f32_e32 v8, v72, v9
	v_mul_f32_e32 v9, v72, v13
	v_cvt_pk_fp8_f32 v17, v8, v9 op_sel:[0,0,1]
	v_mul_f32_e32 v8, v72, v18
	v_mul_f32_e32 v9, v72, v22
	v_mov_b32_e32 v18, v87
	s_mul_i32 s4, s4, s3
	v_cvt_pk_fp8_f32 v18, v8, v9
	v_mul_f32_e32 v8, v72, v19
	v_mul_f32_e32 v9, v72, v23
	v_mov_b32_e32 v19, v87
	s_add_i32 s4, s4, s2
	v_cvt_pk_fp8_f32 v19, v8, v9
	s_mul_hi_i32 s5, s4, 0x2aaaaaab
	s_lshr_b32 s8, s5, 31
	s_ashr_i32 s5, s5, 7
	v_mul_f32_e32 v26, v72, v26
	v_mul_f32_e32 v28, v72, v30
	s_add_i32 s5, s5, s8
	v_cvt_pk_fp8_f32 v34, v26, v28 op_sel:[0,0,1]
	v_mul_f32_e32 v10, v72, v10
	v_mul_f32_e32 v12, v72, v14
	v_mul_f32_e32 v8, v72, v11
	v_mul_f32_e32 v9, v72, v15
	s_add_i32 s8, s5, 11
	s_mulk_i32 s5, 0x300
	v_cvt_pk_fp8_f32 v18, v10, v12 op_sel:[0,0,1]
	v_cvt_pk_fp8_f32 v19, v8, v9 op_sel:[0,0,1]
	s_sub_i32 s31, s4, s5
	s_cmpk_lt_i32 s31, 0x200
	s_cselect_b64 s[4:5], -1, 0
	s_cmpk_gt_i32 s31, 0x1ff
	s_waitcnt lgkmcnt(0)
	s_barrier
	ds_write_b128 v240, v[32:35]
	ds_write_b128 v241, v[16:19]
	s_cbranch_scc0 .LBB0_831
	s_load_dwordx2 s[12:13], s[14:15], 0x110
	s_ashr_i32 s9, s8, 31
	s_lshl_b64 s[56:57], s[8:9], 24
	s_mov_b32 s53, s18
	s_waitcnt lgkmcnt(0)
	s_add_u32 s12, s12, s56
	s_addc_u32 s13, s13, s57
	s_lshl_b32 s9, s31, 3
	s_and_b32 s9, s9, 0x7fffffc0
	s_add_i32 s52, s9, 0xfffff000
	s_mov_b64 s[56:57], 0

.LBB0_833:
	s_lshl_b64 s[52:53], s[52:53], 13
	s_add_u32 s8, s12, s52
	s_addc_u32 s12, s13, s53
	s_lshl_b32 s9, s31, s9
	s_and_b32 s9, s9, 0x700
	s_lshl_b32 s9, s9, 2
	s_add_u32 s8, s8, s9
	s_addc_u32 s9, s12, 0
	s_add_i32 s19, s19, 4
	s_cmp_gt_i32 s19, s59
	s_cselect_b64 s[52:53], -1, 0
	v_cndmask_b32_e64 v8, v180, 0, s[52:53]
	s_and_b64 s[12:13], s[52:53], exec
	s_cselect_b32 s12, 0, 0x800
	v_lshlrev_b32_e32 v86, 2, v8
	v_lshl_add_u64 v[16:17], s[8:9], 0, v[86:87]
	v_mad_i64_i32 v[8:9], s[8:9], s12, v181, 0
	v_mad_i64_i32 v[10:11], s[8:9], s12, v182, 0
	v_lshl_add_u64 v[8:9], v[8:9], 2, v[16:17]
	v_lshl_add_u64 v[10:11], v[10:11], 2, v[16:17]
	global_load_dwordx4 v[24:27], v[8:9], off nt
	global_load_dwordx4 v[28:31], v[10:11], off nt
	v_mad_i64_i32 v[8:9], s[8:9], s12, v183, 0
	v_mad_i64_i32 v[10:11], s[8:9], s12, v184, 0
	v_lshl_add_u64 v[8:9], v[8:9], 2, v[16:17]
	v_lshl_add_u64 v[10:11], v[10:11], 2, v[16:17]
	global_load_dwordx4 v[32:35], v[8:9], off nt
	global_load_dwordx4 v[36:39], v[10:11], off nt
	v_mad_i64_i32 v[8:9], s[8:9], s12, v185, 0
	v_mad_i64_i32 v[10:11], s[8:9], s12, v186, 0
	v_mad_i64_i32 v[18:19], s[8:9], s12, v187, 0
	v_mad_i64_i32 v[20:21], s[8:9], s12, v188, 0
	v_lshl_add_u64 v[8:9], v[8:9], 2, v[16:17]
	v_lshl_add_u64 v[12:13], v[10:11], 2, v[16:17]
	v_lshl_add_u64 v[18:19], v[18:19], 2, v[16:17]
	v_lshl_add_u64 v[20:21], v[20:21], 2, v[16:17]
	global_load_dwordx4 v[8:11], v[8:9], off nt
	s_nop 0
	global_load_dwordx4 v[12:15], v[12:13], off nt
	s_nop 0
	global_load_dwordx4 v[16:19], v[18:19], off nt
	s_nop 0
	global_load_dwordx4 v[20:23], v[20:21], off nt
	s_max_i32 s8, s62, 0
	s_min_i32 s8, s8, s59
	s_mul_i32 s8, s8, s3
	s_add_i32 s9, s8, s2
	s_mul_hi_i32 s8, s9, 0x2aaaaaab
	s_lshr_b32 s12, s8, 31
	s_ashr_i32 s8, s8, 7
	s_add_i32 s12, s8, s12
	s_add_i32 s8, s12, 11
	s_mulk_i32 s12, 0x300
	s_sub_i32 s19, s9, s12
	s_ashr_i32 s9, s8, 31
	s_cmpk_gt_i32 s19, 0x1ff
	s_mov_b64 s[56:57], -1
	s_cbranch_scc0 .LBB0_835
	s_lshl_b32 s12, s19, 3
	s_and_b32 s31, s12, 0x7fffffc0
	s_lshl_b32 s12, s19, 19
	s_and_b32 s39, s12, 0x380000
	s_lshl_b64 s[12:13], s[8:9], 22
	s_add_u32 s12, s16, s12
	s_addc_u32 s13, s17, s13
	s_add_u32 s12, s12, s39
	s_addc_u32 s13, s13, 0
	s_add_u32 s12, s12, s31
	s_addc_u32 s13, s13, 0
	s_add_u32 s12, s12, 0x24dff000
	s_addc_u32 s13, s13, 0
	s_mov_b64 s[56:57], 0

.LBB0_867:
	s_or_b64 exec, exec, s[0:1]
	v_pk_add_f32 v[72:73], v[146:147], v[170:171]
	v_pk_add_f32 v[74:75], v[168:169], v[172:173]
	v_pk_add_f32 v[76:77], v[132:133], v[136:137]
	v_pk_add_f32 v[72:73], v[72:73], v[74:75]
	v_pk_add_f32 v[74:75], v[130:131], v[134:135]
	v_pk_add_f32 v[78:79], v[138:139], v[142:143]
	v_pk_add_f32 v[74:75], v[74:75], v[76:77]
	v_pk_add_f32 v[76:77], v[144:145], v[140:141]
	v_pk_add_f32 v[82:83], v[122:123], v[126:127]
	v_pk_add_f32 v[76:77], v[76:77], v[78:79]
	v_lshlrev_b32_e32 v78, 2, v86
	v_and_b32_e32 v78, -8, v78
	v_lshlrev_b32_e32 v79, 3, v243
	v_add3_u32 v80, v219, v78, v79
	v_mov_b32_e32 v78, v156
	v_mov_b32_e32 v79, v148
	v_mov_b32_e32 v148, v157
	ds_write2_b64 v80, v[78:79], v[148:149] offset1:1
	v_mov_b32_e32 v78, v154
	v_mov_b32_e32 v79, v162
	v_mov_b32_e32 v162, v155
	ds_write2_b64 v80, v[78:79], v[162:163] offset0:2 offset1:3
	v_mov_b32_e32 v78, v158
	v_mov_b32_e32 v79, v164
	v_mov_b32_e32 v164, v159
	ds_write2_b64 v80, v[78:79], v[164:165] offset0:4 offset1:5
	v_mov_b32_e32 v78, v160
	v_mov_b32_e32 v79, v166
	v_mov_b32_e32 v166, v161
	ds_write2_b64 v80, v[78:79], v[166:167] offset0:6 offset1:7
	s_waitcnt lgkmcnt(0)
	s_barrier
	ds_read_b32 v78, v233 offset:120
	v_pk_add_f32 v[80:81], v[128:129], v[124:125]
	s_mov_b32 s56, s34
	v_pk_add_f32 v[80:81], v[80:81], v[82:83]
	ds_read_b64 v[82:83], v222
	ds_read_b64 v[124:125], v223 offset:2048
	ds_read_b64 v[126:127], v224 offset:4096
	ds_read_b64 v[128:129], v225 offset:6144
	ds_read_b64 v[130:131], v226 offset:8192
	ds_read_b64 v[132:133], v227 offset:10240
	ds_read_b64 v[134:135], v228 offset:12288
	ds_read_b64 v[136:137], v229 offset:14336
	s_waitcnt lgkmcnt(8)
	v_pk_fma_f32 v[74:75], v[110:111], v[78:79], v[74:75] op_sel_hi:[1,0,1]
	v_pk_fma_f32 v[114:115], v[102:103], v[78:79], v[114:115] op_sel_hi:[1,0,1]
	s_waitcnt lgkmcnt(6)
	v_pk_mul_f32 v[110:111], v[124:125], v[74:75]
	v_pk_fma_f32 v[76:77], v[108:109], v[78:79], v[76:77] op_sel_hi:[1,0,1]
	s_waitcnt lgkmcnt(2)
	v_pk_mul_f32 v[102:103], v[114:115], v[132:133]
	v_pk_fma_f32 v[116:117], v[100:101], v[78:79], v[116:117] op_sel_hi:[1,0,1]
	v_pk_fma_f32 v[74:75], v[124:125], v[74:75], 0 op_sel_hi:[1,1,0]
	v_pk_fma_f32 v[114:115], v[114:115], v[132:133], 0 op_sel_hi:[1,1,0]
	v_pk_fma_f32 v[122:123], v[112:113], v[78:79], v[72:73] op_sel_hi:[1,0,1]
	v_pk_mul_f32 v[108:109], v[126:127], v[76:77]
	v_pk_fma_f32 v[80:81], v[106:107], v[78:79], v[80:81] op_sel_hi:[1,0,1]
	v_pk_fma_f32 v[120:121], v[104:105], v[78:79], v[120:121] op_sel_hi:[1,0,1]
	s_waitcnt lgkmcnt(1)
	v_pk_mul_f32 v[100:101], v[116:117], v[134:135]
	v_pk_fma_f32 v[78:79], v[98:99], v[78:79], v[118:119] op_sel_hi:[1,0,1]
	v_pk_add_f32 v[124:125], v[74:75], v[114:115]
	v_pk_add_f32 v[74:75], v[74:75], v[114:115] neg_lo:[0,1] neg_hi:[0,1]
	v_pk_fma_f32 v[114:115], v[102:103], s[28:29], v[110:111] op_sel:[1,0,0] op_sel_hi:[0,1,1]
	v_pk_fma_f32 v[76:77], v[126:127], v[76:77], 0 op_sel_hi:[1,1,0]
	v_pk_fma_f32 v[116:117], v[116:117], v[134:135], 0 op_sel_hi:[1,1,0]
	s_mov_b32 s57, s30
	v_pk_mul_f32 v[106:107], v[128:129], v[80:81]
	s_waitcnt lgkmcnt(0)
	v_pk_mul_f32 v[98:99], v[78:79], v[136:137]
	v_pk_add_f32 v[126:127], v[76:77], v[116:117]
	v_pk_add_f32 v[76:77], v[76:77], v[116:117] neg_lo:[0,1] neg_hi:[0,1]
	v_pk_fma_f32 v[116:117], v[100:101], s[28:29], v[108:109] op_sel:[1,0,0] op_sel_hi:[0,1,1]
	v_pk_fma_f32 v[80:81], v[128:129], v[80:81], 0 op_sel_hi:[1,1,0]
	v_pk_fma_f32 v[78:79], v[78:79], v[136:137], 0 op_sel_hi:[1,1,0]
	v_pk_mul_f32 v[138:139], v[114:115], s[56:57] op_sel_hi:[0,1]
	s_mov_b32 s0, s35
	s_mov_b32 s1, s34
	s_mov_b32 s12, s37
	s_mov_b32 s13, s36
	v_pk_add_f32 v[128:129], v[80:81], v[78:79]
	v_pk_add_f32 v[78:79], v[80:81], v[78:79] neg_lo:[0,1] neg_hi:[0,1]
	v_pk_fma_f32 v[80:81], v[98:99], s[28:29], v[106:107] op_sel:[1,0,0] op_sel_hi:[0,1,1]
	v_pk_fma_f32 v[114:115], v[114:115], s[0:1], v[138:139] op_sel:[1,0,0]
	v_pk_mul_f32 v[138:139], v[116:117], s[12:13] op_sel_hi:[0,1]
	s_mov_b32 s58, s37
	s_mov_b32 s8, s35
	s_mov_b32 s9, s38
	v_pk_fma_f32 v[116:117], v[116:117], s[58:59], v[138:139] op_sel:[1,0,0] op_sel_hi:[1,0,1]
	v_pk_mul_f32 v[138:139], v[80:81], s[8:9] op_sel_hi:[0,1]
	v_pk_fma_f32 v[80:81], v[80:81], s[34:35], v[138:139] op_sel:[1,0,0]
	v_pk_mul_f32 v[138:139], v[74:75], s[12:13] op_sel_hi:[0,1]
	s_mov_b32 s19, s26
	v_pk_fma_f32 v[132:133], v[102:103], s[26:27], v[110:111] op_sel:[1,0,0] op_sel_hi:[0,1,1]
	v_pk_fma_f32 v[74:75], v[74:75], s[58:59], v[138:139] op_sel:[1,0,0] op_sel_hi:[1,0,1]
	v_pk_mul_f32 v[138:139], v[76:77], s[18:19] op_sel_hi:[0,1]
	s_mov_b32 s60, s27
	s_mov_b32 s61, s18
	v_pk_mul_f32 v[112:113], v[82:83], v[122:123]
	v_pk_mul_f32 v[104:105], v[120:121], v[130:131]
	v_pk_fma_f32 v[82:83], v[82:83], v[122:123], 0 op_sel_hi:[1,1,0]
	v_pk_fma_f32 v[120:121], v[120:121], v[130:131], 0 op_sel_hi:[1,1,0]
	v_pk_fma_f32 v[136:137], v[98:99], s[26:27], v[106:107] op_sel:[1,0,0] op_sel_hi:[0,1,1]
	v_pk_fma_f32 v[76:77], v[76:77], s[60:61], v[138:139] op_sel:[1,0,0]
	v_pk_mul_f32 v[138:139], v[132:133], s[8:9] op_sel_hi:[0,1]
	s_mov_b32 s39, s35
	v_pk_add_f32 v[122:123], v[82:83], v[120:121]
	v_pk_fma_f32 v[132:133], v[132:133], s[34:35], v[138:139] op_sel:[1,0,0]
	v_pk_mul_f32 v[138:139], v[136:137], s[38:39] op_sel_hi:[0,1]
	s_mov_b32 s31, s38
	v_pk_add_f32 v[82:83], v[82:83], v[120:121] neg_lo:[0,1] neg_hi:[0,1]
	v_pk_fma_f32 v[120:121], v[104:105], s[28:29], v[112:113] op_sel:[1,0,0] op_sel_hi:[0,1,1]
	v_pk_fma_f32 v[134:135], v[100:101], s[26:27], v[108:109] op_sel:[1,0,0] op_sel_hi:[0,1,1]
	v_mul_f32_e32 v86, 0xbf3504f3, v78
	v_pk_fma_f32 v[136:137], v[136:137], s[30:31], v[138:139] op_sel:[1,0,0]
	v_pk_add_f32 v[138:139], v[122:123], v[126:127]
	v_pk_add_f32 v[122:123], v[122:123], v[126:127] neg_lo:[0,1] neg_hi:[0,1]
	v_pk_add_f32 v[126:127], v[124:125], v[128:129]
	v_pk_add_f32 v[124:125], v[124:125], v[128:129] neg_lo:[0,1] neg_hi:[0,1]
	v_pk_fma_f32 v[78:79], v[78:79], s[12:13], v[86:87] op_sel:[1,0,0] op_sel_hi:[1,1,0]
	v_mul_f32_e32 v86, 0xbf3504f3, v134
	v_pk_add_f32 v[128:129], v[138:139], v[126:127]
	v_pk_add_f32 v[126:127], v[138:139], v[126:127] neg_lo:[0,1] neg_hi:[0,1]
	v_pk_fma_f32 v[138:139], v[124:125], s[28:29], v[122:123] op_sel:[1,0,0] op_sel_hi:[0,1,1]
	v_pk_fma_f32 v[122:123], v[124:125], s[26:27], v[122:123] op_sel:[1,0,0] op_sel_hi:[0,1,1]
	v_pk_add_f32 v[124:125], v[120:121], v[116:117]
	v_pk_add_f32 v[116:117], v[120:121], v[116:117] neg_lo:[0,1] neg_hi:[0,1]
	v_pk_add_f32 v[120:121], v[114:115], v[80:81]
	v_pk_add_f32 v[80:81], v[114:115], v[80:81] neg_lo:[0,1] neg_hi:[0,1]
	v_pk_fma_f32 v[130:131], v[104:105], s[26:27], v[112:113] op_sel:[1,0,0] op_sel_hi:[0,1,1]
	v_pk_fma_f32 v[134:135], v[134:135], s[12:13], v[86:87] op_sel:[1,0,0] op_sel_hi:[1,1,0]
	v_pk_add_f32 v[114:115], v[124:125], v[120:121]
	v_pk_add_f32 v[120:121], v[124:125], v[120:121] neg_lo:[0,1] neg_hi:[0,1]
	v_pk_fma_f32 v[124:125], v[80:81], s[28:29], v[116:117] op_sel:[1,0,0] op_sel_hi:[0,1,1]
	v_pk_fma_f32 v[80:81], v[80:81], s[26:27], v[116:117] op_sel:[1,0,0] op_sel_hi:[0,1,1]
	v_pk_add_f32 v[116:117], v[82:83], v[76:77]
	v_pk_add_f32 v[76:77], v[82:83], v[76:77] neg_lo:[0,1] neg_hi:[0,1]
	v_pk_add_f32 v[82:83], v[74:75], v[78:79]
	v_pk_add_f32 v[74:75], v[74:75], v[78:79] neg_lo:[0,1] neg_hi:[0,1]
	v_mov_b32_e32 v118, v217
	v_mov_b32_e32 v72, v218
	v_mov_b32_e32 v162, v215
	v_mov_b32_e32 v119, v220
	v_mov_b32_e32 v73, v221
	v_pk_add_f32 v[78:79], v[116:117], v[82:83]
	v_pk_add_f32 v[82:83], v[116:117], v[82:83] neg_lo:[0,1] neg_hi:[0,1]
	v_pk_fma_f32 v[116:117], v[74:75], s[28:29], v[76:77] op_sel:[1,0,0] op_sel_hi:[0,1,1]
	v_pk_fma_f32 v[74:75], v[74:75], s[26:27], v[76:77] op_sel:[1,0,0] op_sel_hi:[0,1,1]
	v_pk_add_f32 v[76:77], v[130:131], v[134:135]
	v_pk_add_f32 v[130:131], v[130:131], v[134:135] neg_lo:[0,1] neg_hi:[0,1]
	v_pk_add_f32 v[134:135], v[132:133], v[136:137]
	v_pk_add_f32 v[132:133], v[132:133], v[136:137] neg_lo:[0,1] neg_hi:[0,1]
	v_pk_add_f32 v[136:137], v[76:77], v[134:135]
	v_pk_add_f32 v[76:77], v[76:77], v[134:135] neg_lo:[0,1] neg_hi:[0,1]
	v_pk_fma_f32 v[134:135], v[132:133], s[28:29], v[130:131] op_sel:[1,0,0] op_sel_hi:[0,1,1]
	v_pk_fma_f32 v[130:131], v[132:133], s[26:27], v[130:131] op_sel:[1,0,0] op_sel_hi:[0,1,1]
	v_pk_mul_f32 v[132:133], v[118:119], s[28:29]
	v_mov_b32_e32 v86, v119
	v_pk_mul_f32 v[140:141], v[118:119], v[118:119] op_sel_hi:[1,0]
	v_pk_mul_f32 v[160:161], v[118:119], v[114:115] op_sel_hi:[1,0]
	v_pk_fma_f32 v[140:141], v[86:87], v[132:133], v[140:141] op_sel:[0,1,0] op_sel_hi:[0,0,1]
	v_pk_mul_f32 v[144:145], v[140:141], s[28:29]
	v_pk_mul_f32 v[146:147], v[140:141], v[140:141] op_sel_hi:[1,0]
	v_pk_mul_f32 v[142:143], v[118:119], v[140:141] op_sel_hi:[1,0]
	v_pk_fma_f32 v[146:147], v[140:141], v[144:145], v[146:147] op_sel:[1,1,0] op_sel_hi:[1,0,1]
	v_pk_fma_f32 v[142:143], v[140:141], v[132:133], v[142:143] op_sel:[1,1,0] op_sel_hi:[1,0,1]
	v_pk_mul_f32 v[148:149], v[118:119], v[146:147] op_sel_hi:[1,0]
	v_pk_fma_f32 v[114:115], v[114:115], v[132:133], v[160:161] op_sel:[1,1,0] op_sel_hi:[1,0,1]
	v_pk_fma_f32 v[148:149], v[146:147], v[132:133], v[148:149] op_sel:[1,1,0] op_sel_hi:[1,0,1]
	v_pk_mul_f32 v[132:133], v[140:141], v[78:79] op_sel_hi:[1,0]
	v_pk_mul_f32 v[152:153], v[142:143], s[28:29]
	v_pk_fma_f32 v[78:79], v[78:79], v[144:145], v[132:133] op_sel:[1,1,0] op_sel_hi:[1,0,1]
	v_pk_mul_f32 v[132:133], v[136:137], v[142:143] op_sel_hi:[0,1]
	v_pk_mul_f32 v[150:151], v[140:141], v[146:147] op_sel_hi:[1,0]
	v_pk_mul_f32 v[156:157], v[146:147], s[28:29]
	v_pk_fma_f32 v[132:133], v[136:137], v[152:153], v[132:133] op_sel:[1,1,0] op_sel_hi:[1,0,1]
	v_pk_mul_f32 v[136:137], v[138:139], v[146:147] op_sel_hi:[0,1]
	v_pk_fma_f32 v[150:151], v[146:147], v[144:145], v[150:151] op_sel:[1,1,0] op_sel_hi:[1,0,1]
	v_pk_mul_f32 v[154:155], v[142:143], v[146:147] op_sel_hi:[1,0]
	v_pk_fma_f32 v[136:137], v[138:139], v[156:157], v[136:137] op_sel:[1,1,0] op_sel_hi:[1,0,1]
	v_pk_mul_f32 v[138:139], v[148:149], s[28:29]
	v_pk_mul_f32 v[144:145], v[124:125], v[148:149] op_sel_hi:[0,1]
	v_pk_fma_f32 v[154:155], v[146:147], v[152:153], v[154:155] op_sel:[1,1,0] op_sel_hi:[1,0,1]
	v_pk_mul_f32 v[158:159], v[146:147], v[146:147] op_sel_hi:[1,0]
	v_pk_fma_f32 v[124:125], v[124:125], v[138:139], v[144:145] op_sel:[1,1,0] op_sel_hi:[1,0,1]
	v_pk_mul_f32 v[138:139], v[150:151], s[28:29]
	v_pk_mul_f32 v[144:145], v[116:117], v[150:151] op_sel_hi:[0,1]
	v_pk_fma_f32 v[158:159], v[146:147], v[156:157], v[158:159] op_sel:[1,1,0] op_sel_hi:[1,0,1]
	v_pk_fma_f32 v[116:117], v[116:117], v[138:139], v[144:145] op_sel:[1,1,0] op_sel_hi:[1,0,1]
	v_pk_mul_f32 v[138:139], v[154:155], s[28:29]
	v_pk_mul_f32 v[144:145], v[134:135], v[154:155] op_sel_hi:[0,1]
	v_pk_fma_f32 v[134:135], v[134:135], v[138:139], v[144:145] op_sel:[1,1,0] op_sel_hi:[1,0,1]
	v_pk_mul_f32 v[138:139], v[158:159], s[28:29]
	v_pk_mul_f32 v[118:119], v[118:119], v[158:159] op_sel_hi:[0,1]
	v_pk_mul_f32 v[144:145], v[126:127], v[158:159] op_sel_hi:[0,1]
	v_pk_fma_f32 v[118:119], v[86:87], v[138:139], v[118:119] op_sel:[0,1,0] op_sel_hi:[0,0,1]
	v_pk_fma_f32 v[126:127], v[126:127], v[138:139], v[144:145] op_sel:[1,1,0] op_sel_hi:[1,0,1]
	v_pk_mul_f32 v[144:145], v[118:119], s[28:29]
	v_pk_mul_f32 v[118:119], v[120:121], v[118:119] op_sel_hi:[0,1]
	v_pk_fma_f32 v[118:119], v[120:121], v[144:145], v[118:119] op_sel:[1,1,0] op_sel_hi:[1,0,1]
	v_pk_mul_f32 v[120:121], v[140:141], v[158:159] op_sel_hi:[0,1]
	v_pk_fma_f32 v[120:121], v[140:141], v[138:139], v[120:121] op_sel:[1,1,0] op_sel_hi:[1,0,1]
	v_ashrrev_i32_e32 v86, 4, v162
	v_pk_mul_f32 v[140:141], v[120:121], s[28:29]
	v_pk_mul_f32 v[120:121], v[82:83], v[120:121] op_sel_hi:[0,1]
	v_pk_fma_f32 v[82:83], v[82:83], v[140:141], v[120:121] op_sel:[1,1,0] op_sel_hi:[1,0,1]
	v_pk_mul_f32 v[120:121], v[142:143], v[158:159] op_sel_hi:[0,1]
	v_pk_fma_f32 v[120:121], v[142:143], v[138:139], v[120:121] op_sel:[1,1,0] op_sel_hi:[1,0,1]
	s_mov_b32 s79, 0x62704000
	v_pk_mul_f32 v[140:141], v[120:121], s[28:29]
	v_pk_mul_f32 v[120:121], v[76:77], v[120:121] op_sel_hi:[0,1]
	v_pk_fma_f32 v[76:77], v[76:77], v[140:141], v[120:121] op_sel:[1,1,0] op_sel_hi:[1,0,1]
	v_pk_mul_f32 v[120:121], v[146:147], v[158:159] op_sel_hi:[0,1]
	v_pk_fma_f32 v[120:121], v[146:147], v[138:139], v[120:121] op_sel:[1,1,0] op_sel_hi:[1,0,1]
	s_add_i32 s78, s62, 4
	v_pk_mul_f32 v[140:141], v[120:121], s[28:29]
	v_pk_mul_f32 v[120:121], v[122:123], v[120:121] op_sel_hi:[0,1]
	v_pk_fma_f32 v[120:121], v[122:123], v[140:141], v[120:121] op_sel:[1,1,0] op_sel_hi:[1,0,1]
	v_pk_mul_f32 v[122:123], v[158:159], v[148:149] op_sel_hi:[1,0]
	s_nop 0
	v_pk_fma_f32 v[122:123], v[148:149], v[138:139], v[122:123] op_sel:[1,1,0] op_sel_hi:[1,0,1]
	s_nop 0
	v_pk_mul_f32 v[140:141], v[122:123], s[28:29]
	v_pk_mul_f32 v[122:123], v[80:81], v[122:123] op_sel_hi:[0,1]
	v_pk_fma_f32 v[80:81], v[80:81], v[140:141], v[122:123] op_sel:[1,1,0] op_sel_hi:[1,0,1]
	v_pk_mul_f32 v[122:123], v[158:159], v[150:151] op_sel_hi:[1,0]
	s_nop 0
	v_pk_fma_f32 v[122:123], v[150:151], v[138:139], v[122:123] op_sel:[1,1,0] op_sel_hi:[1,0,1]
	s_nop 0
	v_pk_mul_f32 v[140:141], v[122:123], s[28:29]
	v_pk_mul_f32 v[122:123], v[74:75], v[122:123] op_sel_hi:[0,1]
	v_pk_fma_f32 v[74:75], v[74:75], v[140:141], v[122:123] op_sel:[1,1,0] op_sel_hi:[1,0,1]
	v_pk_mul_f32 v[122:123], v[158:159], v[154:155] op_sel_hi:[1,0]
	s_nop 0
	v_pk_fma_f32 v[122:123], v[154:155], v[138:139], v[122:123] op_sel:[1,1,0] op_sel_hi:[1,0,1]
	s_nop 0
	v_pk_mul_f32 v[138:139], v[122:123], s[28:29]
	v_pk_mul_f32 v[122:123], v[130:131], v[122:123] op_sel_hi:[0,1]
	v_pk_fma_f32 v[122:123], v[130:131], v[138:139], v[122:123] op_sel:[1,1,0] op_sel_hi:[1,0,1]
	v_lshlrev_b32_e32 v130, 3, v162
	v_add_u32_e32 v160, v219, v130
	v_lshl_add_u32 v131, v86, 3, v160
	ds_write_b64 v131, v[128:129]
	v_add_u32_e32 v128, 0x100, v162
	v_ashrrev_i32_e32 v128, 4, v128
	v_lshl_add_u32 v128, v128, 3, v160
	ds_write_b64 v128, v[114:115] offset:2048
	v_add_u32_e32 v114, 0x200, v162
	v_ashrrev_i32_e32 v114, 4, v114
	v_lshl_add_u32 v114, v114, 3, v160
	ds_write_b64 v114, v[78:79] offset:4096
	v_add_u32_e32 v78, 0x300, v162
	v_ashrrev_i32_e32 v78, 4, v78
	v_lshl_add_u32 v78, v78, 3, v160
	ds_write_b64 v78, v[132:133] offset:6144
	v_add_u32_e32 v78, 0x400, v162
	v_ashrrev_i32_e32 v78, 4, v78
	v_lshl_add_u32 v78, v78, 3, v160
	ds_write_b64 v78, v[136:137] offset:8192
	v_add_u32_e32 v78, 0x500, v162
	v_ashrrev_i32_e32 v78, 4, v78
	v_lshl_add_u32 v78, v78, 3, v160
	ds_write_b64 v78, v[124:125] offset:10240
	v_add_u32_e32 v78, 0x600, v162
	v_ashrrev_i32_e32 v78, 4, v78
	v_lshl_add_u32 v78, v78, 3, v160
	ds_write_b64 v78, v[116:117] offset:12288
	v_add_u32_e32 v78, 0x700, v162
	v_ashrrev_i32_e32 v78, 4, v78
	v_lshl_add_u32 v78, v78, 3, v160
	ds_write_b64 v78, v[134:135] offset:14336
	v_add_u32_e32 v78, 0x800, v162
	v_ashrrev_i32_e32 v78, 4, v78
	v_lshl_add_u32 v78, v78, 3, v160
	ds_write_b64 v78, v[126:127] offset:16384
	v_add_u32_e32 v78, 0x900, v162
	v_ashrrev_i32_e32 v78, 4, v78
	v_lshl_add_u32 v78, v78, 3, v160
	ds_write_b64 v78, v[118:119] offset:18432
	v_add_u32_e32 v78, 0xa00, v162
	v_ashrrev_i32_e32 v78, 4, v78
	v_lshl_add_u32 v78, v78, 3, v160
	ds_write_b64 v78, v[82:83] offset:20480
	v_add_u32_e32 v78, 0xb00, v162
	v_ashrrev_i32_e32 v78, 4, v78
	v_lshl_add_u32 v78, v78, 3, v160
	ds_write_b64 v78, v[76:77] offset:22528
	v_add_u32_e32 v76, 0xc00, v162
	v_ashrrev_i32_e32 v76, 4, v76
	v_lshl_add_u32 v76, v76, 3, v160
	ds_write_b64 v76, v[120:121] offset:24576
	v_add_u32_e32 v76, 0xd00, v162
	v_ashrrev_i32_e32 v76, 4, v76
	v_lshl_add_u32 v76, v76, 3, v160
	ds_write_b64 v76, v[80:81] offset:26624
	v_add_u32_e32 v76, 0xe00, v162
	v_ashrrev_i32_e32 v76, 4, v76
	v_lshl_add_u32 v76, v76, 3, v160
	ds_write_b64 v76, v[74:75] offset:28672
	v_add_u32_e32 v74, 0xf00, v162
	v_ashrrev_i32_e32 v74, 4, v74
	v_lshl_add_u32 v74, v74, 3, v160
	ds_write_b64 v74, v[122:123] offset:30720
	v_lshlrev_b32_e32 v74, 8, v86
	v_lshl_add_u32 v75, v86, 7, v219
	v_lshlrev_b32_e32 v76, 11, v86
	v_and_b32_e32 v77, 0x78, v130
	v_add3_u32 v161, v75, v76, v77
	v_ashrrev_i32_e32 v74, 1, v74
	s_waitcnt lgkmcnt(0)
	s_barrier
	ds_read_b64 v[82:83], v161
	v_add_u32_e32 v74, v219, v74
	v_add3_u32 v163, v74, v76, v77
	ds_read2_b64 v[74:77], v163 offset0:17 offset1:34
	ds_read2_b64 v[78:81], v163 offset0:51 offset1:68
	ds_read2_b64 v[114:117], v163 offset0:85 offset1:102
	ds_read2_b64 v[118:121], v163 offset0:119 offset1:136
	ds_read2_b64 v[122:125], v163 offset0:153 offset1:170
	ds_read2_b64 v[126:129], v163 offset0:187 offset1:204
	ds_read2_b64 v[130:133], v163 offset0:221 offset1:238
	ds_read_b64 v[134:135], v163 offset:2040
	v_pk_mul_f32 v[138:139], v[72:73], v[72:73] op_sel_hi:[1,0]
	s_waitcnt lgkmcnt(4)
	v_pk_add_f32 v[136:137], v[82:83], v[120:121]
	v_pk_add_f32 v[82:83], v[82:83], v[120:121] neg_lo:[0,1] neg_hi:[0,1]
	s_waitcnt lgkmcnt(2)
	v_pk_add_f32 v[120:121], v[80:81], v[128:129]
	v_pk_add_f32 v[80:81], v[80:81], v[128:129] neg_lo:[0,1] neg_hi:[0,1]
	v_pk_add_f32 v[128:129], v[136:137], v[120:121]
	v_pk_add_f32 v[120:121], v[136:137], v[120:121] neg_lo:[0,1] neg_hi:[0,1]
	v_pk_fma_f32 v[136:137], v[80:81], s[28:29], v[82:83] op_sel:[1,0,0] op_sel_hi:[0,1,1]
	v_pk_fma_f32 v[80:81], v[80:81], s[26:27], v[82:83] op_sel:[1,0,0] op_sel_hi:[0,1,1]
	v_pk_add_f32 v[82:83], v[74:75], v[122:123]
	v_pk_add_f32 v[74:75], v[74:75], v[122:123] neg_lo:[0,1] neg_hi:[0,1]
	s_waitcnt lgkmcnt(1)
	v_pk_add_f32 v[122:123], v[114:115], v[130:131]
	v_pk_add_f32 v[114:115], v[114:115], v[130:131] neg_lo:[0,1] neg_hi:[0,1]
	v_pk_add_f32 v[130:131], v[82:83], v[122:123]
	v_pk_add_f32 v[82:83], v[82:83], v[122:123] neg_lo:[0,1] neg_hi:[0,1]
	v_pk_fma_f32 v[122:123], v[114:115], s[28:29], v[74:75] op_sel:[1,0,0] op_sel_hi:[0,1,1]
	v_pk_fma_f32 v[74:75], v[114:115], s[26:27], v[74:75] op_sel:[1,0,0] op_sel_hi:[0,1,1]
	v_pk_add_f32 v[114:115], v[76:77], v[124:125]
	v_pk_add_f32 v[76:77], v[76:77], v[124:125] neg_lo:[0,1] neg_hi:[0,1]
	v_pk_add_f32 v[124:125], v[116:117], v[132:133]
	v_pk_add_f32 v[116:117], v[116:117], v[132:133] neg_lo:[0,1] neg_hi:[0,1]
	v_pk_add_f32 v[132:133], v[114:115], v[124:125]
	v_pk_add_f32 v[114:115], v[114:115], v[124:125] neg_lo:[0,1] neg_hi:[0,1]
	v_pk_fma_f32 v[124:125], v[116:117], s[28:29], v[76:77] op_sel:[1,0,0] op_sel_hi:[0,1,1]
	v_pk_fma_f32 v[76:77], v[116:117], s[26:27], v[76:77] op_sel:[1,0,0] op_sel_hi:[0,1,1]
	v_pk_add_f32 v[116:117], v[78:79], v[126:127]
	v_pk_add_f32 v[78:79], v[78:79], v[126:127] neg_lo:[0,1] neg_hi:[0,1]
	s_waitcnt lgkmcnt(0)
	v_pk_add_f32 v[126:127], v[118:119], v[134:135]
	v_pk_add_f32 v[118:119], v[118:119], v[134:135] neg_lo:[0,1] neg_hi:[0,1]
	v_pk_add_f32 v[134:135], v[116:117], v[126:127]
	v_pk_add_f32 v[116:117], v[116:117], v[126:127] neg_lo:[0,1] neg_hi:[0,1]
	v_pk_fma_f32 v[126:127], v[118:119], s[28:29], v[78:79] op_sel:[1,0,0] op_sel_hi:[0,1,1]
	v_pk_fma_f32 v[78:79], v[118:119], s[26:27], v[78:79] op_sel:[1,0,0] op_sel_hi:[0,1,1]
	v_pk_mul_f32 v[118:119], v[122:123], s[56:57] op_sel_hi:[0,1]
	v_pk_fma_f32 v[118:119], v[122:123], s[0:1], v[118:119] op_sel:[1,0,0]
	v_pk_mul_f32 v[122:123], v[124:125], s[12:13] op_sel_hi:[0,1]
	v_pk_fma_f32 v[122:123], v[124:125], s[58:59], v[122:123] op_sel:[1,0,0] op_sel_hi:[1,0,1]
	v_pk_mul_f32 v[124:125], v[126:127], s[8:9] op_sel_hi:[0,1]
	v_pk_fma_f32 v[124:125], v[126:127], s[34:35], v[124:125] op_sel:[1,0,0]
	v_pk_mul_f32 v[126:127], v[82:83], s[12:13] op_sel_hi:[0,1]
	v_pk_fma_f32 v[82:83], v[82:83], s[58:59], v[126:127] op_sel:[1,0,0] op_sel_hi:[1,0,1]
	v_pk_mul_f32 v[126:127], v[114:115], s[18:19] op_sel_hi:[0,1]
	v_pk_fma_f32 v[114:115], v[114:115], s[60:61], v[126:127] op_sel:[1,0,0]
	v_pk_mul_f32 v[126:127], v[74:75], s[8:9] op_sel_hi:[0,1]
	v_pk_fma_f32 v[74:75], v[74:75], s[34:35], v[126:127] op_sel:[1,0,0]
	v_pk_mul_f32 v[126:127], v[78:79], s[38:39] op_sel_hi:[0,1]
	v_mul_f32_e32 v86, 0xbf3504f3, v116
	v_pk_fma_f32 v[78:79], v[78:79], s[30:31], v[126:127] op_sel:[1,0,0]
	v_pk_add_f32 v[126:127], v[128:129], v[132:133]
	v_pk_add_f32 v[128:129], v[128:129], v[132:133] neg_lo:[0,1] neg_hi:[0,1]
	v_pk_add_f32 v[132:133], v[130:131], v[134:135]
	v_pk_add_f32 v[130:131], v[130:131], v[134:135] neg_lo:[0,1] neg_hi:[0,1]
	v_pk_fma_f32 v[116:117], v[116:117], s[12:13], v[86:87] op_sel:[1,0,0] op_sel_hi:[1,1,0]
	v_mul_f32_e32 v86, 0xbf3504f3, v76
	v_pk_add_f32 v[134:135], v[126:127], v[132:133]
	v_pk_add_f32 v[126:127], v[126:127], v[132:133] neg_lo:[0,1] neg_hi:[0,1]
	v_pk_fma_f32 v[132:133], v[130:131], s[28:29], v[128:129] op_sel:[1,0,0] op_sel_hi:[0,1,1]
	v_pk_fma_f32 v[128:129], v[130:131], s[26:27], v[128:129] op_sel:[1,0,0] op_sel_hi:[0,1,1]
	v_pk_add_f32 v[130:131], v[136:137], v[122:123]
	v_pk_add_f32 v[122:123], v[136:137], v[122:123] neg_lo:[0,1] neg_hi:[0,1]
	v_pk_add_f32 v[136:137], v[118:119], v[124:125]
	v_pk_add_f32 v[118:119], v[118:119], v[124:125] neg_lo:[0,1] neg_hi:[0,1]
	v_pk_fma_f32 v[76:77], v[76:77], s[12:13], v[86:87] op_sel:[1,0,0] op_sel_hi:[1,1,0]
	v_pk_add_f32 v[124:125], v[130:131], v[136:137]
	v_pk_add_f32 v[130:131], v[130:131], v[136:137] neg_lo:[0,1] neg_hi:[0,1]
	v_pk_fma_f32 v[136:137], v[118:119], s[28:29], v[122:123] op_sel:[1,0,0] op_sel_hi:[0,1,1]
	v_pk_fma_f32 v[118:119], v[118:119], s[26:27], v[122:123] op_sel:[1,0,0] op_sel_hi:[0,1,1]
	v_pk_add_f32 v[122:123], v[120:121], v[114:115]
	v_pk_add_f32 v[114:115], v[120:121], v[114:115] neg_lo:[0,1] neg_hi:[0,1]
	v_pk_add_f32 v[120:121], v[82:83], v[116:117]
	v_pk_add_f32 v[82:83], v[82:83], v[116:117] neg_lo:[0,1] neg_hi:[0,1]
	v_pk_add_f32 v[116:117], v[122:123], v[120:121]
	v_pk_add_f32 v[120:121], v[122:123], v[120:121] neg_lo:[0,1] neg_hi:[0,1]
	v_pk_fma_f32 v[122:123], v[82:83], s[28:29], v[114:115] op_sel:[1,0,0] op_sel_hi:[0,1,1]
	v_pk_fma_f32 v[82:83], v[82:83], s[26:27], v[114:115] op_sel:[1,0,0] op_sel_hi:[0,1,1]
	v_pk_add_f32 v[114:115], v[80:81], v[76:77]
	v_pk_add_f32 v[76:77], v[80:81], v[76:77] neg_lo:[0,1] neg_hi:[0,1]
	v_pk_add_f32 v[80:81], v[74:75], v[78:79]
	v_pk_add_f32 v[74:75], v[74:75], v[78:79] neg_lo:[0,1] neg_hi:[0,1]
	v_pk_add_f32 v[78:79], v[114:115], v[80:81]
	v_pk_add_f32 v[80:81], v[114:115], v[80:81] neg_lo:[0,1] neg_hi:[0,1]
	v_pk_fma_f32 v[114:115], v[74:75], s[28:29], v[76:77] op_sel:[1,0,0] op_sel_hi:[0,1,1]
	v_pk_fma_f32 v[74:75], v[74:75], s[26:27], v[76:77] op_sel:[1,0,0] op_sel_hi:[0,1,1]
	v_pk_mul_f32 v[76:77], v[72:73], s[28:29]
	v_mov_b32_e32 v86, v73
	v_pk_fma_f32 v[138:139], v[86:87], v[76:77], v[138:139] op_sel:[0,1,0] op_sel_hi:[0,0,1]
	v_pk_mul_f32 v[142:143], v[138:139], s[28:29]
	v_pk_mul_f32 v[144:145], v[138:139], v[138:139] op_sel_hi:[1,0]
	v_pk_mul_f32 v[140:141], v[72:73], v[138:139] op_sel_hi:[1,0]
	v_pk_fma_f32 v[144:145], v[138:139], v[142:143], v[144:145] op_sel:[1,1,0] op_sel_hi:[1,0,1]
	v_pk_mul_f32 v[158:159], v[72:73], v[124:125] op_sel_hi:[1,0]
	v_pk_mul_f32 v[146:147], v[72:73], v[144:145] op_sel_hi:[1,0]
	v_pk_fma_f32 v[140:141], v[138:139], v[76:77], v[140:141] op_sel:[1,1,0] op_sel_hi:[1,0,1]
	v_pk_fma_f32 v[146:147], v[144:145], v[76:77], v[146:147] op_sel:[1,1,0] op_sel_hi:[1,0,1]
	v_pk_fma_f32 v[76:77], v[124:125], v[76:77], v[158:159] op_sel:[1,1,0] op_sel_hi:[1,0,1]
	v_pk_mul_f32 v[124:125], v[138:139], v[116:117] op_sel_hi:[1,0]
	v_pk_mul_f32 v[150:151], v[140:141], s[28:29]
	v_pk_fma_f32 v[116:117], v[116:117], v[142:143], v[124:125] op_sel:[1,1,0] op_sel_hi:[1,0,1]
	v_pk_mul_f32 v[124:125], v[140:141], v[78:79] op_sel_hi:[1,0]
	v_pk_mul_f32 v[148:149], v[138:139], v[144:145] op_sel_hi:[1,0]
	v_pk_mul_f32 v[154:155], v[144:145], s[28:29]
	v_pk_fma_f32 v[78:79], v[78:79], v[150:151], v[124:125] op_sel:[1,1,0] op_sel_hi:[1,0,1]
	v_pk_mul_f32 v[124:125], v[144:145], v[132:133] op_sel_hi:[1,0]
	v_pk_fma_f32 v[148:149], v[144:145], v[142:143], v[148:149] op_sel:[1,1,0] op_sel_hi:[1,0,1]
	v_pk_mul_f32 v[152:153], v[140:141], v[144:145] op_sel_hi:[1,0]
	v_pk_fma_f32 v[124:125], v[132:133], v[154:155], v[124:125] op_sel:[1,1,0] op_sel_hi:[1,0,1]
	v_pk_mul_f32 v[132:133], v[146:147], s[28:29]
	v_pk_mul_f32 v[142:143], v[146:147], v[136:137] op_sel_hi:[1,0]
	v_pk_fma_f32 v[152:153], v[144:145], v[150:151], v[152:153] op_sel:[1,1,0] op_sel_hi:[1,0,1]
	v_pk_mul_f32 v[156:157], v[144:145], v[144:145] op_sel_hi:[1,0]
	v_pk_fma_f32 v[132:133], v[136:137], v[132:133], v[142:143] op_sel:[1,1,0] op_sel_hi:[1,0,1]
	v_pk_mul_f32 v[136:137], v[148:149], s[28:29]
	v_pk_mul_f32 v[142:143], v[148:149], v[122:123] op_sel_hi:[1,0]
	v_pk_fma_f32 v[156:157], v[144:145], v[154:155], v[156:157] op_sel:[1,1,0] op_sel_hi:[1,0,1]
	v_pk_fma_f32 v[122:123], v[122:123], v[136:137], v[142:143] op_sel:[1,1,0] op_sel_hi:[1,0,1]
	v_pk_mul_f32 v[136:137], v[152:153], s[28:29]
	v_pk_mul_f32 v[142:143], v[152:153], v[114:115] op_sel_hi:[1,0]
	v_pk_mul_f32 v[72:73], v[72:73], v[156:157] op_sel_hi:[0,1]
	v_pk_fma_f32 v[114:115], v[114:115], v[136:137], v[142:143] op_sel:[1,1,0] op_sel_hi:[1,0,1]
	v_pk_mul_f32 v[136:137], v[156:157], s[28:29]
	v_pk_mul_f32 v[142:143], v[156:157], v[126:127] op_sel_hi:[1,0]
	v_pk_fma_f32 v[72:73], v[86:87], v[136:137], v[72:73] op_sel:[0,1,0] op_sel_hi:[0,0,1]
	v_pk_fma_f32 v[126:127], v[126:127], v[136:137], v[142:143] op_sel:[1,1,0] op_sel_hi:[1,0,1]
	v_pk_mul_f32 v[142:143], v[72:73], s[28:29]
	v_pk_mul_f32 v[72:73], v[72:73], v[130:131] op_sel_hi:[1,0]
	v_lshl_add_u32 v86, v162, 7, v160
	v_pk_fma_f32 v[72:73], v[130:131], v[142:143], v[72:73] op_sel:[1,1,0] op_sel_hi:[1,0,1]
	v_pk_mul_f32 v[130:131], v[138:139], v[156:157] op_sel_hi:[0,1]
	v_pk_fma_f32 v[130:131], v[138:139], v[136:137], v[130:131] op_sel:[1,1,0] op_sel_hi:[1,0,1]
	s_nop 0
	v_pk_mul_f32 v[138:139], v[130:131], s[28:29]
	v_pk_mul_f32 v[130:131], v[130:131], v[120:121] op_sel_hi:[1,0]
	s_nop 0
	v_pk_fma_f32 v[120:121], v[120:121], v[138:139], v[130:131] op_sel:[1,1,0] op_sel_hi:[1,0,1]
	v_pk_mul_f32 v[130:131], v[140:141], v[156:157] op_sel_hi:[0,1]
	v_pk_fma_f32 v[130:131], v[140:141], v[136:137], v[130:131] op_sel:[1,1,0] op_sel_hi:[1,0,1]
	s_nop 0
	v_pk_mul_f32 v[138:139], v[130:131], s[28:29]
	v_pk_mul_f32 v[130:131], v[130:131], v[80:81] op_sel_hi:[1,0]
	s_nop 0
	v_pk_fma_f32 v[80:81], v[80:81], v[138:139], v[130:131] op_sel:[1,1,0] op_sel_hi:[1,0,1]
	v_pk_mul_f32 v[130:131], v[144:145], v[156:157] op_sel_hi:[0,1]
	v_pk_fma_f32 v[130:131], v[144:145], v[136:137], v[130:131] op_sel:[1,1,0] op_sel_hi:[1,0,1]
	s_nop 0
	v_pk_mul_f32 v[138:139], v[130:131], s[28:29]
	v_pk_mul_f32 v[130:131], v[130:131], v[128:129] op_sel_hi:[1,0]
	s_nop 0
	v_pk_fma_f32 v[128:129], v[128:129], v[138:139], v[130:131] op_sel:[1,1,0] op_sel_hi:[1,0,1]
	v_pk_mul_f32 v[130:131], v[156:157], v[146:147] op_sel_hi:[1,0]
	s_nop 0
	v_pk_fma_f32 v[130:131], v[146:147], v[136:137], v[130:131] op_sel:[1,1,0] op_sel_hi:[1,0,1]
	s_nop 0
	v_pk_mul_f32 v[138:139], v[130:131], s[28:29]
	v_pk_mul_f32 v[130:131], v[130:131], v[118:119] op_sel_hi:[1,0]
	s_nop 0
	v_pk_fma_f32 v[118:119], v[118:119], v[138:139], v[130:131] op_sel:[1,1,0] op_sel_hi:[1,0,1]
	v_pk_mul_f32 v[130:131], v[156:157], v[148:149] op_sel_hi:[1,0]
	s_nop 0
	v_pk_fma_f32 v[130:131], v[148:149], v[136:137], v[130:131] op_sel:[1,1,0] op_sel_hi:[1,0,1]
	s_nop 0
	v_pk_mul_f32 v[138:139], v[130:131], s[28:29]
	v_pk_mul_f32 v[130:131], v[130:131], v[82:83] op_sel_hi:[1,0]
	s_nop 0
	v_pk_fma_f32 v[82:83], v[82:83], v[138:139], v[130:131] op_sel:[1,1,0] op_sel_hi:[1,0,1]
	v_pk_mul_f32 v[130:131], v[156:157], v[152:153] op_sel_hi:[1,0]
	s_nop 0
	v_pk_fma_f32 v[130:131], v[152:153], v[136:137], v[130:131] op_sel:[1,1,0] op_sel_hi:[1,0,1]
	s_nop 0
	v_pk_mul_f32 v[136:137], v[130:131], s[28:29]
	v_pk_mul_f32 v[130:131], v[130:131], v[74:75] op_sel_hi:[1,0]
	s_nop 0
	v_pk_fma_f32 v[74:75], v[74:75], v[136:137], v[130:131] op_sel:[1,1,0] op_sel_hi:[1,0,1]
	ds_write_b64 v161, v[134:135]
	ds_write2_b64 v163, v[76:77], v[116:117] offset0:17 offset1:34
	ds_write2_b64 v163, v[78:79], v[124:125] offset0:51 offset1:68
	ds_write2_b64 v163, v[132:133], v[122:123] offset0:85 offset1:102
	ds_write2_b64 v163, v[114:115], v[126:127] offset0:119 offset1:136
	ds_write2_b64 v163, v[72:73], v[120:121] offset0:153 offset1:170
	ds_write2_b64 v163, v[80:81], v[128:129] offset0:187 offset1:204
	ds_write2_b64 v163, v[118:119], v[82:83] offset0:221 offset1:238
	ds_write_b64 v163, v[74:75] offset:2040
	v_add_co_u32_e32 v72, vcc, s79, v96
	s_mov_b32 s79, 0x62705000
	s_nop 0
	v_addc_co_u32_e32 v73, vcc, 0, v97, vcc
	v_add_co_u32_e32 v74, vcc, s79, v96
	s_mov_b32 s79, 0x62706000
	s_nop 0
	v_addc_co_u32_e32 v75, vcc, 0, v97, vcc
	v_add_co_u32_e32 v76, vcc, s79, v96
	s_mov_b32 s79, 0x62707000
	s_nop 0
	v_addc_co_u32_e32 v77, vcc, 0, v97, vcc
	v_add_co_u32_e32 v78, vcc, s79, v96
	s_nop 1
	v_addc_co_u32_e32 v79, vcc, 0, v97, vcc
	global_load_dword v134, v[74:75], off offset:-4096
	global_load_dword v136, v[72:73], off offset:1024
	global_load_dword v137, v[72:73], off offset:2048
	global_load_dword v138, v[72:73], off offset:3072
	global_load_dword v139, v[74:75], off
	global_load_dword v140, v[76:77], off offset:1024
	global_load_dword v141, v[76:77], off offset:2048
	global_load_dword v142, v[76:77], off offset:3072
	global_load_dword v143, v[74:75], off offset:1024
	global_load_dword v144, v[74:75], off offset:2048
	global_load_dword v145, v[74:75], off offset:3072
	global_load_dword v146, v[78:79], off offset:-4096
	global_load_dword v147, v[78:79], off
	global_load_dword v148, v[78:79], off offset:1024
	global_load_dword v149, v[78:79], off offset:2048
	global_load_dword v150, v[78:79], off offset:3072
	s_waitcnt lgkmcnt(0)
	s_barrier
	ds_read2_b64 v[72:75], v86 offset1:1
	ds_read2_b64 v[76:79], v86 offset0:2 offset1:3
	ds_read2_b64 v[80:83], v86 offset0:8 offset1:9
	ds_read2_b64 v[114:117], v86 offset0:4 offset1:5
	ds_read2_b64 v[118:121], v86 offset0:6 offset1:7
	ds_read2_b64 v[122:125], v86 offset0:12 offset1:13
	ds_read2_b64 v[126:129], v86 offset0:10 offset1:11
	ds_read2_b64 v[130:133], v86 offset0:14 offset1:15
	s_waitcnt lgkmcnt(5)
	v_pk_add_f32 v[96:97], v[72:73], v[80:81]
	v_pk_add_f32 v[72:73], v[72:73], v[80:81] neg_lo:[0,1] neg_hi:[0,1]
	s_waitcnt lgkmcnt(2)
	v_pk_add_f32 v[80:81], v[114:115], v[122:123]
	v_pk_add_f32 v[114:115], v[114:115], v[122:123] neg_lo:[0,1] neg_hi:[0,1]
	v_pk_add_f32 v[122:123], v[96:97], v[80:81]
	v_pk_add_f32 v[80:81], v[96:97], v[80:81] neg_lo:[0,1] neg_hi:[0,1]
	v_pk_fma_f32 v[96:97], v[114:115], s[28:29], v[72:73] op_sel:[1,0,0] op_sel_hi:[0,1,1]
	v_pk_fma_f32 v[72:73], v[114:115], s[26:27], v[72:73] op_sel:[1,0,0] op_sel_hi:[0,1,1]
	v_pk_add_f32 v[114:115], v[74:75], v[82:83]
	v_pk_add_f32 v[74:75], v[74:75], v[82:83] neg_lo:[0,1] neg_hi:[0,1]
	v_pk_add_f32 v[82:83], v[116:117], v[124:125]
	v_pk_add_f32 v[116:117], v[116:117], v[124:125] neg_lo:[0,1] neg_hi:[0,1]
	v_pk_add_f32 v[124:125], v[114:115], v[82:83]
	v_pk_add_f32 v[82:83], v[114:115], v[82:83] neg_lo:[0,1] neg_hi:[0,1]
	v_pk_fma_f32 v[114:115], v[116:117], s[28:29], v[74:75] op_sel:[1,0,0] op_sel_hi:[0,1,1]
	v_pk_fma_f32 v[74:75], v[116:117], s[26:27], v[74:75] op_sel:[1,0,0] op_sel_hi:[0,1,1]
	s_waitcnt lgkmcnt(1)
	v_pk_add_f32 v[116:117], v[76:77], v[126:127]
	v_pk_add_f32 v[76:77], v[76:77], v[126:127] neg_lo:[0,1] neg_hi:[0,1]
	s_waitcnt lgkmcnt(0)
	v_pk_add_f32 v[126:127], v[118:119], v[130:131]
	v_pk_add_f32 v[118:119], v[118:119], v[130:131] neg_lo:[0,1] neg_hi:[0,1]
	v_pk_add_f32 v[130:131], v[116:117], v[126:127]
	v_pk_add_f32 v[116:117], v[116:117], v[126:127] neg_lo:[0,1] neg_hi:[0,1]
	v_pk_fma_f32 v[126:127], v[118:119], s[28:29], v[76:77] op_sel:[1,0,0] op_sel_hi:[0,1,1]
	v_pk_fma_f32 v[76:77], v[118:119], s[26:27], v[76:77] op_sel:[1,0,0] op_sel_hi:[0,1,1]
	v_pk_add_f32 v[118:119], v[78:79], v[128:129]
	v_pk_add_f32 v[78:79], v[78:79], v[128:129] neg_lo:[0,1] neg_hi:[0,1]
	v_pk_add_f32 v[128:129], v[120:121], v[132:133]
	v_pk_add_f32 v[120:121], v[120:121], v[132:133] neg_lo:[0,1] neg_hi:[0,1]
	v_pk_add_f32 v[132:133], v[118:119], v[128:129]
	v_pk_add_f32 v[118:119], v[118:119], v[128:129] neg_lo:[0,1] neg_hi:[0,1]
	v_pk_fma_f32 v[128:129], v[120:121], s[28:29], v[78:79] op_sel:[1,0,0] op_sel_hi:[0,1,1]
	v_pk_fma_f32 v[78:79], v[120:121], s[26:27], v[78:79] op_sel:[1,0,0] op_sel_hi:[0,1,1]
	v_pk_mul_f32 v[120:121], v[114:115], s[56:57] op_sel_hi:[0,1]
	v_pk_fma_f32 v[114:115], v[114:115], s[0:1], v[120:121] op_sel:[1,0,0]
	v_pk_mul_f32 v[120:121], v[126:127], s[12:13] op_sel_hi:[0,1]
	v_pk_fma_f32 v[120:121], v[126:127], s[58:59], v[120:121] op_sel:[1,0,0] op_sel_hi:[1,0,1]
	v_pk_mul_f32 v[126:127], v[128:129], s[8:9] op_sel_hi:[0,1]
	v_pk_fma_f32 v[126:127], v[128:129], s[34:35], v[126:127] op_sel:[1,0,0]
	v_pk_mul_f32 v[128:129], v[82:83], s[12:13] op_sel_hi:[0,1]
	v_pk_fma_f32 v[82:83], v[82:83], s[58:59], v[128:129] op_sel:[1,0,0] op_sel_hi:[1,0,1]
	v_pk_mul_f32 v[128:129], v[116:117], s[18:19] op_sel_hi:[0,1]
	v_pk_fma_f32 v[116:117], v[116:117], s[60:61], v[128:129] op_sel:[1,0,0]
	v_pk_mul_f32 v[128:129], v[74:75], s[8:9] op_sel_hi:[0,1]
	v_pk_fma_f32 v[74:75], v[74:75], s[34:35], v[128:129] op_sel:[1,0,0]
	v_pk_mul_f32 v[128:129], v[78:79], s[38:39] op_sel_hi:[0,1]
	v_mul_f32_e32 v86, 0xbf3504f3, v118
	v_pk_fma_f32 v[78:79], v[78:79], s[30:31], v[128:129] op_sel:[1,0,0]
	v_pk_add_f32 v[128:129], v[122:123], v[130:131]
	v_pk_add_f32 v[122:123], v[122:123], v[130:131] neg_lo:[0,1] neg_hi:[0,1]
	v_pk_add_f32 v[130:131], v[124:125], v[132:133]
	v_pk_add_f32 v[124:125], v[124:125], v[132:133] neg_lo:[0,1] neg_hi:[0,1]
	v_pk_fma_f32 v[118:119], v[118:119], s[12:13], v[86:87] op_sel:[1,0,0] op_sel_hi:[1,1,0]
	v_mul_f32_e32 v86, 0xbf3504f3, v76
	v_pk_add_f32 v[132:133], v[128:129], v[130:131]
	v_pk_add_f32 v[128:129], v[128:129], v[130:131] neg_lo:[0,1] neg_hi:[0,1]
	v_pk_fma_f32 v[130:131], v[124:125], s[28:29], v[122:123] op_sel:[1,0,0] op_sel_hi:[0,1,1]
	v_pk_fma_f32 v[122:123], v[124:125], s[26:27], v[122:123] op_sel:[1,0,0] op_sel_hi:[0,1,1]
	v_pk_add_f32 v[124:125], v[96:97], v[120:121]
	v_pk_add_f32 v[96:97], v[96:97], v[120:121] neg_lo:[0,1] neg_hi:[0,1]
	v_pk_add_f32 v[120:121], v[114:115], v[126:127]
	v_pk_add_f32 v[114:115], v[114:115], v[126:127] neg_lo:[0,1] neg_hi:[0,1]
	v_pk_fma_f32 v[76:77], v[76:77], s[12:13], v[86:87] op_sel:[1,0,0] op_sel_hi:[1,1,0]
	v_pk_add_f32 v[126:127], v[124:125], v[120:121]
	v_pk_add_f32 v[120:121], v[124:125], v[120:121] neg_lo:[0,1] neg_hi:[0,1]
	v_pk_fma_f32 v[124:125], v[114:115], s[28:29], v[96:97] op_sel:[1,0,0] op_sel_hi:[0,1,1]
	v_pk_fma_f32 v[96:97], v[114:115], s[26:27], v[96:97] op_sel:[1,0,0] op_sel_hi:[0,1,1]
	v_pk_add_f32 v[114:115], v[80:81], v[116:117]
	v_pk_add_f32 v[80:81], v[80:81], v[116:117] neg_lo:[0,1] neg_hi:[0,1]
	v_pk_add_f32 v[116:117], v[82:83], v[118:119]
	v_pk_add_f32 v[82:83], v[82:83], v[118:119] neg_lo:[0,1] neg_hi:[0,1]
	v_pk_add_f32 v[118:119], v[114:115], v[116:117]
	v_pk_add_f32 v[114:115], v[114:115], v[116:117] neg_lo:[0,1] neg_hi:[0,1]
	v_pk_fma_f32 v[116:117], v[82:83], s[28:29], v[80:81] op_sel:[1,0,0] op_sel_hi:[0,1,1]
	v_pk_fma_f32 v[80:81], v[82:83], s[26:27], v[80:81] op_sel:[1,0,0] op_sel_hi:[0,1,1]
	v_pk_add_f32 v[82:83], v[72:73], v[76:77]
	v_pk_add_f32 v[72:73], v[72:73], v[76:77] neg_lo:[0,1] neg_hi:[0,1]
	v_pk_add_f32 v[76:77], v[74:75], v[78:79]
	v_pk_add_f32 v[74:75], v[74:75], v[78:79] neg_lo:[0,1] neg_hi:[0,1]
	v_pk_add_f32 v[78:79], v[82:83], v[76:77]
	v_pk_add_f32 v[76:77], v[82:83], v[76:77] neg_lo:[0,1] neg_hi:[0,1]
	v_pk_fma_f32 v[82:83], v[74:75], s[28:29], v[72:73] op_sel:[1,0,0] op_sel_hi:[0,1,1]
	v_pk_fma_f32 v[72:73], v[74:75], s[26:27], v[72:73] op_sel:[1,0,0] op_sel_hi:[0,1,1]
	s_waitcnt vmcnt(15)
	v_lshlrev_b32_e32 v74, 16, v134
	v_and_b32_e32 v75, 0xffff0000, v134
	v_pk_mul_f32 v[134:135], v[74:75], s[28:29]
	v_pk_mul_f32 v[74:75], v[132:133], v[74:75] op_sel_hi:[0,1]
	v_pk_fma_f32 v[132:133], v[132:133], v[134:135], v[74:75] op_sel:[1,1,0] op_sel_hi:[1,0,1]
	s_waitcnt vmcnt(14)
	v_lshlrev_b32_e32 v74, 16, v136
	v_and_b32_e32 v75, 0xffff0000, v136
	v_pk_mul_f32 v[134:135], v[74:75], s[28:29]
	v_pk_mul_f32 v[74:75], v[126:127], v[74:75] op_sel_hi:[0,1]
	v_pk_fma_f32 v[126:127], v[126:127], v[134:135], v[74:75] op_sel:[1,1,0] op_sel_hi:[1,0,1]
	s_waitcnt vmcnt(13)
	v_lshlrev_b32_e32 v74, 16, v137
	v_and_b32_e32 v75, 0xffff0000, v137
	v_pk_mul_f32 v[134:135], v[74:75], s[28:29]
	v_pk_mul_f32 v[74:75], v[118:119], v[74:75] op_sel_hi:[0,1]
	v_pk_fma_f32 v[118:119], v[118:119], v[134:135], v[74:75] op_sel:[1,1,0] op_sel_hi:[1,0,1]
	s_waitcnt vmcnt(12)
	v_lshlrev_b32_e32 v74, 16, v138
	v_and_b32_e32 v75, 0xffff0000, v138
	v_pk_mul_f32 v[134:135], v[74:75], s[28:29]
	v_pk_mul_f32 v[74:75], v[78:79], v[74:75] op_sel_hi:[0,1]
	v_pk_fma_f32 v[78:79], v[78:79], v[134:135], v[74:75] op_sel:[1,1,0] op_sel_hi:[1,0,1]
	s_waitcnt vmcnt(11)
	v_lshlrev_b32_e32 v74, 16, v139
	v_and_b32_e32 v75, 0xffff0000, v139
	v_pk_mul_f32 v[134:135], v[74:75], s[28:29]
	v_pk_mul_f32 v[74:75], v[130:131], v[74:75] op_sel_hi:[0,1]
	v_pk_fma_f32 v[130:131], v[130:131], v[134:135], v[74:75] op_sel:[1,1,0] op_sel_hi:[1,0,1]
	s_waitcnt vmcnt(7)
	v_lshlrev_b32_e32 v74, 16, v143
	v_and_b32_e32 v75, 0xffff0000, v143
	v_pk_mul_f32 v[134:135], v[74:75], s[28:29]
	v_pk_mul_f32 v[74:75], v[124:125], v[74:75] op_sel_hi:[0,1]
	v_pk_fma_f32 v[124:125], v[124:125], v[134:135], v[74:75] op_sel:[1,1,0] op_sel_hi:[1,0,1]
	s_waitcnt vmcnt(6)
	v_lshlrev_b32_e32 v74, 16, v144
	v_and_b32_e32 v75, 0xffff0000, v144
	v_pk_mul_f32 v[134:135], v[74:75], s[28:29]
	v_pk_mul_f32 v[74:75], v[116:117], v[74:75] op_sel_hi:[0,1]
	v_pk_fma_f32 v[116:117], v[116:117], v[134:135], v[74:75] op_sel:[1,1,0] op_sel_hi:[1,0,1]
	s_waitcnt vmcnt(5)
	v_lshlrev_b32_e32 v74, 16, v145
	v_and_b32_e32 v75, 0xffff0000, v145
	v_pk_mul_f32 v[134:135], v[74:75], s[28:29]
	v_pk_mul_f32 v[74:75], v[82:83], v[74:75] op_sel_hi:[0,1]
	v_pk_fma_f32 v[82:83], v[82:83], v[134:135], v[74:75] op_sel:[1,1,0] op_sel_hi:[1,0,1]
	s_waitcnt vmcnt(4)
	v_lshlrev_b32_e32 v74, 16, v146
	v_and_b32_e32 v75, 0xffff0000, v146
	v_pk_mul_f32 v[134:135], v[74:75], s[28:29]
	v_pk_mul_f32 v[74:75], v[128:129], v[74:75] op_sel_hi:[0,1]
	v_pk_fma_f32 v[128:129], v[128:129], v[134:135], v[74:75] op_sel:[1,1,0] op_sel_hi:[1,0,1]
	v_lshlrev_b32_e32 v74, 16, v140
	v_and_b32_e32 v75, 0xffff0000, v140
	v_pk_mul_f32 v[134:135], v[74:75], s[28:29]
	v_pk_mul_f32 v[74:75], v[120:121], v[74:75] op_sel_hi:[0,1]
	v_pk_fma_f32 v[120:121], v[120:121], v[134:135], v[74:75] op_sel:[1,1,0] op_sel_hi:[1,0,1]
	v_lshlrev_b32_e32 v74, 16, v141
	v_and_b32_e32 v75, 0xffff0000, v141
	v_pk_mul_f32 v[134:135], v[74:75], s[28:29]
	v_pk_mul_f32 v[74:75], v[114:115], v[74:75] op_sel_hi:[0,1]
	v_pk_fma_f32 v[114:115], v[114:115], v[134:135], v[74:75] op_sel:[1,1,0] op_sel_hi:[1,0,1]
	v_lshlrev_b32_e32 v74, 16, v142
	v_and_b32_e32 v75, 0xffff0000, v142
	v_pk_mul_f32 v[134:135], v[74:75], s[28:29]
	v_pk_mul_f32 v[74:75], v[76:77], v[74:75] op_sel_hi:[0,1]
	v_pk_fma_f32 v[76:77], v[76:77], v[134:135], v[74:75] op_sel:[1,1,0] op_sel_hi:[1,0,1]
	s_waitcnt vmcnt(3)
	v_lshlrev_b32_e32 v74, 16, v147
	v_and_b32_e32 v75, 0xffff0000, v147
	v_pk_mul_f32 v[134:135], v[74:75], s[28:29]
	v_pk_mul_f32 v[74:75], v[122:123], v[74:75] op_sel_hi:[0,1]
	v_pk_fma_f32 v[122:123], v[122:123], v[134:135], v[74:75] op_sel:[1,1,0] op_sel_hi:[1,0,1]
	s_waitcnt vmcnt(2)
	v_lshlrev_b32_e32 v74, 16, v148
	v_and_b32_e32 v75, 0xffff0000, v148
	v_pk_mul_f32 v[134:135], v[74:75], s[28:29]
	v_pk_mul_f32 v[74:75], v[96:97], v[74:75] op_sel_hi:[0,1]
	v_pk_fma_f32 v[134:135], v[96:97], v[134:135], v[74:75] op_sel:[1,1,0] op_sel_hi:[1,0,1]
	s_waitcnt vmcnt(1)
	v_lshlrev_b32_e32 v74, 16, v149
	v_and_b32_e32 v75, 0xffff0000, v149
	v_pk_mul_f32 v[96:97], v[74:75], s[28:29]
	v_pk_mul_f32 v[74:75], v[80:81], v[74:75] op_sel_hi:[0,1]
	v_pk_fma_f32 v[80:81], v[80:81], v[96:97], v[74:75] op_sel:[1,1,0] op_sel_hi:[1,0,1]
	s_waitcnt vmcnt(0)
	v_lshlrev_b32_e32 v74, 16, v150
	v_and_b32_e32 v75, 0xffff0000, v150
	v_pk_add_f32 v[138:139], v[132:133], v[128:129]
	v_pk_add_f32 v[128:129], v[132:133], v[128:129] neg_lo:[0,1] neg_hi:[0,1]
	v_pk_add_f32 v[132:133], v[130:131], v[122:123]
	v_pk_add_f32 v[122:123], v[130:131], v[122:123] neg_lo:[0,1] neg_hi:[0,1]
	v_pk_mul_f32 v[96:97], v[74:75], s[28:29]
	v_pk_mul_f32 v[74:75], v[72:73], v[74:75] op_sel_hi:[0,1]
	v_pk_add_f32 v[130:131], v[138:139], v[132:133]
	v_pk_add_f32 v[132:133], v[138:139], v[132:133] neg_lo:[0,1] neg_hi:[0,1]
	v_pk_fma_f32 v[138:139], v[122:123], s[26:27], v[128:129] op_sel:[1,0,0] op_sel_hi:[0,1,1]
	v_pk_fma_f32 v[122:123], v[122:123], s[28:29], v[128:129] op_sel:[1,0,0] op_sel_hi:[0,1,1]
	v_pk_add_f32 v[128:129], v[126:127], v[120:121]
	v_pk_add_f32 v[120:121], v[126:127], v[120:121] neg_lo:[0,1] neg_hi:[0,1]
	v_pk_add_f32 v[126:127], v[124:125], v[134:135]
	v_pk_add_f32 v[124:125], v[124:125], v[134:135] neg_lo:[0,1] neg_hi:[0,1]
	v_pk_fma_f32 v[136:137], v[72:73], v[96:97], v[74:75] op_sel:[1,1,0] op_sel_hi:[1,0,1]
	v_pk_add_f32 v[134:135], v[128:129], v[126:127]
	v_pk_add_f32 v[126:127], v[128:129], v[126:127] neg_lo:[0,1] neg_hi:[0,1]
	v_pk_fma_f32 v[128:129], v[124:125], s[26:27], v[120:121] op_sel:[1,0,0] op_sel_hi:[0,1,1]
	v_pk_fma_f32 v[120:121], v[124:125], s[28:29], v[120:121] op_sel:[1,0,0] op_sel_hi:[0,1,1]
	v_pk_add_f32 v[124:125], v[118:119], v[114:115]
	v_pk_add_f32 v[114:115], v[118:119], v[114:115] neg_lo:[0,1] neg_hi:[0,1]
	v_pk_add_f32 v[118:119], v[116:117], v[80:81]
	v_pk_add_f32 v[80:81], v[116:117], v[80:81] neg_lo:[0,1] neg_hi:[0,1]
	v_pk_add_f32 v[116:117], v[124:125], v[118:119]
	v_pk_add_f32 v[118:119], v[124:125], v[118:119] neg_lo:[0,1] neg_hi:[0,1]
	v_pk_fma_f32 v[124:125], v[80:81], s[26:27], v[114:115] op_sel:[1,0,0] op_sel_hi:[0,1,1]
	v_pk_fma_f32 v[80:81], v[80:81], s[28:29], v[114:115] op_sel:[1,0,0] op_sel_hi:[0,1,1]
	v_pk_add_f32 v[114:115], v[78:79], v[76:77]
	v_pk_add_f32 v[76:77], v[78:79], v[76:77] neg_lo:[0,1] neg_hi:[0,1]
	v_pk_add_f32 v[78:79], v[82:83], v[136:137]
	v_pk_add_f32 v[82:83], v[82:83], v[136:137] neg_lo:[0,1] neg_hi:[0,1]
	v_pk_add_f32 v[136:137], v[114:115], v[78:79]
	v_pk_add_f32 v[78:79], v[114:115], v[78:79] neg_lo:[0,1] neg_hi:[0,1]
	v_pk_fma_f32 v[114:115], v[82:83], s[26:27], v[76:77] op_sel:[1,0,0] op_sel_hi:[0,1,1]
	v_pk_fma_f32 v[76:77], v[82:83], s[28:29], v[76:77] op_sel:[1,0,0] op_sel_hi:[0,1,1]
	v_pk_mul_f32 v[82:83], v[128:129], s[34:35] op_sel_hi:[0,1]
	s_mov_b32 s31, s34
	v_pk_fma_f32 v[82:83], v[128:129], s[30:31], v[82:83] op_sel:[1,0,0]
	v_pk_mul_f32 v[128:129], v[114:115], s[0:1] op_sel_hi:[0,1]
	s_mov_b32 s19, s27
	v_pk_fma_f32 v[114:115], v[114:115], s[38:39], v[128:129] op_sel:[1,0,0]
	v_pk_mul_f32 v[128:129], v[118:119], s[18:19] op_sel_hi:[0,1]
	s_mov_b32 s12, s26
	s_mov_b32 s13, s18
	v_pk_fma_f32 v[118:119], v[118:119], s[12:13], v[128:129] op_sel:[1,0,0]
	v_pk_mul_f32 v[128:129], v[78:79], s[36:37] op_sel_hi:[0,1]
	v_pk_fma_f32 v[78:79], v[78:79], s[36:37], v[128:129] op_sel:[1,0,0] op_sel_hi:[1,0,1]
	v_pk_mul_f32 v[128:129], v[120:121], s[0:1] op_sel_hi:[0,1]
	v_pk_fma_f32 v[120:121], v[120:121], s[38:39], v[128:129] op_sel:[1,0,0]
	v_pk_mul_f32 v[128:129], v[80:81], s[36:37] op_sel_hi:[0,1]
	s_mov_b32 s39, s30
	v_mul_f32_e32 v86, 0x3f3504f3, v124
	v_pk_fma_f32 v[80:81], v[80:81], s[36:37], v[128:129] op_sel:[1,0,0] op_sel_hi:[1,0,1]
	v_pk_mul_f32 v[128:129], v[76:77], s[38:39] op_sel_hi:[0,1]
	v_pk_fma_f32 v[124:125], v[124:125], s[36:37], v[86:87] op_sel:[1,0,0] op_sel_hi:[1,1,0]
	v_mul_f32_e32 v86, 0x3f3504f3, v126
	v_pk_fma_f32 v[76:77], v[76:77], s[8:9], v[128:129] op_sel:[1,0,0]
	v_pk_add_f32 v[128:129], v[130:131], v[116:117]
	v_pk_add_f32 v[116:117], v[130:131], v[116:117] neg_lo:[0,1] neg_hi:[0,1]
	v_pk_add_f32 v[130:131], v[134:135], v[136:137]
	v_pk_add_f32 v[134:135], v[134:135], v[136:137] neg_lo:[0,1] neg_hi:[0,1]
	v_pk_fma_f32 v[126:127], v[126:127], s[36:37], v[86:87] op_sel:[1,0,0] op_sel_hi:[1,1,0]
	v_pk_add_f32 v[136:137], v[128:129], v[130:131]
	v_pk_add_f32 v[128:129], v[128:129], v[130:131] neg_lo:[0,1] neg_hi:[0,1]
	v_pk_fma_f32 v[130:131], v[134:135], s[26:27], v[116:117] op_sel:[1,0,0] op_sel_hi:[0,1,1]
	v_pk_fma_f32 v[116:117], v[134:135], s[28:29], v[116:117] op_sel:[1,0,0] op_sel_hi:[0,1,1]
	v_pk_add_f32 v[134:135], v[138:139], v[124:125]
	v_pk_add_f32 v[124:125], v[138:139], v[124:125] neg_lo:[0,1] neg_hi:[0,1]
	v_pk_add_f32 v[138:139], v[82:83], v[114:115]
	v_pk_add_f32 v[82:83], v[82:83], v[114:115] neg_lo:[0,1] neg_hi:[0,1]
	v_pk_add_f32 v[114:115], v[134:135], v[138:139]
	v_pk_add_f32 v[134:135], v[134:135], v[138:139] neg_lo:[0,1] neg_hi:[0,1]
	v_pk_fma_f32 v[138:139], v[82:83], s[26:27], v[124:125] op_sel:[1,0,0] op_sel_hi:[0,1,1]
	v_pk_fma_f32 v[82:83], v[82:83], s[28:29], v[124:125] op_sel:[1,0,0] op_sel_hi:[0,1,1]
	v_pk_add_f32 v[124:125], v[132:133], v[118:119]
	v_pk_add_f32 v[118:119], v[132:133], v[118:119] neg_lo:[0,1] neg_hi:[0,1]
	v_pk_add_f32 v[132:133], v[126:127], v[78:79]
	v_pk_add_f32 v[78:79], v[126:127], v[78:79] neg_lo:[0,1] neg_hi:[0,1]
	v_mov_b32_e32 v96, v217
	v_mov_b32_e32 v72, v218
	v_mov_b32_e32 v74, v215
	v_mov_b32_e32 v97, v220
	v_mov_b32_e32 v73, v221
	v_pk_add_f32 v[126:127], v[124:125], v[132:133]
	v_pk_add_f32 v[124:125], v[124:125], v[132:133] neg_lo:[0,1] neg_hi:[0,1]
	v_pk_fma_f32 v[132:133], v[78:79], s[26:27], v[118:119] op_sel:[1,0,0] op_sel_hi:[0,1,1]
	v_pk_fma_f32 v[78:79], v[78:79], s[28:29], v[118:119] op_sel:[1,0,0] op_sel_hi:[0,1,1]
	v_pk_add_f32 v[118:119], v[122:123], v[80:81]
	v_pk_add_f32 v[80:81], v[122:123], v[80:81] neg_lo:[0,1] neg_hi:[0,1]
	v_pk_add_f32 v[122:123], v[120:121], v[76:77]
	v_pk_add_f32 v[76:77], v[120:121], v[76:77] neg_lo:[0,1] neg_hi:[0,1]
	v_pk_add_f32 v[120:121], v[118:119], v[122:123]
	v_pk_add_f32 v[118:119], v[118:119], v[122:123] neg_lo:[0,1] neg_hi:[0,1]
	v_pk_fma_f32 v[122:123], v[76:77], s[26:27], v[80:81] op_sel:[1,0,0] op_sel_hi:[0,1,1]
	v_pk_fma_f32 v[76:77], v[76:77], s[28:29], v[80:81] op_sel:[1,0,0] op_sel_hi:[0,1,1]
	v_lshlrev_b32_e32 v75, 3, v74
	v_lshlrev_b32_e32 v80, 7, v74
	v_add3_u32 v80, v219, v75, v80
	ds_write2_b64 v80, v[136:137], v[114:115] offset1:1
	ds_write2_b64 v80, v[126:127], v[120:121] offset0:2 offset1:3
	ds_write2_b64 v80, v[130:131], v[138:139] offset0:4 offset1:5
	ds_write2_b64 v80, v[132:133], v[122:123] offset0:6 offset1:7
	ds_write2_b64 v80, v[128:129], v[134:135] offset0:8 offset1:9
	ds_write2_b64 v80, v[124:125], v[118:119] offset0:10 offset1:11
	ds_write2_b64 v80, v[116:117], v[82:83] offset0:12 offset1:13
	ds_write2_b64 v80, v[78:79], v[76:77] offset0:14 offset1:15
	v_cndmask_b32_e64 v76, v211, v212, s[6:7]
	v_mul_f32_e32 v77, v76, v56
	v_mul_f32_e32 v60, v76, v60
	v_mov_b32_e32 v56, v87
	v_cvt_pk_fp8_f32 v56, v77, v60
	v_mul_f32_e32 v60, v76, v57
	v_mul_f32_e32 v61, v76, v61
	v_mov_b32_e32 v57, v87
	v_cvt_pk_fp8_f32 v57, v60, v61
	v_mul_f32_e32 v60, v76, v65
	v_mul_f32_e32 v61, v76, v69
	v_mul_f32_e32 v44, v76, v44
	v_cvt_pk_fp8_f32 v57, v60, v61 op_sel:[0,0,1]
	v_mul_f32_e32 v60, v76, v58
	v_mul_f32_e32 v61, v76, v62
	v_mov_b32_e32 v58, v87
	v_cvt_pk_fp8_f32 v58, v60, v61
	v_mul_f32_e32 v60, v76, v59
	v_mul_f32_e32 v61, v76, v63
	v_mov_b32_e32 v59, v87
	v_cvt_pk_fp8_f32 v59, v60, v61
	v_mul_f32_e32 v60, v76, v67
	v_mul_f32_e32 v61, v76, v71
	v_mul_f32_e32 v45, v76, v45
	v_cvt_pk_fp8_f32 v59, v60, v61 op_sel:[0,0,1]
	v_mul_f32_e32 v60, v76, v40
	v_mov_b32_e32 v40, v87
	v_cvt_pk_fp8_f32 v40, v60, v44
	v_mul_f32_e32 v44, v76, v41
	v_mov_b32_e32 v41, v87
	v_cvt_pk_fp8_f32 v41, v44, v45
	v_mul_f32_e32 v44, v76, v49
	v_mul_f32_e32 v45, v76, v53
	s_min_i32 s0, s78, s59
	v_cvt_pk_fp8_f32 v41, v44, v45 op_sel:[0,0,1]
	v_mul_f32_e32 v44, v76, v42
	v_mul_f32_e32 v45, v76, v46
	v_mov_b32_e32 v42, v87
	s_mul_i32 s0, s0, s3
	v_cvt_pk_fp8_f32 v42, v44, v45
	v_mul_f32_e32 v44, v76, v43
	v_mul_f32_e32 v45, v76, v47
	v_mov_b32_e32 v43, v87
	s_add_i32 s1, s0, s2
	v_cvt_pk_fp8_f32 v43, v44, v45
	s_mul_hi_i32 s0, s1, 0x2aaaaaab
	v_mul_f32_e32 v64, v76, v64
	v_mul_f32_e32 v68, v76, v68
	s_lshr_b32 s6, s0, 31
	s_ashr_i32 s0, s0, 7
	v_cvt_pk_fp8_f32 v56, v64, v68 op_sel:[0,0,1]
	v_mul_f32_e32 v62, v76, v66
	v_mul_f32_e32 v64, v76, v70
	v_mul_f32_e32 v48, v76, v48
	v_mul_f32_e32 v52, v76, v52
	s_add_i32 s6, s0, s6
	v_cvt_pk_fp8_f32 v58, v62, v64 op_sel:[0,0,1]
	v_cvt_pk_fp8_f32 v40, v48, v52 op_sel:[0,0,1]
	v_mul_f32_e32 v46, v76, v50
	v_mul_f32_e32 v48, v76, v54
	v_mul_f32_e32 v44, v76, v51
	v_mul_f32_e32 v45, v76, v55
	s_add_i32 s0, s6, 11
	s_mulk_i32 s6, 0x300
	v_cvt_pk_fp8_f32 v42, v46, v48 op_sel:[0,0,1]
	v_cvt_pk_fp8_f32 v43, v44, v45 op_sel:[0,0,1]
	s_sub_i32 s19, s1, s6
	s_cmpk_lt_i32 s19, 0x200
	s_cselect_b64 s[6:7], -1, 0
	s_cmpk_gt_i32 s19, 0x1ff
	s_mov_b64 s[56:57], -1
	s_waitcnt lgkmcnt(0)
	s_barrier
	ds_write_b128 v236, v[56:59]
	ds_write_b128 v237, v[40:43]
	s_cbranch_scc0 .LBB0_869
	s_load_dwordx2 s[8:9], s[14:15], 0x110
	s_ashr_i32 s1, s0, 31
	s_lshl_b64 s[56:57], s[0:1], 24
	s_mov_b32 s13, s18
	s_waitcnt lgkmcnt(0)
	s_add_u32 s8, s8, s56
	s_addc_u32 s9, s9, s57
	s_lshl_b32 s1, s19, 3
	s_and_b32 s1, s1, 0x7fffffc0
	s_add_i32 s12, s1, 0xfffff000
	s_mov_b64 s[56:57], 0

.LBB0_871:
	s_lshl_b64 s[12:13], s[12:13], 13
	s_add_u32 s0, s8, s12
	s_addc_u32 s9, s9, s13
	s_lshl_b32 s1, s19, s1
	s_and_b32 s1, s1, 0x700
	s_lshl_b32 s1, s1, 2
	s_add_u32 s8, s0, s1
	s_addc_u32 s9, s9, 0
	s_cmp_gt_i32 s78, s59
	s_cselect_b64 s[0:1], -1, 0
	v_cndmask_b32_e64 v40, v180, 0, s[0:1]
	s_and_b64 s[12:13], s[0:1], exec
	s_cselect_b32 s12, 0, 0x800
	v_lshlrev_b32_e32 v86, 2, v40
	v_lshl_add_u64 v[48:49], s[8:9], 0, v[86:87]
	v_mad_i64_i32 v[40:41], s[8:9], s12, v181, 0
	v_mad_i64_i32 v[42:43], s[8:9], s12, v182, 0
	v_lshl_add_u64 v[40:41], v[40:41], 2, v[48:49]
	v_lshl_add_u64 v[42:43], v[42:43], 2, v[48:49]
	global_load_dwordx4 v[56:59], v[40:41], off nt
	global_load_dwordx4 v[60:63], v[42:43], off nt
	v_mad_i64_i32 v[40:41], s[8:9], s12, v183, 0
	v_mad_i64_i32 v[42:43], s[8:9], s12, v184, 0
	v_lshl_add_u64 v[40:41], v[40:41], 2, v[48:49]
	v_lshl_add_u64 v[42:43], v[42:43], 2, v[48:49]
	global_load_dwordx4 v[64:67], v[40:41], off nt
	global_load_dwordx4 v[68:71], v[42:43], off nt
	v_mad_i64_i32 v[40:41], s[8:9], s12, v185, 0
	v_mad_i64_i32 v[42:43], s[8:9], s12, v186, 0
	v_mad_i64_i32 v[50:51], s[8:9], s12, v187, 0
	v_mad_i64_i32 v[52:53], s[8:9], s12, v188, 0
	v_lshl_add_u64 v[40:41], v[40:41], 2, v[48:49]
	v_lshl_add_u64 v[44:45], v[42:43], 2, v[48:49]
	v_lshl_add_u64 v[50:51], v[50:51], 2, v[48:49]
	v_lshl_add_u64 v[52:53], v[52:53], 2, v[48:49]
	global_load_dwordx4 v[40:43], v[40:41], off nt
	s_nop 0
	global_load_dwordx4 v[44:47], v[44:45], off nt
	s_nop 0
	global_load_dwordx4 v[48:51], v[50:51], off nt
	s_nop 0
	global_load_dwordx4 v[52:55], v[52:53], off nt
	s_cmp_gt_i32 s62, -2
	s_cselect_b32 s8, s76, 0
	s_min_i32 s8, s8, s59
	s_mul_i32 s8, s8, s3
	s_add_i32 s9, s8, s2
	s_mul_hi_i32 s8, s9, 0x2aaaaaab
	s_lshr_b32 s12, s8, 31
	s_ashr_i32 s8, s8, 7
	s_add_i32 s12, s8, s12
	s_add_i32 s8, s12, 11
	s_mulk_i32 s12, 0x300
	s_sub_i32 s19, s9, s12
	s_ashr_i32 s9, s8, 31
	s_cmpk_gt_i32 s19, 0x1ff
	s_mov_b64 s[56:57], -1
	s_cbranch_scc0 .LBB0_873
	s_lshl_b32 s12, s19, 3
	s_and_b32 s31, s12, 0x7fffffc0
	s_lshl_b32 s12, s19, 19
	s_and_b32 s39, s12, 0x380000
	s_lshl_b64 s[12:13], s[8:9], 22
	s_add_u32 s12, s16, s12
	s_addc_u32 s13, s17, s13
	s_add_u32 s12, s12, s39
	s_addc_u32 s13, s13, 0
	s_add_u32 s12, s12, s31
	s_addc_u32 s13, s13, 0
	s_add_u32 s12, s12, 0x24dff000
	s_addc_u32 s13, s13, 0
	s_mov_b64 s[56:57], 0

.LBB0_875:
	s_add_i32 s58, s62, 5
	s_cmp_lt_i32 s62, -1
	s_cselect_b64 s[8:9], -1, 0
	s_or_b64 s[8:9], s[8:9], s[54:55]
	s_and_b64 s[8:9], s[8:9], exec
	s_cselect_b32 s8, s65, s12
	s_cselect_b32 s12, 0x80, s31
	v_mul_i32_i24_e32 v76, s12, v191
	v_or_b32_e32 v76, v76, v189
	v_ashrrev_i32_e32 v77, 31, v76
	s_cselect_b32 s9, s66, s13
	v_lshlrev_b64 v[76:77], 11, v[76:77]
	v_lshl_add_u64 v[76:77], s[8:9], 0, v[76:77]
	v_lshl_add_u64 v[114:115], v[76:77], 0, v[88:89]
	ds_read_b32 v76, v235
	ds_read_b32 v77, v235 offset:1040
	ds_read_b32 v78, v235 offset:2080
	ds_read_b32 v79, v235 offset:3120
	ds_read_b32 v80, v238
	ds_read_b32 v81, v238 offset:1040
	ds_read_b32 v82, v238 offset:2080
	ds_read_b32 v83, v238 offset:3120
	s_waitcnt lgkmcnt(4)
	global_store_dwordx4 v[114:115], v[76:79], off nt
	v_pk_mul_f32 v[72:73], v[72:73], s[28:29]
	s_mov_b32 s31, s34
	v_mul_i32_i24_e32 v76, s12, v201
	v_or_b32_e32 v76, v76, v189
	v_ashrrev_i32_e32 v77, 31, v76
	v_lshlrev_b64 v[76:77], 11, v[76:77]
	v_lshl_add_u64 v[76:77], s[8:9], 0, v[76:77]
	v_lshl_add_u64 v[76:77], v[76:77], 0, v[88:89]
	s_waitcnt lgkmcnt(0)
	global_store_dwordx4 v[76:77], v[80:83], off nt
	v_ashrrev_i32_e32 v76, 4, v74
	v_lshlrev_b32_e32 v77, 8, v76
	v_pk_mul_f32 v[140:141], v[72:73], s[28:29]
	v_pk_mul_f32 v[142:143], v[72:73], v[72:73] op_sel_hi:[1,0]
	v_ashrrev_i32_e32 v77, 1, v77
	v_pk_fma_f32 v[142:143], v[72:73], v[140:141], v[142:143] op_sel:[1,1,0] op_sel_hi:[1,0,1]
	v_lshlrev_b32_e32 v79, 11, v76
	v_and_b32_e32 v80, 0x78, v75
	v_add_u32_e32 v77, v219, v77
	v_pk_mul_f32 v[146:147], v[142:143], s[28:29]
	v_pk_mul_f32 v[148:149], v[142:143], v[142:143] op_sel_hi:[1,0]
	v_lshl_add_u32 v78, v76, 7, v219
	v_add3_u32 v77, v77, v79, v80
	v_pk_fma_f32 v[148:149], v[142:143], v[146:147], v[148:149] op_sel:[1,1,0] op_sel_hi:[1,0,1]
	v_add3_u32 v164, v78, v79, v80
	ds_read2_b64 v[78:81], v77 offset0:17 offset1:34
	ds_read2_b64 v[114:117], v77 offset0:51 offset1:68
	ds_read2_b64 v[118:121], v77 offset0:85 offset1:102
	ds_read2_b64 v[122:125], v77 offset0:119 offset1:136
	ds_read2_b64 v[126:129], v77 offset0:153 offset1:170
	ds_read2_b64 v[130:133], v77 offset0:187 offset1:204
	ds_read2_b64 v[134:137], v77 offset0:221 offset1:238
	ds_read_b64 v[82:83], v164
	ds_read_b64 v[138:139], v77 offset:2040
	v_pk_mul_f32 v[144:145], v[72:73], v[142:143] op_sel_hi:[1,0]
	v_pk_mul_f32 v[150:151], v[72:73], v[148:149] op_sel_hi:[1,0]
	s_waitcnt lgkmcnt(8)
	v_pk_mul_f32 v[162:163], v[72:73], v[78:79] op_sel_hi:[1,0]
	v_pk_fma_f32 v[144:145], v[142:143], v[140:141], v[144:145] op_sel:[1,1,0] op_sel_hi:[1,0,1]
	v_pk_fma_f32 v[150:151], v[148:149], v[140:141], v[150:151] op_sel:[1,1,0] op_sel_hi:[1,0,1]
	v_pk_fma_f32 v[78:79], v[78:79], v[140:141], v[162:163] op_sel:[1,1,0] op_sel_hi:[1,0,1]
	v_pk_mul_f32 v[140:141], v[142:143], v[80:81] op_sel_hi:[1,0]
	v_pk_mul_f32 v[154:155], v[144:145], s[28:29]
	v_pk_fma_f32 v[80:81], v[80:81], v[146:147], v[140:141] op_sel:[1,1,0] op_sel_hi:[1,0,1]
	s_waitcnt lgkmcnt(7)
	v_pk_mul_f32 v[140:141], v[144:145], v[114:115] op_sel_hi:[1,0]
	v_pk_mul_f32 v[152:153], v[142:143], v[148:149] op_sel_hi:[1,0]
	v_pk_mul_f32 v[158:159], v[148:149], s[28:29]
	v_pk_fma_f32 v[114:115], v[114:115], v[154:155], v[140:141] op_sel:[1,1,0] op_sel_hi:[1,0,1]
	v_pk_mul_f32 v[140:141], v[148:149], v[116:117] op_sel_hi:[1,0]
	v_pk_fma_f32 v[152:153], v[148:149], v[146:147], v[152:153] op_sel:[1,1,0] op_sel_hi:[1,0,1]
	v_pk_mul_f32 v[156:157], v[144:145], v[148:149] op_sel_hi:[1,0]
	v_pk_fma_f32 v[116:117], v[116:117], v[158:159], v[140:141] op_sel:[1,1,0] op_sel_hi:[1,0,1]
	v_pk_mul_f32 v[140:141], v[150:151], s[28:29]
	s_waitcnt lgkmcnt(6)
	v_pk_mul_f32 v[146:147], v[150:151], v[118:119] op_sel_hi:[1,0]
	v_pk_fma_f32 v[156:157], v[148:149], v[154:155], v[156:157] op_sel:[1,1,0] op_sel_hi:[1,0,1]
	v_pk_mul_f32 v[160:161], v[148:149], v[148:149] op_sel_hi:[1,0]
	v_pk_fma_f32 v[118:119], v[118:119], v[140:141], v[146:147] op_sel:[1,1,0] op_sel_hi:[1,0,1]
	v_pk_mul_f32 v[140:141], v[152:153], s[28:29]
	v_pk_mul_f32 v[146:147], v[152:153], v[120:121] op_sel_hi:[1,0]
	v_pk_fma_f32 v[160:161], v[148:149], v[158:159], v[160:161] op_sel:[1,1,0] op_sel_hi:[1,0,1]
	v_pk_fma_f32 v[120:121], v[120:121], v[140:141], v[146:147] op_sel:[1,1,0] op_sel_hi:[1,0,1]
	v_pk_mul_f32 v[140:141], v[156:157], s[28:29]
	s_waitcnt lgkmcnt(5)
	v_pk_mul_f32 v[146:147], v[156:157], v[122:123] op_sel_hi:[1,0]
	s_mov_b32 s8, s35
	v_pk_fma_f32 v[122:123], v[122:123], v[140:141], v[146:147] op_sel:[1,1,0] op_sel_hi:[1,0,1]
	v_pk_mul_f32 v[140:141], v[160:161], s[28:29]
	v_pk_mul_f32 v[146:147], v[160:161], v[124:125] op_sel_hi:[1,0]
	s_mov_b32 s9, s34
	v_pk_fma_f32 v[124:125], v[124:125], v[140:141], v[146:147] op_sel:[1,1,0] op_sel_hi:[1,0,1]
	v_pk_mul_f32 v[146:147], v[72:73], v[160:161] op_sel_hi:[0,1]
	v_pk_fma_f32 v[72:73], v[72:73], v[140:141], v[146:147] op_sel:[1,1,0] op_sel_hi:[1,0,1]
	s_mov_b32 s39, s35
	v_pk_mul_f32 v[146:147], v[72:73], s[28:29]
	s_waitcnt lgkmcnt(4)
	v_pk_mul_f32 v[72:73], v[72:73], v[126:127] op_sel_hi:[1,0]
	s_mov_b32 s19, s27
	v_pk_fma_f32 v[72:73], v[126:127], v[146:147], v[72:73] op_sel:[1,1,0] op_sel_hi:[1,0,1]
	v_pk_mul_f32 v[126:127], v[142:143], v[160:161] op_sel_hi:[0,1]
	v_pk_fma_f32 v[126:127], v[142:143], v[140:141], v[126:127] op_sel:[1,1,0] op_sel_hi:[1,0,1]
	s_mov_b32 s12, s26
	v_pk_mul_f32 v[142:143], v[126:127], s[28:29]
	v_pk_mul_f32 v[126:127], v[126:127], v[128:129] op_sel_hi:[1,0]
	s_mov_b32 s13, s18
	v_pk_fma_f32 v[126:127], v[128:129], v[142:143], v[126:127] op_sel:[1,1,0] op_sel_hi:[1,0,1]
	v_pk_mul_f32 v[128:129], v[144:145], v[160:161] op_sel_hi:[0,1]
	v_pk_fma_f32 v[128:129], v[144:145], v[140:141], v[128:129] op_sel:[1,1,0] op_sel_hi:[1,0,1]
	s_mov_b64 s[56:57], -1
	v_pk_mul_f32 v[142:143], v[128:129], s[28:29]
	s_waitcnt lgkmcnt(3)
	v_pk_mul_f32 v[128:129], v[128:129], v[130:131] op_sel_hi:[1,0]
	s_nop 0
	v_pk_fma_f32 v[128:129], v[130:131], v[142:143], v[128:129] op_sel:[1,1,0] op_sel_hi:[1,0,1]
	v_pk_mul_f32 v[130:131], v[148:149], v[160:161] op_sel_hi:[0,1]
	v_pk_fma_f32 v[130:131], v[148:149], v[140:141], v[130:131] op_sel:[1,1,0] op_sel_hi:[1,0,1]
	s_nop 0
	v_pk_mul_f32 v[142:143], v[130:131], s[28:29]
	v_pk_mul_f32 v[130:131], v[130:131], v[132:133] op_sel_hi:[1,0]
	s_nop 0
	v_pk_fma_f32 v[130:131], v[132:133], v[142:143], v[130:131] op_sel:[1,1,0] op_sel_hi:[1,0,1]
	v_pk_mul_f32 v[132:133], v[160:161], v[150:151] op_sel_hi:[1,0]
	s_nop 0
	v_pk_fma_f32 v[132:133], v[150:151], v[140:141], v[132:133] op_sel:[1,1,0] op_sel_hi:[1,0,1]
	s_nop 0
	v_pk_mul_f32 v[142:143], v[132:133], s[28:29]
	s_waitcnt lgkmcnt(2)
	v_pk_mul_f32 v[132:133], v[132:133], v[134:135] op_sel_hi:[1,0]
	s_nop 0
	v_pk_fma_f32 v[132:133], v[134:135], v[142:143], v[132:133] op_sel:[1,1,0] op_sel_hi:[1,0,1]
	v_pk_mul_f32 v[134:135], v[160:161], v[152:153] op_sel_hi:[1,0]
	s_nop 0
	v_pk_fma_f32 v[134:135], v[152:153], v[140:141], v[134:135] op_sel:[1,1,0] op_sel_hi:[1,0,1]
	s_nop 0
	v_pk_mul_f32 v[142:143], v[134:135], s[28:29]
	v_pk_mul_f32 v[134:135], v[134:135], v[136:137] op_sel_hi:[1,0]
	s_nop 0
	v_pk_fma_f32 v[134:135], v[136:137], v[142:143], v[134:135] op_sel:[1,1,0] op_sel_hi:[1,0,1]
	v_pk_mul_f32 v[136:137], v[160:161], v[156:157] op_sel_hi:[1,0]
	s_nop 0
	v_pk_fma_f32 v[136:137], v[156:157], v[140:141], v[136:137] op_sel:[1,1,0] op_sel_hi:[1,0,1]
	s_nop 0
	v_pk_mul_f32 v[140:141], v[136:137], s[28:29]
	s_waitcnt lgkmcnt(0)
	v_pk_mul_f32 v[136:137], v[136:137], v[138:139] op_sel_hi:[1,0]
	s_nop 0
	v_pk_fma_f32 v[136:137], v[138:139], v[140:141], v[136:137] op_sel:[1,1,0] op_sel_hi:[1,0,1]
	v_pk_add_f32 v[138:139], v[82:83], v[124:125]
	v_pk_add_f32 v[82:83], v[82:83], v[124:125] neg_lo:[0,1] neg_hi:[0,1]
	v_pk_add_f32 v[124:125], v[116:117], v[130:131]
	v_pk_add_f32 v[116:117], v[116:117], v[130:131] neg_lo:[0,1] neg_hi:[0,1]
	v_pk_add_f32 v[130:131], v[138:139], v[124:125]
	v_pk_add_f32 v[124:125], v[138:139], v[124:125] neg_lo:[0,1] neg_hi:[0,1]
	v_pk_fma_f32 v[138:139], v[116:117], s[26:27], v[82:83] op_sel:[1,0,0] op_sel_hi:[0,1,1]
	v_pk_fma_f32 v[82:83], v[116:117], s[28:29], v[82:83] op_sel:[1,0,0] op_sel_hi:[0,1,1]
	v_pk_add_f32 v[116:117], v[78:79], v[72:73]
	v_pk_add_f32 v[72:73], v[78:79], v[72:73] neg_lo:[0,1] neg_hi:[0,1]
	v_pk_add_f32 v[78:79], v[118:119], v[132:133]
	v_pk_add_f32 v[118:119], v[118:119], v[132:133] neg_lo:[0,1] neg_hi:[0,1]
	v_pk_add_f32 v[132:133], v[116:117], v[78:79]
	v_pk_add_f32 v[78:79], v[116:117], v[78:79] neg_lo:[0,1] neg_hi:[0,1]
	v_pk_fma_f32 v[116:117], v[118:119], s[26:27], v[72:73] op_sel:[1,0,0] op_sel_hi:[0,1,1]
	v_pk_fma_f32 v[72:73], v[118:119], s[28:29], v[72:73] op_sel:[1,0,0] op_sel_hi:[0,1,1]
	v_pk_add_f32 v[118:119], v[80:81], v[126:127]
	v_pk_add_f32 v[80:81], v[80:81], v[126:127] neg_lo:[0,1] neg_hi:[0,1]
	v_pk_add_f32 v[126:127], v[120:121], v[134:135]
	v_pk_add_f32 v[120:121], v[120:121], v[134:135] neg_lo:[0,1] neg_hi:[0,1]
	v_pk_add_f32 v[134:135], v[118:119], v[126:127]
	v_pk_add_f32 v[118:119], v[118:119], v[126:127] neg_lo:[0,1] neg_hi:[0,1]
	v_pk_fma_f32 v[126:127], v[120:121], s[26:27], v[80:81] op_sel:[1,0,0] op_sel_hi:[0,1,1]
	v_pk_fma_f32 v[80:81], v[120:121], s[28:29], v[80:81] op_sel:[1,0,0] op_sel_hi:[0,1,1]
	v_pk_add_f32 v[120:121], v[114:115], v[128:129]
	v_pk_add_f32 v[114:115], v[114:115], v[128:129] neg_lo:[0,1] neg_hi:[0,1]
	v_pk_add_f32 v[128:129], v[122:123], v[136:137]
	v_pk_add_f32 v[122:123], v[122:123], v[136:137] neg_lo:[0,1] neg_hi:[0,1]
	v_pk_add_f32 v[136:137], v[120:121], v[128:129]
	v_pk_add_f32 v[120:121], v[120:121], v[128:129] neg_lo:[0,1] neg_hi:[0,1]
	v_pk_fma_f32 v[128:129], v[122:123], s[26:27], v[114:115] op_sel:[1,0,0] op_sel_hi:[0,1,1]
	v_pk_fma_f32 v[114:115], v[122:123], s[28:29], v[114:115] op_sel:[1,0,0] op_sel_hi:[0,1,1]
	v_pk_mul_f32 v[122:123], v[116:117], s[34:35] op_sel_hi:[0,1]
	v_mul_f32_e32 v86, 0x3f3504f3, v126
	v_pk_fma_f32 v[116:117], v[116:117], s[30:31], v[122:123] op_sel:[1,0,0]
	v_pk_fma_f32 v[122:123], v[126:127], s[36:37], v[86:87] op_sel:[1,0,0] op_sel_hi:[1,1,0]
	v_pk_mul_f32 v[126:127], v[128:129], s[8:9] op_sel_hi:[0,1]
	v_pk_fma_f32 v[126:127], v[128:129], s[38:39], v[126:127] op_sel:[1,0,0]
	v_pk_mul_f32 v[128:129], v[118:119], s[18:19] op_sel_hi:[0,1]
	v_pk_fma_f32 v[118:119], v[118:119], s[12:13], v[128:129] op_sel:[1,0,0]
	v_pk_mul_f32 v[128:129], v[120:121], s[36:37] op_sel_hi:[0,1]
	v_pk_fma_f32 v[120:121], v[120:121], s[36:37], v[128:129] op_sel:[1,0,0] op_sel_hi:[1,0,1]
	v_pk_mul_f32 v[128:129], v[72:73], s[8:9] op_sel_hi:[0,1]
	v_pk_fma_f32 v[72:73], v[72:73], s[38:39], v[128:129] op_sel:[1,0,0]
	v_pk_mul_f32 v[128:129], v[80:81], s[36:37] op_sel_hi:[0,1]
	s_mov_b32 s39, s30
	v_pk_fma_f32 v[80:81], v[80:81], s[36:37], v[128:129] op_sel:[1,0,0] op_sel_hi:[1,0,1]
	v_pk_mul_f32 v[128:129], v[114:115], s[38:39] op_sel_hi:[0,1]
	s_mov_b32 s9, s38
	v_mul_f32_e32 v86, 0x3f3504f3, v78
	v_pk_fma_f32 v[114:115], v[114:115], s[8:9], v[128:129] op_sel:[1,0,0]
	v_pk_add_f32 v[128:129], v[130:131], v[134:135]
	v_pk_add_f32 v[130:131], v[130:131], v[134:135] neg_lo:[0,1] neg_hi:[0,1]
	v_pk_add_f32 v[134:135], v[132:133], v[136:137]
	v_pk_add_f32 v[132:133], v[132:133], v[136:137] neg_lo:[0,1] neg_hi:[0,1]
	v_pk_fma_f32 v[78:79], v[78:79], s[36:37], v[86:87] op_sel:[1,0,0] op_sel_hi:[1,1,0]
	v_pk_add_f32 v[136:137], v[128:129], v[134:135]
	v_pk_add_f32 v[128:129], v[128:129], v[134:135] neg_lo:[0,1] neg_hi:[0,1]
	v_pk_fma_f32 v[134:135], v[132:133], s[26:27], v[130:131] op_sel:[1,0,0] op_sel_hi:[0,1,1]
	v_pk_fma_f32 v[130:131], v[132:133], s[28:29], v[130:131] op_sel:[1,0,0] op_sel_hi:[0,1,1]
	v_pk_add_f32 v[132:133], v[138:139], v[122:123]
	v_pk_add_f32 v[122:123], v[138:139], v[122:123] neg_lo:[0,1] neg_hi:[0,1]
	v_pk_add_f32 v[138:139], v[116:117], v[126:127]
	v_pk_add_f32 v[116:117], v[116:117], v[126:127] neg_lo:[0,1] neg_hi:[0,1]
	v_pk_add_f32 v[126:127], v[132:133], v[138:139]
	v_pk_add_f32 v[132:133], v[132:133], v[138:139] neg_lo:[0,1] neg_hi:[0,1]
	v_pk_fma_f32 v[138:139], v[116:117], s[26:27], v[122:123] op_sel:[1,0,0] op_sel_hi:[0,1,1]
	v_pk_fma_f32 v[116:117], v[116:117], s[28:29], v[122:123] op_sel:[1,0,0] op_sel_hi:[0,1,1]
	v_pk_add_f32 v[122:123], v[124:125], v[118:119]
	v_pk_add_f32 v[118:119], v[124:125], v[118:119] neg_lo:[0,1] neg_hi:[0,1]
	v_pk_add_f32 v[124:125], v[78:79], v[120:121]
	v_pk_add_f32 v[78:79], v[78:79], v[120:121] neg_lo:[0,1] neg_hi:[0,1]
	v_pk_add_f32 v[120:121], v[122:123], v[124:125]
	v_pk_add_f32 v[122:123], v[122:123], v[124:125] neg_lo:[0,1] neg_hi:[0,1]
	v_pk_fma_f32 v[124:125], v[78:79], s[26:27], v[118:119] op_sel:[1,0,0] op_sel_hi:[0,1,1]
	v_pk_fma_f32 v[78:79], v[78:79], s[28:29], v[118:119] op_sel:[1,0,0] op_sel_hi:[0,1,1]
	v_pk_add_f32 v[118:119], v[82:83], v[80:81]
	v_pk_add_f32 v[80:81], v[82:83], v[80:81] neg_lo:[0,1] neg_hi:[0,1]
	v_pk_add_f32 v[82:83], v[72:73], v[114:115]
	v_pk_add_f32 v[72:73], v[72:73], v[114:115] neg_lo:[0,1] neg_hi:[0,1]
	v_pk_add_f32 v[114:115], v[118:119], v[82:83]
	v_pk_add_f32 v[82:83], v[118:119], v[82:83] neg_lo:[0,1] neg_hi:[0,1]
	v_pk_fma_f32 v[118:119], v[72:73], s[26:27], v[80:81] op_sel:[1,0,0] op_sel_hi:[0,1,1]
	v_pk_fma_f32 v[72:73], v[72:73], s[28:29], v[80:81] op_sel:[1,0,0] op_sel_hi:[0,1,1]
	ds_write_b64 v164, v[136:137]
	ds_write2_b64 v77, v[126:127], v[120:121] offset0:17 offset1:34
	ds_write2_b64 v77, v[114:115], v[134:135] offset0:51 offset1:68
	ds_write2_b64 v77, v[138:139], v[124:125] offset0:85 offset1:102
	ds_write2_b64 v77, v[118:119], v[128:129] offset0:119 offset1:136
	ds_write2_b64 v77, v[132:133], v[122:123] offset0:153 offset1:170
	ds_write2_b64 v77, v[82:83], v[130:131] offset0:187 offset1:204
	ds_write2_b64 v77, v[116:117], v[78:79] offset0:221 offset1:238
	ds_write_b64 v77, v[72:73] offset:2040
	v_cndmask_b32_e64 v72, v211, v212, s[4:5]
	v_mul_f32_e32 v73, v72, v24
	v_mul_f32_e32 v28, v72, v28
	v_mov_b32_e32 v24, v87
	v_cvt_pk_fp8_f32 v24, v73, v28
	v_mul_f32_e32 v28, v72, v25
	v_mul_f32_e32 v29, v72, v29
	v_mov_b32_e32 v25, v87
	v_cvt_pk_fp8_f32 v25, v28, v29
	v_mul_f32_e32 v28, v72, v33
	v_mul_f32_e32 v29, v72, v37
	v_mul_f32_e32 v12, v72, v12
	v_cvt_pk_fp8_f32 v25, v28, v29 op_sel:[0,0,1]
	v_mul_f32_e32 v28, v72, v26
	v_mul_f32_e32 v29, v72, v30
	v_mov_b32_e32 v26, v87
	v_cvt_pk_fp8_f32 v26, v28, v29
	v_mul_f32_e32 v28, v72, v27
	v_mul_f32_e32 v29, v72, v31
	v_mov_b32_e32 v27, v87
	v_cvt_pk_fp8_f32 v27, v28, v29
	v_mul_f32_e32 v28, v72, v35
	v_mul_f32_e32 v29, v72, v39
	v_mul_f32_e32 v13, v72, v13
	v_cvt_pk_fp8_f32 v27, v28, v29 op_sel:[0,0,1]
	v_mul_f32_e32 v28, v72, v8
	v_mov_b32_e32 v8, v87
	v_cvt_pk_fp8_f32 v8, v28, v12
	v_mul_f32_e32 v12, v72, v9
	v_mov_b32_e32 v9, v87
	v_cvt_pk_fp8_f32 v9, v12, v13
	v_mul_f32_e32 v12, v72, v17
	v_mul_f32_e32 v13, v72, v21
	s_min_i32 s4, s58, s59
	v_cvt_pk_fp8_f32 v9, v12, v13 op_sel:[0,0,1]
	v_mul_f32_e32 v12, v72, v10
	v_mul_f32_e32 v13, v72, v14
	v_mov_b32_e32 v10, v87
	s_mul_i32 s4, s4, s3
	v_cvt_pk_fp8_f32 v10, v12, v13
	v_mul_f32_e32 v12, v72, v11
	v_mul_f32_e32 v13, v72, v15
	v_mov_b32_e32 v11, v87
	s_add_i32 s4, s4, s2
	v_cvt_pk_fp8_f32 v11, v12, v13
	s_mul_hi_i32 s5, s4, 0x2aaaaaab
	v_mul_f32_e32 v32, v72, v32
	v_mul_f32_e32 v36, v72, v36
	s_lshr_b32 s8, s5, 31
	s_ashr_i32 s5, s5, 7
	v_cvt_pk_fp8_f32 v24, v32, v36 op_sel:[0,0,1]
	v_mul_f32_e32 v30, v72, v34
	v_mul_f32_e32 v32, v72, v38
	v_mul_f32_e32 v16, v72, v16
	v_mul_f32_e32 v20, v72, v20
	s_add_i32 s5, s5, s8
	v_cvt_pk_fp8_f32 v26, v30, v32 op_sel:[0,0,1]
	v_cvt_pk_fp8_f32 v8, v16, v20 op_sel:[0,0,1]
	v_mul_f32_e32 v14, v72, v18
	v_mul_f32_e32 v16, v72, v22
	v_mul_f32_e32 v12, v72, v19
	v_mul_f32_e32 v13, v72, v23
	s_add_i32 s8, s5, 11
	s_mulk_i32 s5, 0x300
	v_cvt_pk_fp8_f32 v10, v14, v16 op_sel:[0,0,1]
	v_cvt_pk_fp8_f32 v11, v12, v13 op_sel:[0,0,1]
	s_sub_i32 s19, s4, s5
	s_cmpk_lt_i32 s19, 0x200
	s_cselect_b64 s[4:5], -1, 0
	s_cmpk_gt_i32 s19, 0x1ff
	s_waitcnt lgkmcnt(0)
	s_barrier
	ds_write_b128 v240, v[24:27]
	ds_write_b128 v241, v[8:11]
	s_cbranch_scc0 .LBB0_877
	s_load_dwordx2 s[12:13], s[14:15], 0x110
	s_ashr_i32 s9, s8, 31
	s_lshl_b64 s[56:57], s[8:9], 24
	s_mov_b32 s55, s18
	s_waitcnt lgkmcnt(0)
	s_add_u32 s12, s12, s56
	s_addc_u32 s13, s13, s57
	s_lshl_b32 s9, s19, 3
	s_and_b32 s9, s9, 0x7fffffc0
	s_add_i32 s54, s9, 0xfffff000
	s_mov_b64 s[56:57], 0

.LBB0_879:
	s_lshl_b64 s[54:55], s[54:55], 13
	s_add_u32 s8, s12, s54
	s_addc_u32 s12, s13, s55
	s_lshl_b32 s9, s19, s9
	s_and_b32 s9, s9, 0x700
	s_lshl_b32 s9, s9, 2
	s_add_u32 s8, s8, s9
	s_addc_u32 s9, s12, 0
	s_cmp_gt_i32 s58, s59
	s_cselect_b64 s[12:13], -1, 0
	v_cndmask_b32_e64 v8, v180, 0, s[12:13]
	s_and_b64 s[12:13], s[12:13], exec
	s_cselect_b32 s12, 0, 0x800
	v_lshlrev_b32_e32 v86, 2, v8
	v_lshl_add_u64 v[16:17], s[8:9], 0, v[86:87]
	v_mad_i64_i32 v[8:9], s[8:9], s12, v181, 0
	v_mad_i64_i32 v[10:11], s[8:9], s12, v182, 0
	v_lshl_add_u64 v[8:9], v[8:9], 2, v[16:17]
	v_lshl_add_u64 v[10:11], v[10:11], 2, v[16:17]
	global_load_dwordx4 v[24:27], v[8:9], off nt
	global_load_dwordx4 v[28:31], v[10:11], off nt
	v_mad_i64_i32 v[8:9], s[8:9], s12, v183, 0
	v_mad_i64_i32 v[10:11], s[8:9], s12, v184, 0
	v_lshl_add_u64 v[8:9], v[8:9], 2, v[16:17]
	v_lshl_add_u64 v[10:11], v[10:11], 2, v[16:17]
	global_load_dwordx4 v[32:35], v[8:9], off nt
	global_load_dwordx4 v[36:39], v[10:11], off nt
	v_mad_i64_i32 v[8:9], s[8:9], s12, v185, 0
	v_mad_i64_i32 v[10:11], s[8:9], s12, v186, 0
	v_mad_i64_i32 v[18:19], s[8:9], s12, v187, 0
	v_mad_i64_i32 v[20:21], s[8:9], s12, v188, 0
	v_lshl_add_u64 v[8:9], v[8:9], 2, v[16:17]
	v_lshl_add_u64 v[12:13], v[10:11], 2, v[16:17]
	v_lshl_add_u64 v[18:19], v[18:19], 2, v[16:17]
	v_lshl_add_u64 v[20:21], v[20:21], 2, v[16:17]
	global_load_dwordx4 v[8:11], v[8:9], off nt
	s_nop 0
	global_load_dwordx4 v[12:15], v[12:13], off nt
	s_nop 0
	global_load_dwordx4 v[16:19], v[18:19], off nt
	s_nop 0
	global_load_dwordx4 v[20:23], v[20:21], off nt
	s_cmp_gt_i32 s62, -3
	s_cselect_b32 s8, s33, 0
	s_min_i32 s8, s8, s59
	s_mul_i32 s8, s8, s3
	s_add_i32 s9, s8, s2
	s_mul_hi_i32 s8, s9, 0x2aaaaaab
	s_lshr_b32 s12, s8, 31
	s_ashr_i32 s8, s8, 7
	s_add_i32 s12, s8, s12
	s_add_i32 s8, s12, 11
	s_mulk_i32 s12, 0x300
	s_sub_i32 s19, s9, s12
	s_ashr_i32 s9, s8, 31
	s_cmpk_gt_i32 s19, 0x1ff
	s_mov_b64 s[54:55], -1
	s_cbranch_scc0 .LBB0_881
	s_lshl_b32 s12, s19, 3
	s_and_b32 s31, s12, 0x7fffffc0
	s_lshl_b32 s12, s19, 19
	s_and_b32 s33, s12, 0x380000
	s_lshl_b64 s[12:13], s[8:9], 22
	s_add_u32 s12, s16, s12
	s_addc_u32 s13, s17, s13
	s_add_u32 s12, s12, s33
	s_addc_u32 s13, s13, 0
	s_add_u32 s12, s12, s31
	s_addc_u32 s13, s13, 0
	s_add_u32 s12, s12, 0x24dff000
	s_addc_u32 s13, s13, 0
	s_mov_b64 s[54:55], 0

.LBB0_883:
	s_add_i32 s19, s62, 6
	s_cmp_lt_i32 s62, -2
	s_cselect_b64 s[8:9], -1, 0
	s_or_b64 s[8:9], s[8:9], s[50:51]
	s_and_b64 s[8:9], s[8:9], exec
	s_cselect_b32 s8, s65, s12
	s_cselect_b32 s12, 0x80, s31
	v_mul_i32_i24_e32 v72, s12, v191
	v_or_b32_e32 v72, v72, v189
	v_ashrrev_i32_e32 v73, 31, v72
	s_cselect_b32 s9, s66, s13
	v_lshlrev_b64 v[72:73], 11, v[72:73]
	v_lshl_add_u64 v[72:73], s[8:9], 0, v[72:73]
	v_lshl_add_u64 v[72:73], v[72:73], 0, v[88:89]
	ds_read_b32 v78, v239
	ds_read_b32 v79, v239 offset:1040
	ds_read_b32 v80, v239 offset:2080
	ds_read_b32 v81, v239 offset:3120
	ds_read_b32 v114, v242
	ds_read_b32 v115, v242 offset:1040
	ds_read_b32 v116, v242 offset:2080
	ds_read_b32 v117, v242 offset:3120
	s_waitcnt lgkmcnt(4)
	global_store_dwordx4 v[72:73], v[78:81], off nt
	v_mul_i32_i24_e32 v72, s12, v201
	v_or_b32_e32 v72, v72, v189
	v_ashrrev_i32_e32 v73, 31, v72
	v_lshlrev_b64 v[72:73], 11, v[72:73]
	v_lshl_add_u64 v[72:73], s[8:9], 0, v[72:73]
	v_lshl_add_u64 v[72:73], v[72:73], 0, v[88:89]
	s_waitcnt lgkmcnt(0)
	global_store_dwordx4 v[72:73], v[114:117], off nt
	v_lshlrev_b32_e32 v72, 3, v76
	v_add_u32_e32 v73, 0x100, v74
	v_add_u32_e32 v76, 0x200, v74
	v_add_u32_e32 v77, 0x300, v74
	v_ashrrev_i32_e32 v73, 4, v73
	v_ashrrev_i32_e32 v76, 4, v76
	v_ashrrev_i32_e32 v77, 4, v77
	v_add3_u32 v72, v219, v72, v75
	v_lshlrev_b32_e32 v73, 3, v73
	v_lshlrev_b32_e32 v76, 3, v76
	v_lshlrev_b32_e32 v77, 3, v77
	v_add3_u32 v73, v219, v73, v75
	v_add3_u32 v76, v219, v76, v75
	v_add3_u32 v77, v219, v77, v75
	ds_read_b64 v[114:115], v72
	ds_read_b64 v[128:129], v73 offset:2048
	ds_read_b64 v[120:121], v76 offset:4096
	ds_read_b64 v[130:131], v77 offset:6144
	v_add_u32_e32 v72, 0x400, v74
	v_ashrrev_i32_e32 v72, 4, v72
	v_add_u32_e32 v73, 0x500, v74
	v_add_u32_e32 v76, 0x600, v74
	v_add_u32_e32 v77, 0x700, v74
	v_lshlrev_b32_e32 v72, 3, v72
	v_ashrrev_i32_e32 v73, 4, v73
	v_ashrrev_i32_e32 v76, 4, v76
	v_ashrrev_i32_e32 v77, 4, v77
	v_add3_u32 v72, v219, v72, v75
	v_lshlrev_b32_e32 v73, 3, v73
	v_lshlrev_b32_e32 v76, 3, v76
	v_lshlrev_b32_e32 v77, 3, v77
	v_add3_u32 v73, v219, v73, v75
	v_add3_u32 v76, v219, v76, v75
	v_add3_u32 v77, v219, v77, v75
	ds_read_b64 v[116:117], v72 offset:8192
	ds_read_b64 v[136:137], v73 offset:10240
	ds_read_b64 v[124:125], v76 offset:12288
	ds_read_b64 v[134:135], v77 offset:14336
	v_add_u32_e32 v72, 0x800, v74
	v_ashrrev_i32_e32 v72, 4, v72
	v_add_u32_e32 v73, 0x900, v74
	v_add_u32_e32 v76, 0xa00, v74
	v_add_u32_e32 v77, 0xb00, v74
	v_lshlrev_b32_e32 v72, 3, v72
	v_ashrrev_i32_e32 v73, 4, v73
	v_ashrrev_i32_e32 v76, 4, v76
	v_ashrrev_i32_e32 v77, 4, v77
	v_add3_u32 v72, v219, v72, v75
	v_lshlrev_b32_e32 v73, 3, v73
	v_lshlrev_b32_e32 v76, 3, v76
	v_lshlrev_b32_e32 v77, 3, v77
	v_add3_u32 v73, v219, v73, v75
	v_add3_u32 v76, v219, v76, v75
	v_add3_u32 v77, v219, v77, v75
	ds_read_b64 v[118:119], v72 offset:16384
	ds_read_b64 v[140:141], v73 offset:18432
	ds_read_b64 v[126:127], v76 offset:20480
	ds_read_b64 v[138:139], v77 offset:22528
	v_add_u32_e32 v72, 0xc00, v74
	v_ashrrev_i32_e32 v72, 4, v72
	v_add_u32_e32 v73, 0xd00, v74
	v_add_u32_e32 v76, 0xe00, v74
	v_add_u32_e32 v74, 0xf00, v74
	v_lshlrev_b32_e32 v72, 3, v72
	v_ashrrev_i32_e32 v73, 4, v73
	v_ashrrev_i32_e32 v76, 4, v76
	v_ashrrev_i32_e32 v74, 4, v74
	v_add3_u32 v72, v219, v72, v75
	v_lshlrev_b32_e32 v73, 3, v73
	v_lshlrev_b32_e32 v76, 3, v76
	v_lshlrev_b32_e32 v74, 3, v74
	v_add3_u32 v73, v219, v73, v75
	v_add3_u32 v76, v219, v76, v75
	v_add3_u32 v74, v219, v74, v75
	ds_read_b64 v[122:123], v72 offset:24576
	ds_read_b64 v[144:145], v73 offset:26624
	ds_read_b64 v[132:133], v76 offset:28672
	ds_read_b64 v[142:143], v74 offset:30720
	v_cndmask_b32_e64 v72, v211, v212, s[6:7]
	s_waitcnt vmcnt(19)
	v_mul_f32_e32 v73, v72, v56
	s_waitcnt vmcnt(18)
	v_mul_f32_e32 v60, v72, v60
	v_mov_b32_e32 v56, v87
	v_cvt_pk_fp8_f32 v56, v73, v60
	v_mul_f32_e32 v60, v72, v57
	v_mul_f32_e32 v61, v72, v61
	v_mov_b32_e32 v57, v87
	v_cvt_pk_fp8_f32 v57, v60, v61
	s_waitcnt vmcnt(17)
	v_mul_f32_e32 v60, v72, v65
	s_waitcnt vmcnt(16)
	v_mul_f32_e32 v61, v72, v69
	s_waitcnt vmcnt(14)
	v_mul_f32_e32 v44, v72, v44
	v_cvt_pk_fp8_f32 v57, v60, v61 op_sel:[0,0,1]
	v_mul_f32_e32 v60, v72, v58
	v_mul_f32_e32 v61, v72, v62
	v_mov_b32_e32 v58, v87
	v_cvt_pk_fp8_f32 v58, v60, v61
	v_mul_f32_e32 v60, v72, v59
	v_mul_f32_e32 v61, v72, v63
	v_mov_b32_e32 v59, v87
	v_cvt_pk_fp8_f32 v59, v60, v61
	v_mul_f32_e32 v60, v72, v67
	v_mul_f32_e32 v61, v72, v71
	v_mul_f32_e32 v45, v72, v45
	v_cvt_pk_fp8_f32 v59, v60, v61 op_sel:[0,0,1]
	v_mul_f32_e32 v60, v72, v40
	v_mov_b32_e32 v40, v87
	v_cvt_pk_fp8_f32 v40, v60, v44
	v_mul_f32_e32 v44, v72, v41
	v_mov_b32_e32 v41, v87
	v_cvt_pk_fp8_f32 v41, v44, v45
	s_waitcnt vmcnt(13)
	v_mul_f32_e32 v44, v72, v49
	s_waitcnt vmcnt(12)
	v_mul_f32_e32 v45, v72, v53
	s_min_i32 s6, s19, s59
	v_cvt_pk_fp8_f32 v41, v44, v45 op_sel:[0,0,1]
	v_mul_f32_e32 v44, v72, v42
	v_mul_f32_e32 v45, v72, v46
	v_mov_b32_e32 v42, v87
	v_cvt_pk_fp8_f32 v42, v44, v45
	v_mul_f32_e32 v44, v72, v43
	v_mul_f32_e32 v45, v72, v47
	v_mov_b32_e32 v43, v87
	s_mul_i32 s6, s6, s3
	v_cvt_pk_fp8_f32 v43, v44, v45
	s_add_i32 s7, s6, s2
	v_mul_f32_e32 v64, v72, v64
	v_mul_f32_e32 v68, v72, v68
	s_mul_hi_i32 s6, s7, 0x2aaaaaab
	v_cvt_pk_fp8_f32 v56, v64, v68 op_sel:[0,0,1]
	v_mul_f32_e32 v62, v72, v66
	v_mul_f32_e32 v64, v72, v70
	v_mul_f32_e32 v48, v72, v48
	v_mul_f32_e32 v52, v72, v52
	s_lshr_b32 s8, s6, 31
	s_ashr_i32 s6, s6, 7
	v_cvt_pk_fp8_f32 v58, v62, v64 op_sel:[0,0,1]
	v_cvt_pk_fp8_f32 v40, v48, v52 op_sel:[0,0,1]
	v_mul_f32_e32 v46, v72, v50
	v_mul_f32_e32 v48, v72, v54
	v_mul_f32_e32 v44, v72, v51
	v_mul_f32_e32 v45, v72, v55
	s_add_i32 s8, s6, s8
	v_cvt_pk_fp8_f32 v42, v46, v48 op_sel:[0,0,1]
	v_cvt_pk_fp8_f32 v43, v44, v45 op_sel:[0,0,1]
	s_add_i32 s6, s8, 11
	s_mulk_i32 s8, 0x300
	s_sub_i32 s31, s7, s8
	s_cmpk_gt_i32 s31, 0x1ff
	s_mov_b64 s[50:51], -1
	s_waitcnt lgkmcnt(0)
	s_barrier
	ds_write_b128 v236, v[56:59]
	ds_write_b128 v237, v[40:43]
	s_cbranch_scc0 .LBB0_885
	s_load_dwordx2 s[8:9], s[14:15], 0x110
	s_ashr_i32 s7, s6, 31
	s_lshl_b64 s[50:51], s[6:7], 24
	s_mov_b32 s13, s18
	s_waitcnt lgkmcnt(0)
	s_add_u32 s8, s8, s50
	s_addc_u32 s9, s9, s51
	s_lshl_b32 s7, s31, 3
	s_and_b32 s7, s7, 0x7fffffc0
	s_add_i32 s12, s7, 0xfffff000
	s_mov_b64 s[50:51], 0

.LBB0_887:
	s_lshl_b64 s[12:13], s[12:13], 13
	s_add_u32 s6, s8, s12
	s_addc_u32 s8, s9, s13
	s_lshl_b32 s7, s31, s7
	s_and_b32 s7, s7, 0x700
	s_lshl_b32 s7, s7, 2
	s_add_u32 s6, s6, s7
	s_addc_u32 s7, s8, 0
	s_cmp_gt_i32 s19, s59
	s_cselect_b64 s[8:9], -1, 0
	v_cndmask_b32_e64 v40, v180, 0, s[8:9]
	s_and_b64 s[8:9], s[8:9], exec
	s_cselect_b32 s8, 0, 0x800
	v_lshlrev_b32_e32 v86, 2, v40
	v_lshl_add_u64 v[56:57], s[6:7], 0, v[86:87]
	v_mad_i64_i32 v[40:41], s[6:7], s8, v181, 0
	v_mad_i64_i32 v[42:43], s[6:7], s8, v182, 0
	v_lshl_add_u64 v[40:41], v[40:41], 2, v[56:57]
	v_lshl_add_u64 v[42:43], v[42:43], 2, v[56:57]
	global_load_dwordx4 v[48:51], v[40:41], off nt
	global_load_dwordx4 v[52:55], v[42:43], off nt
	v_mad_i64_i32 v[40:41], s[6:7], s8, v183, 0
	v_mad_i64_i32 v[42:43], s[6:7], s8, v184, 0
	v_lshl_add_u64 v[40:41], v[40:41], 2, v[56:57]
	v_lshl_add_u64 v[42:43], v[42:43], 2, v[56:57]
	global_load_dwordx4 v[64:67], v[40:41], off nt
	global_load_dwordx4 v[68:71], v[42:43], off nt
	v_mad_i64_i32 v[40:41], s[6:7], s8, v185, 0
	v_mad_i64_i32 v[42:43], s[6:7], s8, v186, 0
	v_mad_i64_i32 v[58:59], s[6:7], s8, v187, 0
	v_mad_i64_i32 v[60:61], s[6:7], s8, v188, 0
	v_lshl_add_u64 v[40:41], v[40:41], 2, v[56:57]
	v_lshl_add_u64 v[44:45], v[42:43], 2, v[56:57]
	v_lshl_add_u64 v[58:59], v[58:59], 2, v[56:57]
	v_lshl_add_u64 v[60:61], v[60:61], 2, v[56:57]
	global_load_dwordx4 v[40:43], v[40:41], off nt
	s_nop 0
	global_load_dwordx4 v[44:47], v[44:45], off nt
	s_nop 0
	global_load_dwordx4 v[56:59], v[58:59], off nt
	s_nop 0
	global_load_dwordx4 v[60:63], v[60:61], off nt
	s_cmp_gt_i32 s62, -4
	s_cselect_b32 s6, s77, 0
	s_min_i32 s6, s6, s59
	s_mul_i32 s6, s6, s3
	s_add_i32 s7, s6, s2
	s_mul_hi_i32 s6, s7, 0x2aaaaaab
	s_lshr_b32 s8, s6, 31
	s_ashr_i32 s6, s6, 7
	s_add_i32 s8, s6, s8
	s_add_i32 s6, s8, 11
	s_mulk_i32 s8, 0x300
	s_sub_i32 s19, s7, s8
	s_ashr_i32 s7, s6, 31
	s_cmpk_gt_i32 s19, 0x1ff
	s_mov_b64 s[12:13], -1
	s_cbranch_scc0 .LBB0_889
	s_lshl_b32 s8, s19, 3
	s_and_b32 s12, s8, 0x7fffffc0
	s_lshl_b32 s8, s19, 19
	s_and_b32 s13, s8, 0x380000
	s_lshl_b64 s[8:9], s[6:7], 22
	s_add_u32 s8, s16, s8
	s_addc_u32 s9, s17, s9
	s_add_u32 s8, s8, s13
	s_addc_u32 s9, s9, 0
	s_add_u32 s8, s8, s12
	s_addc_u32 s9, s9, 0
	s_add_u32 s8, s8, 0x24dff000
	s_addc_u32 s9, s9, 0
	s_mov_b64 s[12:13], 0

.LBB0_893:
	v_cndmask_b32_e64 v72, v211, v212, s[4:5]
	s_waitcnt vmcnt(19)
	v_mul_f32_e32 v73, v72, v24
	s_waitcnt vmcnt(18)
	v_mul_f32_e32 v28, v72, v28
	v_mov_b32_e32 v24, v87
	v_cvt_pk_fp8_f32 v24, v73, v28
	v_mul_f32_e32 v28, v72, v25
	v_mul_f32_e32 v29, v72, v29
	v_mov_b32_e32 v25, v87
	v_cvt_pk_fp8_f32 v25, v28, v29
	s_waitcnt vmcnt(17)
	v_mul_f32_e32 v28, v72, v33
	s_waitcnt vmcnt(16)
	v_mul_f32_e32 v29, v72, v37
	s_waitcnt vmcnt(14)
	v_mul_f32_e32 v12, v72, v12
	v_cvt_pk_fp8_f32 v25, v28, v29 op_sel:[0,0,1]
	v_mul_f32_e32 v28, v72, v26
	v_mul_f32_e32 v29, v72, v30
	v_mov_b32_e32 v26, v87
	v_cvt_pk_fp8_f32 v26, v28, v29
	v_mul_f32_e32 v28, v72, v27
	v_mul_f32_e32 v29, v72, v31
	v_mov_b32_e32 v27, v87
	v_cvt_pk_fp8_f32 v27, v28, v29
	v_mul_f32_e32 v28, v72, v35
	v_mul_f32_e32 v29, v72, v39
	v_mul_f32_e32 v13, v72, v13
	v_cvt_pk_fp8_f32 v27, v28, v29 op_sel:[0,0,1]
	v_mul_f32_e32 v28, v72, v8
	v_mov_b32_e32 v8, v87
	v_cvt_pk_fp8_f32 v8, v28, v12
	v_mul_f32_e32 v12, v72, v9
	v_mov_b32_e32 v9, v87
	v_cvt_pk_fp8_f32 v9, v12, v13
	s_add_i32 s19, s62, 7
	s_waitcnt vmcnt(13)
	v_mul_f32_e32 v12, v72, v17
	s_waitcnt vmcnt(12)
	v_mul_f32_e32 v13, v72, v21
	v_cvt_pk_fp8_f32 v9, v12, v13 op_sel:[0,0,1]
	v_mul_f32_e32 v12, v72, v10
	v_mul_f32_e32 v13, v72, v14
	v_mov_b32_e32 v10, v87
	s_min_i32 s4, s19, s59
	v_cvt_pk_fp8_f32 v10, v12, v13
	v_mul_f32_e32 v12, v72, v11
	v_mul_f32_e32 v13, v72, v15
	v_mov_b32_e32 v11, v87
	s_mul_i32 s4, s4, s3
	v_cvt_pk_fp8_f32 v11, v12, v13
	s_add_i32 s5, s4, s2
	v_mul_f32_e32 v32, v72, v32
	v_mul_f32_e32 v36, v72, v36
	s_mul_hi_i32 s4, s5, 0x2aaaaaab
	v_cvt_pk_fp8_f32 v24, v32, v36 op_sel:[0,0,1]
	v_mul_f32_e32 v30, v72, v34
	v_mul_f32_e32 v32, v72, v38
	v_mul_f32_e32 v16, v72, v16
	v_mul_f32_e32 v20, v72, v20
	s_lshr_b32 s6, s4, 31
	s_ashr_i32 s4, s4, 7
	v_cvt_pk_fp8_f32 v26, v30, v32 op_sel:[0,0,1]
	v_cvt_pk_fp8_f32 v8, v16, v20 op_sel:[0,0,1]
	v_mul_f32_e32 v14, v72, v18
	v_mul_f32_e32 v16, v72, v22
	v_mul_f32_e32 v12, v72, v19
	v_mul_f32_e32 v13, v72, v23
	s_add_i32 s6, s4, s6
	v_cvt_pk_fp8_f32 v10, v14, v16 op_sel:[0,0,1]
	v_cvt_pk_fp8_f32 v11, v12, v13 op_sel:[0,0,1]
	s_add_i32 s4, s6, 11
	s_mulk_i32 s6, 0x300
	s_sub_i32 s31, s5, s6
	s_cmpk_gt_i32 s31, 0x1ff
	s_mov_b64 s[12:13], -1
	s_waitcnt lgkmcnt(0)
	s_barrier
	ds_write_b128 v240, v[24:27]
	ds_write_b128 v241, v[8:11]
	s_cbranch_scc0 .LBB0_895
	s_load_dwordx2 s[6:7], s[14:15], 0x110
	s_ashr_i32 s5, s4, 31
	s_lshl_b64 s[12:13], s[4:5], 24
	s_mov_b32 s9, s18
	s_waitcnt lgkmcnt(0)
	s_add_u32 s6, s6, s12
	s_addc_u32 s7, s7, s13
	s_lshl_b32 s5, s31, 3
	s_and_b32 s5, s5, 0x7fffffc0
	s_add_i32 s8, s5, 0xfffff000
	s_mov_b64 s[12:13], 0

.LBB0_897:
	s_lshl_b64 s[8:9], s[8:9], 13
	s_add_u32 s4, s6, s8
	s_addc_u32 s6, s7, s9
	s_lshl_b32 s5, s31, s5
	s_and_b32 s5, s5, 0x700
	s_lshl_b32 s5, s5, 2
	s_add_u32 s4, s4, s5
	s_addc_u32 s5, s6, 0
	s_cmp_gt_i32 s19, s59
	s_cselect_b64 s[6:7], -1, 0
	v_cndmask_b32_e64 v8, v180, 0, s[6:7]
	s_and_b64 s[6:7], s[6:7], exec
	s_cselect_b32 s6, 0, 0x800
	v_lshlrev_b32_e32 v86, 2, v8
	v_lshl_add_u64 v[24:25], s[4:5], 0, v[86:87]
	v_mad_i64_i32 v[8:9], s[4:5], s6, v181, 0
	v_mad_i64_i32 v[10:11], s[4:5], s6, v182, 0
	v_lshl_add_u64 v[8:9], v[8:9], 2, v[24:25]
	v_lshl_add_u64 v[10:11], v[10:11], 2, v[24:25]
	global_load_dwordx4 v[20:23], v[8:9], off nt
	global_load_dwordx4 v[16:19], v[10:11], off nt
	v_mad_i64_i32 v[8:9], s[4:5], s6, v183, 0
	v_mad_i64_i32 v[10:11], s[4:5], s6, v184, 0
	v_lshl_add_u64 v[8:9], v[8:9], 2, v[24:25]
	v_lshl_add_u64 v[10:11], v[10:11], 2, v[24:25]
	global_load_dwordx4 v[36:39], v[8:9], off nt
	global_load_dwordx4 v[32:35], v[10:11], off nt
	v_mad_i64_i32 v[8:9], s[4:5], s6, v185, 0
	v_mad_i64_i32 v[10:11], s[4:5], s6, v186, 0
	v_mad_i64_i32 v[26:27], s[4:5], s6, v187, 0
	v_mad_i64_i32 v[28:29], s[4:5], s6, v188, 0
	v_lshl_add_u64 v[8:9], v[8:9], 2, v[24:25]
	v_lshl_add_u64 v[10:11], v[10:11], 2, v[24:25]
	v_lshl_add_u64 v[26:27], v[26:27], 2, v[24:25]
	v_lshl_add_u64 v[24:25], v[28:29], 2, v[24:25]
	global_load_dwordx4 v[12:15], v[8:9], off nt
	s_nop 0
	global_load_dwordx4 v[8:11], v[10:11], off nt
	s_nop 0
	global_load_dwordx4 v[28:31], v[26:27], off nt
	s_nop 0
	global_load_dwordx4 v[24:27], v[24:25], off nt
	s_cmp_gt_i32 s62, -5
	s_cselect_b32 s4, s78, 0
	s_min_i32 s4, s4, s59
	s_mul_i32 s4, s4, s3
	s_add_i32 s5, s4, s2
	s_mul_hi_i32 s4, s5, 0x2aaaaaab
	s_lshr_b32 s6, s4, 31
	s_ashr_i32 s4, s4, 7
	s_add_i32 s6, s4, s6
	s_add_i32 s4, s6, 11
	s_mulk_i32 s6, 0x300
	s_sub_i32 s12, s5, s6
	s_ashr_i32 s5, s4, 31
	s_cmpk_gt_i32 s12, 0x1ff
	s_mov_b64 s[8:9], -1
	s_cbranch_scc0 .LBB0_899
	s_lshl_b32 s6, s12, 3
	s_and_b32 s8, s6, 0x7fffffc0
	s_lshl_b32 s6, s12, 19
	s_and_b32 s9, s6, 0x380000
	s_lshl_b64 s[6:7], s[4:5], 22
	s_add_u32 s6, s16, s6
	s_addc_u32 s7, s17, s7
	s_add_u32 s6, s6, s9
	s_addc_u32 s7, s7, 0
	s_add_u32 s6, s6, s8
	s_addc_u32 s7, s7, 0
	s_add_u32 s6, s6, 0x24dff000
	s_addc_u32 s7, s7, 0
	s_mov_b64 s[8:9], 0

.LBB0_938:
	s_add_i32 s4, s62, -2
	s_min_i32 s4, s4, s59
	s_mul_i32 s4, s4, s3
	s_add_i32 s4, s4, s2
	s_mul_hi_i32 s5, s4, 0x2aaaaaab
	s_lshr_b32 s6, s5, 31
	s_lshr_b32 s5, s5, 7
	s_add_i32 s5, s5, s6
	s_mulk_i32 s5, 0x300
	s_and_b32 s0, s62, 1
	s_sub_i32 s4, s4, s5
	s_cmpk_lt_i32 s4, 0x200
	s_cselect_b64 vcc, -1, 0
	s_cmp_eq_u32 s0, 0
	v_cndmask_b32_e32 v114, v112, v113, vcc
	s_mov_b64 s[6:7], -1
	s_barrier
	s_cbranch_scc1 .LBB0_948
	s_waitcnt vmcnt(7)
	v_mul_f32_e32 v1, v114, v20
	s_waitcnt vmcnt(6)
	v_mul_f32_e32 v2, v114, v16
	v_mov_b32_e32 v0, v103
	v_cvt_pk_fp8_f32 v0, v1, v2
	v_mul_f32_e32 v2, v114, v21
	v_mul_f32_e32 v5, v114, v17
	v_mov_b32_e32 v1, v103
	v_cvt_pk_fp8_f32 v1, v2, v5
	s_waitcnt vmcnt(5)
	v_mul_f32_e32 v3, v114, v36
	s_waitcnt vmcnt(4)
	v_mul_f32_e32 v4, v114, v32
	v_cvt_pk_fp8_f32 v0, v3, v4 op_sel:[0,0,1]
	v_mul_f32_e32 v2, v114, v37
	v_mul_f32_e32 v3, v114, v33
	v_cvt_pk_fp8_f32 v1, v2, v3 op_sel:[0,0,1]
	v_mul_f32_e32 v3, v114, v22
	v_mul_f32_e32 v4, v114, v18
	v_mov_b32_e32 v2, v103
	v_cvt_pk_fp8_f32 v2, v3, v4
	v_mul_f32_e32 v4, v114, v23
	v_mul_f32_e32 v7, v114, v19
	v_mov_b32_e32 v3, v103
	v_cvt_pk_fp8_f32 v3, v4, v7
	v_mul_f32_e32 v5, v114, v38
	v_mul_f32_e32 v6, v114, v34
	v_cvt_pk_fp8_f32 v2, v5, v6 op_sel:[0,0,1]
	v_mul_f32_e32 v4, v114, v39
	v_mul_f32_e32 v5, v114, v35
	v_cvt_pk_fp8_f32 v3, v4, v5 op_sel:[0,0,1]
	s_waitcnt vmcnt(3)
	v_mul_f32_e32 v5, v114, v12
	s_waitcnt vmcnt(2)
	v_mul_f32_e32 v6, v114, v8
	v_mov_b32_e32 v4, v103
	v_cvt_pk_fp8_f32 v4, v5, v6
	v_mul_f32_e32 v6, v114, v13
	v_mul_f32_e32 v73, v114, v9
	v_mov_b32_e32 v5, v103
	v_cvt_pk_fp8_f32 v5, v6, v73
	s_waitcnt vmcnt(1)
	v_mul_f32_e32 v7, v114, v28
	s_waitcnt vmcnt(0)
	v_mul_f32_e32 v72, v114, v24
	v_cvt_pk_fp8_f32 v4, v7, v72 op_sel:[0,0,1]
	v_mul_f32_e32 v6, v114, v29
	v_mul_f32_e32 v7, v114, v25
	v_cvt_pk_fp8_f32 v5, v6, v7 op_sel:[0,0,1]
	v_mul_f32_e32 v7, v114, v14
	v_mul_f32_e32 v72, v114, v10
	v_mov_b32_e32 v6, v103
	v_cvt_pk_fp8_f32 v6, v7, v72
	v_mul_f32_e32 v72, v114, v15
	v_mul_f32_e32 v75, v114, v11
	v_mov_b32_e32 v7, v103
	s_min_i32 s0, s62, s59
	v_cvt_pk_fp8_f32 v7, v72, v75
	s_mul_i32 s0, s0, s3
	s_add_i32 s0, s0, s2
	v_mul_f32_e32 v73, v114, v30
	v_mul_f32_e32 v74, v114, v26
	s_mul_hi_i32 s4, s0, 0x2aaaaaab
	v_cvt_pk_fp8_f32 v6, v73, v74 op_sel:[0,0,1]
	v_mul_f32_e32 v72, v114, v31
	v_mul_f32_e32 v73, v114, v27
	s_lshr_b32 s5, s4, 31
	s_ashr_i32 s4, s4, 7
	v_cvt_pk_fp8_f32 v7, v72, v73 op_sel:[0,0,1]
	s_add_i32 s5, s4, s5
	s_add_i32 s4, s5, 11
	s_mulk_i32 s5, 0x300
	v_add_u32_e32 v72, v104, v105
	s_sub_i32 s22, s0, s5
	ds_write_b128 v72, v[0:3]
	v_add_u32_e32 v0, v104, v106
	s_cmpk_gt_i32 s22, 0x1ff
	s_mov_b64 s[10:11], -1
	ds_write_b128 v0, v[4:7]
	s_cbranch_scc0 .LBB0_941
	s_load_dwordx2 s[6:7], s[14:15], 0x110
	s_ashr_i32 s5, s4, 31
	s_lshl_b64 s[8:9], s[4:5], 24
	s_mov_b64 s[10:11], 0
	s_waitcnt lgkmcnt(0)
	s_add_u32 s6, s6, s8
	s_addc_u32 s7, s7, s9
	s_lshl_b32 s0, s22, 3
	s_and_b32 s0, s0, 0x7fffffc0
	s_addk_i32 s0, 0xf000
	s_mov_b64 s[8:9], s[0:1]

.LBB0_943:
	s_lshl_b64 s[4:5], s[8:9], 13
	s_add_u32 s4, s6, s4
	s_addc_u32 s5, s7, s5
	s_lshl_b32 s0, s22, s0
	s_and_b32 s0, s0, 0x700
	s_lshl_b32 s0, s0, 2
	s_add_u32 s4, s4, s0
	s_addc_u32 s5, s5, 0
	s_cmp_gt_i32 s62, s59
	s_cselect_b64 s[6:7], -1, 0
	v_cndmask_b32_e64 v0, v180, 0, s[6:7]
	s_and_b64 s[6:7], s[6:7], exec
	s_cselect_b32 s0, 0, 0x800
	v_lshlrev_b32_e32 v102, 2, v0
	v_lshl_add_u64 v[88:89], s[4:5], 0, v[102:103]
	v_mad_i64_i32 v[0:1], s[4:5], s0, v181, 0
	v_lshl_add_u64 v[72:73], v[0:1], 2, v[88:89]
	v_mad_i64_i32 v[0:1], s[4:5], s0, v182, 0
	v_lshl_add_u64 v[74:75], v[0:1], 2, v[88:89]
	global_load_dwordx4 v[0:3], v[72:73], off nt
	global_load_dwordx4 v[4:7], v[74:75], off nt
	v_mad_i64_i32 v[72:73], s[4:5], s0, v183, 0
	v_lshl_add_u64 v[80:81], v[72:73], 2, v[88:89]
	v_mad_i64_i32 v[72:73], s[4:5], s0, v184, 0
	v_lshl_add_u64 v[82:83], v[72:73], 2, v[88:89]
	global_load_dwordx4 v[72:75], v[80:81], off nt
	global_load_dwordx4 v[76:79], v[82:83], off nt
	v_mad_i64_i32 v[80:81], s[4:5], s0, v185, 0
	v_lshl_add_u64 v[90:91], v[80:81], 2, v[88:89]
	v_mad_i64_i32 v[80:81], s[4:5], s0, v186, 0
	v_lshl_add_u64 v[92:93], v[80:81], 2, v[88:89]
	global_load_dwordx4 v[80:83], v[90:91], off nt
	global_load_dwordx4 v[84:87], v[92:93], off nt
	v_mad_i64_i32 v[90:91], s[4:5], s0, v187, 0
	v_lshl_add_u64 v[96:97], v[90:91], 2, v[88:89]
	v_mad_i64_i32 v[90:91], s[4:5], s0, v188, 0
	v_lshl_add_u64 v[98:99], v[90:91], 2, v[88:89]
	global_load_dwordx4 v[88:91], v[96:97], off nt
	global_load_dwordx4 v[92:95], v[98:99], off nt
	s_max_i32 s0, s62, 3
	s_add_i32 s0, s0, -3
	s_min_i32 s0, s0, s59
	s_mul_i32 s0, s0, s3
	s_add_i32 s0, s0, s2
	s_mul_hi_i32 s4, s0, 0x2aaaaaab
	s_lshr_b32 s5, s4, 31
	s_ashr_i32 s4, s4, 7
	s_add_i32 s5, s4, s5
	s_add_i32 s4, s5, 11
	s_mulk_i32 s5, 0x300
	s_sub_i32 s0, s0, s5
	s_ashr_i32 s5, s4, 31
	s_cmpk_gt_i32 s0, 0x1ff
	s_mov_b64 s[8:9], -1
	s_cbranch_scc0 .LBB0_945
	s_lshl_b32 s6, s0, 3
	s_and_b32 s8, s6, 0x7fffffc0
	s_lshl_b32 s6, s0, 19
	s_and_b32 s9, s6, 0x380000
	s_lshl_b64 s[6:7], s[4:5], 22
	s_add_u32 s6, s16, s6
	s_addc_u32 s7, s17, s7
	s_add_u32 s6, s6, s9
	s_addc_u32 s7, s7, 0
	s_add_u32 s6, s6, s8
	s_addc_u32 s7, s7, 0
	s_add_u32 s6, s6, 0x24dff000
	s_addc_u32 s7, s7, 0
	s_mov_b64 s[8:9], 0

.LBB0_948:
	s_and_b64 vcc, exec, s[6:7]
	s_cbranch_vccz .LBB0_957
	s_waitcnt vmcnt(8)
	v_mul_f32_e32 v1, v48, v114
	v_mul_f32_e32 v2, v52, v114
	v_mov_b32_e32 v0, v103
	v_cvt_pk_fp8_f32 v0, v1, v2
	v_mul_f32_e32 v2, v49, v114
	s_waitcnt vmcnt(7)
	v_mul_f32_e32 v5, v53, v114
	v_mov_b32_e32 v1, v103
	v_cvt_pk_fp8_f32 v1, v2, v5
	v_mul_f32_e32 v3, v64, v114
	s_waitcnt vmcnt(6)
	v_mul_f32_e32 v4, v68, v114
	v_cvt_pk_fp8_f32 v0, v3, v4 op_sel:[0,0,1]
	v_mul_f32_e32 v2, v65, v114
	v_mul_f32_e32 v3, v69, v114
	v_cvt_pk_fp8_f32 v1, v2, v3 op_sel:[0,0,1]
	v_mul_f32_e32 v3, v50, v114
	v_mul_f32_e32 v4, v54, v114
	v_mov_b32_e32 v2, v103
	v_cvt_pk_fp8_f32 v2, v3, v4
	v_mul_f32_e32 v4, v51, v114
	v_mul_f32_e32 v7, v55, v114
	v_mov_b32_e32 v3, v103
	v_cvt_pk_fp8_f32 v3, v4, v7
	v_mul_f32_e32 v5, v66, v114
	v_mul_f32_e32 v6, v70, v114
	v_cvt_pk_fp8_f32 v2, v5, v6 op_sel:[0,0,1]
	v_mul_f32_e32 v4, v67, v114
	v_mul_f32_e32 v5, v71, v114
	v_cvt_pk_fp8_f32 v3, v4, v5 op_sel:[0,0,1]
	s_waitcnt vmcnt(5)
	v_mul_f32_e32 v5, v40, v114
	s_waitcnt vmcnt(4)
	v_mul_f32_e32 v6, v114, v44
	v_mov_b32_e32 v4, v103
	v_cvt_pk_fp8_f32 v4, v5, v6
	v_mul_f32_e32 v6, v41, v114
	v_mul_f32_e32 v41, v114, v45
	v_mov_b32_e32 v5, v103
	v_cvt_pk_fp8_f32 v5, v6, v41
	s_waitcnt vmcnt(3)
	v_mul_f32_e32 v7, v114, v56
	s_waitcnt vmcnt(2)
	v_mul_f32_e32 v40, v114, v60
	v_cvt_pk_fp8_f32 v4, v7, v40 op_sel:[0,0,1]
	v_mul_f32_e32 v6, v114, v57
	v_mul_f32_e32 v7, v114, v61
	v_cvt_pk_fp8_f32 v5, v6, v7 op_sel:[0,0,1]
	v_mul_f32_e32 v7, v42, v114
	v_mul_f32_e32 v40, v114, v46
	v_mov_b32_e32 v6, v103
	v_cvt_pk_fp8_f32 v6, v7, v40
	v_mul_f32_e32 v40, v43, v114
	v_mul_f32_e32 v43, v114, v47
	v_mov_b32_e32 v7, v103
	s_min_i32 s0, s62, s59
	v_cvt_pk_fp8_f32 v7, v40, v43
	s_mul_i32 s0, s0, s3
	s_add_i32 s0, s0, s2
	v_mul_f32_e32 v41, v114, v58
	v_mul_f32_e32 v42, v114, v62
	s_mul_hi_i32 s4, s0, 0x2aaaaaab
	v_cvt_pk_fp8_f32 v6, v41, v42 op_sel:[0,0,1]
	v_mul_f32_e32 v40, v114, v59
	v_mul_f32_e32 v41, v114, v63
	s_lshr_b32 s5, s4, 31
	s_ashr_i32 s4, s4, 7
	v_cvt_pk_fp8_f32 v7, v40, v41 op_sel:[0,0,1]
	s_add_i32 s5, s4, s5
	s_add_i32 s4, s5, 11
	s_mulk_i32 s5, 0x300
	v_add_u32_e32 v40, v110, v105
	s_sub_i32 s22, s0, s5
	ds_write_b128 v40, v[0:3]
	v_add_u32_e32 v0, v110, v106
	s_cmpk_gt_i32 s22, 0x1ff
	s_mov_b64 s[10:11], -1
	ds_write_b128 v0, v[4:7]
	s_cbranch_scc0 .LBB0_951
	s_load_dwordx2 s[6:7], s[14:15], 0x110
	s_ashr_i32 s5, s4, 31
	s_lshl_b64 s[8:9], s[4:5], 24
	s_mov_b64 s[10:11], 0
	s_waitcnt lgkmcnt(0)
	s_add_u32 s6, s6, s8
	s_addc_u32 s7, s7, s9
	s_lshl_b32 s0, s22, 3
	s_and_b32 s0, s0, 0x7fffffc0
	s_addk_i32 s0, 0xf000
	s_mov_b64 s[8:9], s[0:1]

.LBB0_953:
	s_lshl_b64 s[4:5], s[8:9], 13
	s_add_u32 s4, s6, s4
	s_addc_u32 s5, s7, s5
	s_lshl_b32 s0, s22, s0
	s_and_b32 s0, s0, 0x700
	s_lshl_b32 s0, s0, 2
	s_add_u32 s4, s4, s0
	s_addc_u32 s5, s5, 0
	s_cmp_gt_i32 s62, s59
	s_cselect_b64 s[6:7], -1, 0
	v_cndmask_b32_e64 v0, v180, 0, s[6:7]
	s_and_b64 s[6:7], s[6:7], exec
	s_cselect_b32 s0, 0, 0x800
	v_lshlrev_b32_e32 v102, 2, v0
	v_lshl_add_u64 v[0:1], s[4:5], 0, v[102:103]
	v_mad_i64_i32 v[2:3], s[4:5], s0, v181, 0
	v_lshl_add_u64 v[2:3], v[2:3], 2, v[0:1]
	v_mad_i64_i32 v[4:5], s[4:5], s0, v182, 0
	v_lshl_add_u64 v[4:5], v[4:5], 2, v[0:1]
	global_load_dwordx4 v[48:51], v[2:3], off nt
	global_load_dwordx4 v[52:55], v[4:5], off nt
	v_mad_i64_i32 v[2:3], s[4:5], s0, v183, 0
	v_lshl_add_u64 v[2:3], v[2:3], 2, v[0:1]
	v_mad_i64_i32 v[4:5], s[4:5], s0, v184, 0
	v_lshl_add_u64 v[4:5], v[4:5], 2, v[0:1]
	global_load_dwordx4 v[64:67], v[2:3], off nt
	global_load_dwordx4 v[68:71], v[4:5], off nt
	v_mad_i64_i32 v[2:3], s[4:5], s0, v185, 0
	v_lshl_add_u64 v[2:3], v[2:3], 2, v[0:1]
	v_mad_i64_i32 v[4:5], s[4:5], s0, v186, 0
	v_lshl_add_u64 v[4:5], v[4:5], 2, v[0:1]
	global_load_dwordx4 v[40:43], v[2:3], off nt
	global_load_dwordx4 v[44:47], v[4:5], off nt
	v_mad_i64_i32 v[2:3], s[4:5], s0, v187, 0
	v_lshl_add_u64 v[2:3], v[2:3], 2, v[0:1]
	v_mad_i64_i32 v[4:5], s[4:5], s0, v188, 0
	v_lshl_add_u64 v[0:1], v[4:5], 2, v[0:1]
	global_load_dwordx4 v[56:59], v[2:3], off nt
	global_load_dwordx4 v[60:63], v[0:1], off nt
	s_max_i32 s0, s62, 3
	s_add_i32 s0, s0, -3
	s_min_i32 s0, s0, s59
	s_mul_i32 s0, s0, s3
	s_add_i32 s0, s0, s2
	s_mul_hi_i32 s4, s0, 0x2aaaaaab
	s_lshr_b32 s5, s4, 31
	s_ashr_i32 s4, s4, 7
	s_add_i32 s5, s4, s5
	s_add_i32 s4, s5, 11
	s_mulk_i32 s5, 0x300
	s_sub_i32 s0, s0, s5
	s_ashr_i32 s5, s4, 31
	s_cmpk_gt_i32 s0, 0x1ff
	s_mov_b64 s[8:9], -1
	s_cbranch_scc0 .LBB0_955
	s_lshl_b32 s6, s0, 3
	s_and_b32 s8, s6, 0x7fffffc0
	s_lshl_b32 s6, s0, 19
	s_and_b32 s9, s6, 0x380000
	s_lshl_b64 s[6:7], s[4:5], 22
	s_add_u32 s6, s16, s6
	s_addc_u32 s7, s17, s7
	s_add_u32 s6, s6, s9
	s_addc_u32 s7, s7, 0
	s_add_u32 s6, s6, s8
	s_addc_u32 s7, s7, 0
	s_add_u32 s6, s6, 0x24dff000
	s_addc_u32 s7, s7, 0
	s_mov_b64 s[8:9], 0

.LBB0_1223:
	s_andn2_b64 vcc, exec, s[0:1]
	s_cbranch_vccnz .LBB0_1245
	s_add_i32 s8, s33, -4
	s_lshl_b32 s0, s2, 2
	s_add_i32 s20, s8, s0
	s_cmpk_gt_i32 s20, 0x6bff
	s_cbranch_scc1 .LBB0_1245
	s_add_i32 s0, s20, 0xb800
	s_cmpk_lt_i32 s20, 0x4800
	s_cselect_b32 s9, s20, s0
	s_cmp_gt_i32 s9, 0xffff
	s_cbranch_scc0 .LBB0_1227
	s_load_dwordx2 s[0:1], s[16:17], 0x110
	s_add_i32 s4, s9, 0xffff0000
	s_mov_b32 s7, 0
	s_lshr_b32 s6, s4, 10
	s_lshl_b64 s[4:5], s[6:7], 24
	s_waitcnt lgkmcnt(0)
	s_add_u32 s0, s0, s4
	s_addc_u32 s1, s1, s5
	s_lshl_b32 s4, s9, 1
	s_and_b32 s10, s4, 0x780
	s_lshl_b32 s4, s10, 13
	s_add_u32 s0, s0, s4
	s_addc_u32 s1, s1, 0
	s_lshl_b32 s4, s9, 5
	s_and_b32 s11, s4, 0x7e0
	s_lshl_b32 s4, s11, 2
	s_add_u32 s4, s0, s4
	s_addc_u32 s5, s1, 0
	s_lshl_b64 s[0:1], s[6:7], 22
	s_lshl_b32 s6, s11, 11
	s_add_u32 s0, s18, s0
	s_addc_u32 s1, s19, s1
	s_add_u32 s0, s0, s6
	s_addc_u32 s1, s1, 0
	s_add_u32 s0, s0, s10
	s_addc_u32 s1, s1, 0
	s_add_u32 s0, s0, 0x24e00000
	s_addc_u32 s1, s1, 0
	s_mov_b32 s21, 0x42800000
	s_cbranch_execz .LBB0_1228
	s_branch .LBB0_1229

.LBB0_1233:
	s_add_i32 s20, s20, s22
	s_cmpk_lt_i32 s20, 0x6c00
	s_cselect_b64 s[8:9], -1, 0
	s_cmpk_gt_i32 s20, 0x6bff
	s_cbranch_scc1 .LBB0_1239
	s_add_i32 s0, s20, 0xb800
	s_cmpk_lt_i32 s20, 0x4800
	s_cselect_b32 s27, s20, s0
	s_cmp_gt_i32 s27, 0xffff
	s_mov_b64 s[12:13], -1
	s_cbranch_scc0 .LBB0_1236
	s_load_dwordx2 s[0:1], s[16:17], 0x110
	s_add_i32 s4, s27, 0xffff0000
	s_lshr_b32 s4, s4, 10
	s_lshl_b64 s[10:11], s[4:5], 24
	s_waitcnt lgkmcnt(0)
	s_add_u32 s0, s0, s10
	s_addc_u32 s1, s1, s11
	s_lshl_b32 s10, s27, 1
	s_and_b32 s12, s10, 0x780
	s_lshl_b32 s10, s12, 13
	s_add_u32 s0, s0, s10
	s_addc_u32 s1, s1, 0
	s_lshl_b32 s10, s27, 5
	s_and_b32 s13, s10, 0x7e0
	s_lshl_b32 s10, s13, 2
	s_add_u32 s10, s0, s10
	s_addc_u32 s11, s1, 0
	s_lshl_b64 s[0:1], s[4:5], 22
	s_lshl_b32 s4, s13, 11
	s_add_u32 s0, s23, s0
	s_addc_u32 s1, s24, s1
	s_add_u32 s0, s0, s4
	s_addc_u32 s1, s1, 0
	s_add_u32 s0, s0, s12
	s_addc_u32 s1, s1, 0
	s_mov_b64 s[12:13], 0

.LBB0_1239:
	s_waitcnt vmcnt(15)
	v_mul_f32_e32 v130, s26, v0
	s_waitcnt vmcnt(14)
	v_mul_f32_e32 v175, s26, v4
	v_mov_b32_e32 v176, v131
	v_cvt_pk_fp8_f32 v176, v130, v175
	s_waitcnt vmcnt(11)
	v_mul_f32_e32 v130, s26, v16
	s_waitcnt vmcnt(10)
	v_mul_f32_e32 v175, s26, v20
	v_mov_b32_e32 v177, v131
	v_cvt_pk_fp8_f32 v177, v130, v175
	v_mul_f32_e32 v178, s26, v8
	v_mul_f32_e32 v179, s26, v12
	s_waitcnt vmcnt(9)
	v_mul_f32_e32 v130, s26, v24
	s_waitcnt vmcnt(8)
	v_mul_f32_e32 v175, s26, v28
	v_cvt_pk_fp8_f32 v176, v178, v179 op_sel:[0,0,1]
	v_cvt_pk_fp8_f32 v177, v130, v175 op_sel:[0,0,1]
	s_waitcnt vmcnt(7)
	v_mul_f32_e32 v130, s26, v32
	s_waitcnt vmcnt(6)
	v_mul_f32_e32 v175, s26, v36
	v_mov_b32_e32 v178, v131
	v_cvt_pk_fp8_f32 v178, v130, v175
	s_waitcnt vmcnt(3)
	v_mul_f32_e32 v130, s26, v48
	s_waitcnt vmcnt(2)
	v_mul_f32_e32 v175, s26, v52
	v_mov_b32_e32 v179, v131
	v_cvt_pk_fp8_f32 v179, v130, v175
	v_mul_f32_e32 v180, s26, v40
	v_mul_f32_e32 v181, s26, v44
	s_waitcnt vmcnt(1)
	v_mul_f32_e32 v130, s26, v56
	s_waitcnt vmcnt(0)
	v_mul_f32_e32 v175, s26, v60
	v_cvt_pk_fp8_f32 v178, v180, v181 op_sel:[0,0,1]
	v_cvt_pk_fp8_f32 v179, v130, v175 op_sel:[0,0,1]
	v_mul_f32_e32 v130, s26, v1
	v_mul_f32_e32 v175, s26, v5
	v_mov_b32_e32 v180, v131
	v_cvt_pk_fp8_f32 v180, v130, v175
	v_mul_f32_e32 v130, s26, v17
	v_mul_f32_e32 v175, s26, v21
	v_mov_b32_e32 v181, v131
	v_cvt_pk_fp8_f32 v181, v130, v175
	v_mul_f32_e32 v182, s26, v9
	v_mul_f32_e32 v183, s26, v13
	v_mul_f32_e32 v130, s26, v25
	v_mul_f32_e32 v175, s26, v29
	v_cvt_pk_fp8_f32 v180, v182, v183 op_sel:[0,0,1]
	v_cvt_pk_fp8_f32 v181, v130, v175 op_sel:[0,0,1]
	v_mul_f32_e32 v130, s26, v33
	v_mul_f32_e32 v175, s26, v37
	v_mov_b32_e32 v182, v131
	v_cvt_pk_fp8_f32 v182, v130, v175
	v_mul_f32_e32 v130, s26, v49
	v_mul_f32_e32 v175, s26, v53
	v_mov_b32_e32 v183, v131
	v_cvt_pk_fp8_f32 v183, v130, v175
	v_mul_f32_e32 v184, s26, v41
	v_mul_f32_e32 v185, s26, v45
	v_mul_f32_e32 v130, s26, v57
	v_mul_f32_e32 v175, s26, v61
	v_cvt_pk_fp8_f32 v182, v184, v185 op_sel:[0,0,1]
	v_cvt_pk_fp8_f32 v183, v130, v175 op_sel:[0,0,1]
	v_mul_f32_e32 v130, s26, v2
	v_mul_f32_e32 v175, s26, v6
	v_mov_b32_e32 v184, v131
	v_cvt_pk_fp8_f32 v184, v130, v175
	v_mul_f32_e32 v130, s26, v18
	v_mul_f32_e32 v175, s26, v22
	v_mov_b32_e32 v185, v131
	v_cvt_pk_fp8_f32 v185, v130, v175
	v_mul_f32_e32 v186, s26, v10
	v_mul_f32_e32 v187, s26, v14
	v_mul_f32_e32 v130, s26, v26
	v_mul_f32_e32 v175, s26, v30
	v_cvt_pk_fp8_f32 v184, v186, v187 op_sel:[0,0,1]
	v_cvt_pk_fp8_f32 v185, v130, v175 op_sel:[0,0,1]
	v_mul_f32_e32 v130, s26, v34
	v_mul_f32_e32 v175, s26, v38
	v_mov_b32_e32 v186, v131
	v_cvt_pk_fp8_f32 v186, v130, v175
	v_mul_f32_e32 v130, s26, v50
	v_mul_f32_e32 v175, s26, v54
	v_mov_b32_e32 v187, v131
	v_cvt_pk_fp8_f32 v187, v130, v175
	v_mul_f32_e32 v188, s26, v42
	v_mul_f32_e32 v189, s26, v46
	v_mul_f32_e32 v130, s26, v58
	v_mul_f32_e32 v175, s26, v62
	v_cvt_pk_fp8_f32 v186, v188, v189 op_sel:[0,0,1]
	v_cvt_pk_fp8_f32 v187, v130, v175 op_sel:[0,0,1]
	v_mul_f32_e32 v130, s26, v3
	v_mul_f32_e32 v175, s26, v7
	v_mov_b32_e32 v188, v131
	v_cvt_pk_fp8_f32 v188, v130, v175
	v_mul_f32_e32 v130, s26, v19
	v_mul_f32_e32 v175, s26, v23
	v_mov_b32_e32 v189, v131
	v_cvt_pk_fp8_f32 v189, v130, v175
	v_mul_f32_e32 v190, s26, v11
	v_mul_f32_e32 v191, s26, v15
	v_mul_f32_e32 v130, s26, v27
	v_mul_f32_e32 v175, s26, v31
	v_cvt_pk_fp8_f32 v188, v190, v191 op_sel:[0,0,1]
	v_cvt_pk_fp8_f32 v189, v130, v175 op_sel:[0,0,1]
	v_mul_f32_e32 v130, s26, v35
	v_mul_f32_e32 v175, s26, v39
	v_mov_b32_e32 v190, v131
	v_cvt_pk_fp8_f32 v190, v130, v175
	v_mul_f32_e32 v130, s26, v51
	v_mul_f32_e32 v175, s26, v55
	v_mov_b32_e32 v191, v131
	v_cvt_pk_fp8_f32 v191, v130, v175
	v_mul_f32_e32 v192, s26, v43
	v_mul_f32_e32 v193, s26, v47
	v_mul_f32_e32 v130, s26, v59
	v_mul_f32_e32 v175, s26, v63
	v_cvt_pk_fp8_f32 v190, v192, v193 op_sel:[0,0,1]
	v_cvt_pk_fp8_f32 v191, v130, v175 op_sel:[0,0,1]
	ds_write_b128 v129, v[176:179]
	ds_write_b128 v129, v[180:183] offset:144
	ds_write_b128 v129, v[184:187] offset:288
	ds_write_b128 v129, v[188:191] offset:432
	s_waitcnt lgkmcnt(0)
	ds_read_b128 v[176:179], v174
	ds_read_b128 v[180:183], v174 offset:1152
	v_lshl_add_u64 v[188:189], s[6:7], 0, v[164:165]
	v_lshl_add_u64 v[184:185], v[188:189], 0, v[166:167]
	v_lshl_add_u64 v[190:191], v[188:189], 0, v[168:169]
	s_waitcnt lgkmcnt(1)
	global_store_dwordx4 v[184:185], v[176:179], off nt
	ds_read_b128 v[176:179], v174 offset:2304
	ds_read_b128 v[184:187], v174 offset:3456
	s_waitcnt lgkmcnt(2)
	global_store_dwordx4 v[190:191], v[180:183], off nt
	s_andn2_b64 vcc, exec, s[8:9]
	s_mov_b64 s[8:9], -1
	v_lshl_add_u64 v[180:181], v[188:189], 0, v[170:171]
	s_waitcnt lgkmcnt(1)
	global_store_dwordx4 v[180:181], v[176:179], off nt
	s_nop 1
	v_lshl_add_u64 v[176:177], v[188:189], 0, v[172:173]
	s_waitcnt lgkmcnt(0)
	global_store_dwordx4 v[176:177], v[184:187], off nt
	s_waitcnt lgkmcnt(0)
	s_cbranch_vccnz .LBB0_1232
	s_add_i32 s27, s20, s22
	s_cmpk_gt_i32 s27, 0x6bff
	s_cselect_b64 s[8:9], -1, 0
	s_and_b64 vcc, exec, s[8:9]
	s_cbranch_vccnz .LBB0_1231
	s_add_i32 s4, s27, 0xb800
	s_cmpk_lt_i32 s27, 0x4800
	s_cselect_b32 s20, s27, s4
	s_cmp_gt_i32 s20, 0xffff
	s_mov_b64 s[12:13], -1
	s_cbranch_scc0 .LBB0_1243
	s_load_dwordx2 s[6:7], s[16:17], 0x110
	s_add_i32 s4, s20, 0xffff0000
	s_lshr_b32 s4, s4, 10
	s_lshl_b64 s[10:11], s[4:5], 24
	s_waitcnt lgkmcnt(0)
	s_add_u32 s6, s6, s10
	s_addc_u32 s7, s7, s11
	s_lshl_b32 s10, s20, 1
	s_and_b32 s12, s10, 0x780
	s_lshl_b32 s10, s12, 13
	s_add_u32 s6, s6, s10
	s_addc_u32 s7, s7, 0
	s_lshl_b32 s10, s20, 5
	s_and_b32 s13, s10, 0x7e0
	s_lshl_b32 s10, s13, 2
	s_add_u32 s10, s6, s10
	s_addc_u32 s11, s7, 0
	s_lshl_b64 s[6:7], s[4:5], 22
	s_lshl_b32 s4, s13, 11
	s_add_u32 s6, s23, s6
	s_addc_u32 s7, s24, s7
	s_add_u32 s4, s6, s4
	s_addc_u32 s7, s7, 0
	s_add_u32 s6, s4, s12
	s_addc_u32 s7, s7, 0
	s_mov_b64 s[12:13], 0
